# nt (streaming) hint on the read-once projection-row loads of the mixer preparation phase (P2), both layers
# speedup vs baseline: 1.0106x; 1.0106x over previous
.LBB0_217:
	v_add_u32_e32 v8, s6, v67
	v_ashrrev_i32_e32 v8, 5, v8
	v_and_b32_e32 v52, -8, v8
	v_add_u32_e32 v12, s96, v8
	v_or_b32_e32 v10, 7, v8
	v_add_u32_e32 v24, -1, v52
	v_mad_i64_i32 v[8:9], s[2:3], v52, s73, v[4:5]
	v_or_b32_e32 v25, 2, v52
	v_or_b32_e32 v26, 3, v52
	v_or_b32_e32 v27, 4, v52
	v_or_b32_e32 v28, 5, v52
	v_or_b32_e32 v29, 6, v52
	v_cmp_gt_u32_e32 vcc, s74, v12
	v_add_u32_e32 v32, s96, v24
	global_load_dword v33, v[8:9], off offset:1024 nt
	global_load_dword v34, v[8:9], off offset:2048 nt
	v_add_u32_e32 v30, 8, v52
	v_or_b32_e32 v13, 1, v52
	v_mad_i64_i32 v[10:11], s[2:3], v10, s73, v[4:5]
	v_cndmask_b32_e64 v31, 0, 1, vcc
	v_mad_i64_i32 v[14:15], s[2:3], v25, s73, v[4:5]
	v_mad_i64_i32 v[16:17], s[2:3], v26, s73, v[4:5]
	v_mad_i64_i32 v[18:19], s[2:3], v27, s73, v[4:5]
	v_mad_i64_i32 v[20:21], s[2:3], v28, s73, v[4:5]
	v_mad_i64_i32 v[22:23], s[2:3], v29, s73, v[4:5]
	v_cndmask_b32_e32 v25, v52, v25, vcc
	v_cndmask_b32_e32 v26, v52, v26, vcc
	v_cndmask_b32_e32 v27, v52, v27, vcc
	v_cndmask_b32_e32 v28, v52, v28, vcc
	v_cmp_gt_u32_e64 s[4:5], s74, v32
	v_add_u32_e32 v35, s96, v30
	v_mad_i64_i32 v[12:13], s[2:3], v13, s73, v[4:5]
	v_or_b32_e32 v31, v52, v31
	v_cndmask_b32_e32 v29, v52, v29, vcc
	v_cndmask_b32_e64 v36, 0, 7, vcc
	global_load_dword v37, v[18:19], off nt
	global_load_dword v38, v[20:21], off nt
	global_load_dword v39, v[22:23], off nt
	global_load_dword v40, v[10:11], off nt
	v_cndmask_b32_e64 v32, v52, v24, s[4:5]
	v_mad_i64_i32 v[10:11], s[8:9], v25, s73, v[4:5]
	v_mad_i64_i32 v[20:21], s[8:9], v26, s73, v[4:5]
	v_mad_i64_i32 v[22:23], s[8:9], v27, s73, v[4:5]
	v_mad_i64_i32 v[24:25], s[8:9], v28, s73, v[4:5]
	v_cmp_gt_u32_e64 s[2:3], s74, v35
	v_mad_i64_i32 v[18:19], s[8:9], v31, s73, v[4:5]
	v_mad_i64_i32 v[26:27], s[8:9], v29, s73, v[4:5]
	v_or_b32_e32 v35, v36, v52
	v_mad_i64_i32 v[28:29], s[8:9], v32, s73, v[4:5]
	global_load_dword v32, v[10:11], off offset:2048 nt
	global_load_dword v36, v[18:19], off offset:1024 nt
	global_load_dword v41, v[18:19], off offset:2048 nt
	global_load_dword v42, v[10:11], off offset:1024 nt
	global_load_dword v43, v[20:21], off offset:1024 nt
	s_nop 0
	global_load_dword v20, v[20:21], off offset:2048 nt
	s_nop 0
	global_load_dword v21, v[22:23], off offset:1024 nt
	s_nop 0
	global_load_dword v22, v[22:23], off offset:2048 nt
	s_nop 0
	global_load_dword v23, v[24:25], off offset:1024 nt
	s_nop 0
	global_load_dword v24, v[24:25], off offset:2048 nt
	s_nop 0
	global_load_dword v25, v[26:27], off offset:1024 nt
	v_cndmask_b32_e64 v30, v52, v30, s[2:3]
	v_mad_i64_i32 v[30:31], s[8:9], v30, s73, v[4:5]
	v_mad_i64_i32 v[10:11], s[8:9], v35, s73, v[4:5]
	global_load_dword v26, v[26:27], off offset:2048 nt
	s_nop 0
	global_load_dword v27, v[28:29], off offset:1024 nt
	global_load_dword v35, v[8:9], off nt
	global_load_dword v45, v[12:13], off nt
	global_load_dword v47, v[14:15], off nt
	global_load_dword v53, v[28:29], off offset:2048 nt
	global_load_dword v54, v[10:11], off offset:1024 nt
	global_load_dword v55, v[10:11], off offset:2048 nt
	global_load_dword v56, v[30:31], off offset:1024 nt
	global_load_dword v57, v[30:31], off offset:2048 nt
	global_load_dword v58, v[16:17], off nt
	global_load_dwordx2 v[50:51], v[0:1], off offset:2048
	v_add_u32_e32 v52, s97, v52
	s_addk_i32 s6, 0x200
	s_cmpk_eq_i32 s6, 0x800
	s_waitcnt vmcnt(28)
	v_cndmask_b32_e32 v9, 0, v33, vcc
	s_waitcnt vmcnt(27)
	v_cndmask_b32_e32 v11, 0, v34, vcc
	v_lshlrev_b32_e32 v8, 16, v9
	v_lshlrev_b32_e32 v10, 16, v11
	v_and_b32_e32 v9, 0xffff0000, v9
	v_and_b32_e32 v11, 0xffff0000, v11
	v_pk_mul_f32 v[8:9], v[8:9], v[10:11]
	s_waitcnt vmcnt(26)
	v_lshlrev_b32_e32 v12, 16, v37
	v_and_b32_e32 v13, 0xffff0000, v37
	s_waitcnt vmcnt(24)
	v_lshlrev_b32_e32 v16, 16, v39
	v_and_b32_e32 v17, 0xffff0000, v39
	v_lshlrev_b32_e32 v14, 16, v38
	v_and_b32_e32 v15, 0xffff0000, v38
	s_waitcnt vmcnt(23)
	v_lshlrev_b32_e32 v18, 16, v40
	v_and_b32_e32 v19, 0xffff0000, v40
	s_waitcnt vmcnt(22)
	v_cndmask_b32_e32 v11, 0, v32, vcc
	s_waitcnt vmcnt(21)
	v_cndmask_b32_e32 v28, 0, v36, vcc
	s_waitcnt vmcnt(20)
	v_cndmask_b32_e32 v29, 0, v41, vcc
	s_waitcnt vmcnt(19)
	v_cndmask_b32_e32 v30, 0, v42, vcc
	s_waitcnt vmcnt(18)
	v_cndmask_b32_e32 v31, 0, v43, vcc
	v_lshlrev_b32_e32 v10, 16, v11
	s_waitcnt vmcnt(11)
	v_cndmask_b32_e32 v43, 0, v26, vcc
	v_cndmask_b32_e32 v36, 0, v22, vcc
	v_cndmask_b32_e32 v37, 0, v23, vcc
	v_cndmask_b32_e32 v39, 0, v24, vcc
	v_cndmask_b32_e32 v41, 0, v25, vcc
	s_waitcnt vmcnt(10)
	v_cndmask_b32_e64 v49, 0, v27, s[4:5]
	v_and_b32_e32 v11, 0xffff0000, v11
	v_lshlrev_b32_e32 v22, 16, v28
	v_lshlrev_b32_e32 v24, 16, v29
	v_and_b32_e32 v23, 0xffff0000, v28
	v_and_b32_e32 v25, 0xffff0000, v29
	v_lshlrev_b32_e32 v26, 16, v30
	v_and_b32_e32 v27, 0xffff0000, v30
	v_pk_mul_f32 v[22:23], v[22:23], v[24:25]
	v_pk_mul_f32 v[10:11], v[26:27], v[10:11]
	global_load_dwordx2 v[26:27], v[2:3], off
	global_load_dwordx2 v[24:25], v[0:1], off
	v_cndmask_b32_e32 v32, 0, v20, vcc
	v_cndmask_b32_e32 v33, 0, v21, vcc
	s_waitcnt vmcnt(11)
	v_lshlrev_b32_e32 v20, 16, v35
	v_and_b32_e32 v21, 0xffff0000, v35
	v_lshlrev_b32_e32 v28, 16, v31
	v_lshlrev_b32_e32 v30, 16, v32
	v_and_b32_e32 v29, 0xffff0000, v31
	v_and_b32_e32 v31, 0xffff0000, v32
	v_lshlrev_b32_e32 v32, 16, v33
	v_lshlrev_b32_e32 v34, 16, v36
	v_and_b32_e32 v33, 0xffff0000, v33
	v_and_b32_e32 v35, 0xffff0000, v36
	v_lshlrev_b32_e32 v36, 16, v37
	v_lshlrev_b32_e32 v38, 16, v39
	v_and_b32_e32 v37, 0xffff0000, v37
	v_and_b32_e32 v39, 0xffff0000, v39
	v_lshlrev_b32_e32 v40, 16, v41
	v_lshlrev_b32_e32 v42, 16, v43
	v_and_b32_e32 v41, 0xffff0000, v41
	v_and_b32_e32 v43, 0xffff0000, v43
	s_waitcnt vmcnt(8)
	v_cndmask_b32_e64 v53, 0, v53, s[4:5]
	s_waitcnt vmcnt(7)
	v_cndmask_b32_e32 v54, 0, v54, vcc
	s_waitcnt vmcnt(6)
	v_cndmask_b32_e32 v55, 0, v55, vcc
	s_waitcnt vmcnt(5)
	v_cndmask_b32_e64 v56, 0, v56, s[2:3]
	s_waitcnt vmcnt(4)
	v_cndmask_b32_e64 v57, 0, v57, s[2:3]
	v_lshlrev_b32_e32 v48, 16, v49
	v_and_b32_e32 v49, 0xffff0000, v49
	v_pk_mul_f32 v[28:29], v[28:29], v[30:31]
	v_lshlrev_b32_e32 v30, 16, v53
	v_and_b32_e32 v31, 0xffff0000, v53
	v_pk_mul_f32 v[32:33], v[32:33], v[34:35]
	v_pk_mul_f32 v[34:35], v[36:37], v[38:39]
	v_pk_mul_f32 v[36:37], v[40:41], v[42:43]
	v_lshlrev_b32_e32 v38, 16, v54
	v_lshlrev_b32_e32 v40, 16, v55
	v_and_b32_e32 v39, 0xffff0000, v54
	v_and_b32_e32 v41, 0xffff0000, v55
	v_lshlrev_b32_e32 v42, 16, v56
	v_lshlrev_b32_e32 v54, 16, v57
	v_and_b32_e32 v43, 0xffff0000, v56
	v_and_b32_e32 v55, 0xffff0000, v57
	v_pk_mul_f32 v[30:31], v[48:49], v[30:31]
	v_pk_mul_f32 v[42:43], v[42:43], v[54:55]
	s_waitcnt vmcnt(2)
	v_pk_mul_f32 v[54:55], v[50:51], v[8:9]
	v_pk_mul_f32 v[38:39], v[38:39], v[40:41]
	v_lshlrev_b32_e32 v44, 16, v45
	v_and_b32_e32 v45, 0xffff0000, v45
	v_ashrrev_i32_e32 v53, 31, v52
	v_or_b32_e32 v56, 1, v52
	v_or_b32_e32 v48, 2, v52
	v_or_b32_e32 v40, 3, v52
	v_lshlrev_b32_e32 v46, 16, v47
	v_and_b32_e32 v47, 0xffff0000, v47
	v_ashrrev_i32_e32 v57, 31, v56
	v_ashrrev_i32_e32 v49, 31, v48
	v_ashrrev_i32_e32 v41, 31, v40
	v_lshlrev_b64 v[56:57], 12, v[56:57]
	v_lshlrev_b64 v[48:49], 12, v[48:49]
	v_lshlrev_b64 v[40:41], 12, v[40:41]
	v_lshl_add_u64 v[56:57], v[6:7], 0, v[56:57]
	v_lshl_add_u64 v[48:49], v[6:7], 0, v[48:49]
	v_lshl_add_u64 v[40:41], v[6:7], 0, v[40:41]
	s_waitcnt vmcnt(0)
	v_pk_fma_f32 v[30:31], v[24:25], v[30:31], v[54:55]
	v_pk_mul_f32 v[54:55], v[50:51], v[22:23]
	s_nop 0
	v_pk_fma_f32 v[8:9], v[24:25], v[8:9], v[54:55]
	v_pk_mul_f32 v[54:55], v[50:51], v[10:11]
	v_pk_fma_f32 v[8:9], v[26:27], v[10:11], v[8:9]
	v_pk_fma_f32 v[54:55], v[24:25], v[22:23], v[54:55]
	v_pk_fma_f32 v[22:23], v[26:27], v[22:23], v[30:31]
	v_pk_mul_f32 v[30:31], v[50:51], v[28:29]
	v_pk_mul_f32 v[20:21], v[22:23], v[20:21]
	v_pk_fma_f32 v[30:31], v[24:25], v[10:11], v[30:31]
	v_pk_mul_f32 v[10:11], v[50:51], v[32:33]
	v_pk_fma_f32 v[30:31], v[26:27], v[32:33], v[30:31]
	v_pk_fma_f32 v[10:11], v[24:25], v[28:29], v[10:11]
	v_pk_fma_f32 v[28:29], v[26:27], v[28:29], v[54:55]
	v_pk_mul_f32 v[54:55], v[50:51], v[34:35]
	v_pk_fma_f32 v[10:11], v[26:27], v[34:35], v[10:11]
	v_pk_fma_f32 v[54:55], v[24:25], v[32:33], v[54:55]
	v_pk_mul_f32 v[32:33], v[50:51], v[36:37]
	v_pk_mul_f32 v[50:51], v[50:51], v[38:39]
	v_pk_fma_f32 v[32:33], v[24:25], v[34:35], v[32:33]
	v_pk_fma_f32 v[24:25], v[24:25], v[36:37], v[50:51]
	v_pk_fma_f32 v[36:37], v[26:27], v[36:37], v[54:55]
	v_pk_fma_f32 v[32:33], v[26:27], v[38:39], v[32:33]
	v_or_b32_e32 v38, 7, v52
	v_or_b32_e32 v34, 4, v52
	v_or_b32_e32 v50, 5, v52
	v_or_b32_e32 v54, 6, v52
	v_ashrrev_i32_e32 v39, 31, v38
	v_pk_mul_f32 v[8:9], v[8:9], v[44:45]
	v_pk_mul_f32 v[10:11], v[10:11], v[12:13]
	v_pk_mul_f32 v[12:13], v[36:37], v[14:15]
	v_pk_mul_f32 v[14:15], v[32:33], v[16:17]
	v_pk_fma_f32 v[16:17], v[26:27], v[42:43], v[24:25]
	v_lshlrev_b64 v[52:53], 12, v[52:53]
	v_ashrrev_i32_e32 v35, 31, v34
	v_ashrrev_i32_e32 v51, 31, v50
	v_ashrrev_i32_e32 v55, 31, v54
	v_lshlrev_b64 v[38:39], 12, v[38:39]
	v_lshlrev_b32_e32 v22, 16, v58
	v_and_b32_e32 v23, 0xffff0000, v58
	v_cvt_pk_bf16_f32 v20, v20, v21
	v_cvt_pk_bf16_f32 v21, v8, v9
	v_pk_mul_f32 v[8:9], v[16:17], v[18:19]
	v_lshl_add_u64 v[52:53], v[6:7], 0, v[52:53]
	v_lshlrev_b64 v[34:35], 12, v[34:35]
	v_lshlrev_b64 v[50:51], 12, v[50:51]
	v_lshlrev_b64 v[54:55], 12, v[54:55]
	v_lshl_add_u64 v[38:39], v[6:7], 0, v[38:39]
	v_pk_mul_f32 v[28:29], v[28:29], v[46:47]
	v_pk_mul_f32 v[22:23], v[30:31], v[22:23]
	v_cvt_pk_bf16_f32 v8, v8, v9
	v_lshl_add_u64 v[34:35], v[6:7], 0, v[34:35]
	v_lshl_add_u64 v[50:51], v[6:7], 0, v[50:51]
	v_lshl_add_u64 v[54:55], v[6:7], 0, v[54:55]
	v_cvt_pk_bf16_f32 v24, v28, v29
	v_cvt_pk_bf16_f32 v22, v22, v23
	v_cvt_pk_bf16_f32 v10, v10, v11
	v_cvt_pk_bf16_f32 v11, v12, v13
	v_cvt_pk_bf16_f32 v12, v14, v15
	global_store_dword v[52:53], v20, off
	global_store_dword v[56:57], v21, off
	global_store_dword v[48:49], v24, off
	global_store_dword v[40:41], v22, off
	global_store_dword v[34:35], v10, off
	global_store_dword v[50:51], v11, off
	global_store_dword v[54:55], v12, off
	global_store_dword v[38:39], v8, off
	s_cbranch_scc0 .LBB0_217
	v_mov_b32_e32 v123, v67
	s_load_dwordx2 s[2:3], s[30:31], 0x8
	s_load_dwordx4 s[8:11], s[30:31], 0x28
	v_ashrrev_i32_e32 v0, 3, v123
	v_add_u32_e32 v2, s97, v0
	v_ashrrev_i32_e32 v3, 31, v2
	v_and_b32_e32 v16, 7, v123
	s_waitcnt lgkmcnt(0)
	v_lshl_add_u64 v[2:3], v[2:3], 2, s[2:3]
	global_load_dword v1, v[2:3], off nt
	v_lshlrev_b32_e32 v2, 1, v16
	v_cvt_f32_ubyte0_e32 v2, v2
	v_mul_f32_e32 v17, 0xbd800000, v2
	v_cmp_eq_f32_e32 vcc, 0, v17
	v_readfirstlane_b32 s14, v123
	s_waitcnt vmcnt(0)
	v_cvt_f32_i32_e32 v1, v1
	v_cndmask_b32_e64 v12, v110, 1.0, vcc
	v_frexp_mant_f32_e32 v2, v12
	v_cmp_gt_f32_e64 s[2:3], s75, v2
	s_nop 1
	v_cndmask_b32_e64 v3, 1.0, 2.0, s[2:3]
	v_mul_f32_e32 v2, v2, v3
	v_add_f32_e32 v5, 1.0, v2
	v_rcp_f32_e32 v10, v5
	v_add_f32_e32 v3, -1.0, v5
	v_sub_f32_e32 v7, v2, v3
	v_add_f32_e32 v3, -1.0, v2
	v_mul_f32_e32 v11, v3, v10
	v_mul_f32_e32 v4, v5, v11
	v_fma_f32 v6, v11, v5, -v4
	v_fmac_f32_e32 v6, v11, v7
	v_add_f32_e32 v2, v4, v6
	v_sub_f32_e32 v5, v3, v2
	v_pk_add_f32 v[8:9], v[2:3], v[4:5] neg_lo:[0,1] neg_hi:[0,1]
	v_mov_b32_e32 v7, v2
	v_pk_add_f32 v[2:3], v[8:9], v[6:7] neg_lo:[0,1] neg_hi:[0,1]
	s_nop 0
	v_add_f32_e32 v2, v2, v3
	v_add_f32_e32 v2, v5, v2
	v_mul_f32_e32 v3, v10, v2
	v_add_f32_e32 v2, v11, v3
	v_sub_f32_e32 v4, v2, v11
	v_sub_f32_e32 v13, v3, v4
	v_mul_f32_e32 v3, v2, v2
	v_fma_f32 v5, v2, v2, -v3
	v_add_f32_e32 v4, v13, v13
	v_fmac_f32_e32 v5, v2, v4
	v_add_f32_e32 v4, v3, v5
	v_fmamk_f32 v6, v4, 0x3e76c4e1, v104
	v_fmaak_f32 v6, v4, v6, 0x3ecccdef
	v_sub_f32_e32 v3, v4, v3
	v_sub_f32_e32 v14, v5, v3
	v_mul_f32_e32 v3, v4, v6
	v_fma_f32 v5, v4, v6, -v3
	v_fmac_f32_e32 v5, v14, v6
	v_add_f32_e32 v6, v3, v5
	v_add_f32_e32 v7, 0x3f2aaaaa, v6
	v_sub_f32_e32 v3, v6, v3
	v_sub_f32_e32 v3, v5, v3
	v_add_f32_e32 v5, 0xbf2aaaaa, v7
	v_add_f32_e32 v3, 0x31739010, v3
	v_sub_f32_e32 v5, v6, v5
	v_pk_mul_f32 v[8:9], v[2:3], v[4:5]
	v_pk_add_f32 v[10:11], v[2:3], v[4:5]
	v_fma_f32 v6, v4, v2, -v8
	v_fmac_f32_e32 v6, v4, v13
	v_mov_b32_e32 v9, v11
	v_fmac_f32_e32 v6, v14, v2
	v_pk_add_f32 v[4:5], v[8:9], v[6:7]
	v_ldexp_f32 v14, v13, 1
	v_sub_f32_e32 v3, v4, v8
	v_sub_f32_e32 v3, v6, v3
	v_sub_f32_e32 v6, v7, v5
	v_add_f32_e32 v10, v11, v6
	v_pk_mul_f32 v[6:7], v[4:5], v[4:5] op_sel:[0,1] op_sel_hi:[1,0]
	v_cvt_f64_f32_e32 v[8:9], v12
	v_frexp_exp_i32_f64_e32 v7, v[8:9]
	v_subbrev_co_u32_e64 v7, s[2:3], 0, v7, s[2:3]
	v_cvt_f32_i32_e32 v7, v7
	v_fma_f32 v8, v4, v5, -v6
	v_fmac_f32_e32 v8, v4, v10
	v_fmac_f32_e32 v8, v3, v5
	v_mul_f32_e32 v4, 0x3f317218, v7
	v_fma_f32 v10, v7, s76, -v4
	v_fmac_f32_e32 v10, 0xb102e308, v7
	v_ldexp_f32 v11, v2, 1
	v_add_f32_e32 v5, v6, v8
	v_pk_add_f32 v[2:3], v[4:5], v[10:11]
	v_mov_b32_e32 v12, v5
	v_mov_b32_e32 v13, v3
	v_mov_b32_e32 v7, v11
	v_pk_add_f32 v[6:7], v[12:13], v[6:7] neg_lo:[0,1] neg_hi:[0,1]
	v_mov_b32_e32 v9, v5
	v_pk_add_f32 v[6:7], v[8:9], v[6:7] neg_lo:[0,1] neg_hi:[0,1]
	v_mov_b32_e32 v11, v2
	v_add_f32_e32 v5, v14, v6
	v_add_f32_e32 v5, v5, v7
	v_pk_add_f32 v[6:7], v[2:3], v[4:5] neg_lo:[0,1] neg_hi:[0,1]
	v_pk_add_f32 v[8:9], v[2:3], v[4:5]
	v_mov_b32_e32 v4, v5
	v_mov_b32_e32 v7, v9
	v_pk_add_f32 v[12:13], v[10:11], v[6:7] neg_lo:[0,1] neg_hi:[0,1]
	v_pk_add_f32 v[6:7], v[10:11], v[6:7]
	v_mov_b32_e32 v5, v2
	v_pk_add_f32 v[10:11], v[6:7], v[2:3] op_sel:[1,0] op_sel_hi:[0,1] neg_lo:[0,1] neg_hi:[0,1]
	v_pk_add_f32 v[14:15], v[8:9], v[10:11] op_sel_hi:[1,0] neg_lo:[0,1] neg_hi:[0,1]
	v_mov_b32_e32 v8, v9
	v_mov_b32_e32 v9, v7
	v_pk_mov_b32 v[10:11], v[2:3], v[10:11] op_sel:[1,0]
	v_mov_b32_e32 v14, v12
	v_pk_add_f32 v[8:9], v[8:9], v[10:11] neg_lo:[0,1] neg_hi:[0,1]
	v_mov_b32_e32 v13, v7
	v_pk_add_f32 v[2:3], v[4:5], v[8:9] neg_lo:[0,1] neg_hi:[0,1]
	s_nop 0
	v_pk_add_f32 v[4:5], v[14:15], v[2:3]
	s_nop 0
	v_pk_add_f32 v[8:9], v[4:5], v[4:5] op_sel:[0,1] op_sel_hi:[1,0]
	s_nop 0
	v_pk_add_f32 v[6:7], v[6:7], v[8:9] op_sel:[1,0] op_sel_hi:[0,1]
	v_mov_b32_e32 v5, v6
	v_pk_add_f32 v[10:11], v[4:5], v[12:13] neg_lo:[0,1] neg_hi:[0,1]
	v_mov_b32_e32 v3, v8
	v_sub_f32_e32 v4, v4, v10
	v_pk_add_f32 v[2:3], v[2:3], v[10:11] neg_lo:[0,1] neg_hi:[0,1]
	v_sub_f32_e32 v4, v12, v4
	v_add_f32_e32 v2, v2, v4
	v_add_f32_e32 v2, v2, v3
	v_add_f32_e32 v3, v6, v2
	v_sub_f32_e32 v4, v3, v6
	v_sub_f32_e32 v2, v2, v4
	v_mul_f32_e32 v4, v17, v3
	v_fma_f32 v3, v17, v3, -v4
	v_fmac_f32_e32 v3, v17, v2
	v_add_f32_e32 v2, v4, v3
	v_cmp_class_f32_e64 s[2:3], v4, s77
	v_sub_f32_e32 v5, v2, v4
	v_sub_f32_e32 v3, v3, v5
	v_cndmask_b32_e64 v2, v2, v4, s[2:3]
	v_cmp_eq_f32_e64 s[2:3], s79, v2
	s_nop 1
	v_cndmask_b32_e64 v4, 0, v111, s[2:3]
	v_sub_f32_e32 v5, v2, v4
	v_mul_f32_e32 v6, 0x3fb8aa3b, v5
	v_fma_f32 v7, v5, s80, -v6
	v_rndne_f32_e32 v8, v6
	v_fmac_f32_e32 v7, 0x32a5705f, v5
	v_sub_f32_e32 v6, v6, v8
	v_add_f32_e32 v6, v6, v7
	v_exp_f32_e32 v6, v6
	v_cvt_i32_f32_e32 v7, v8
	v_cmp_neq_f32_e64 s[2:3], |v2|, s78
	s_nop 1
	v_cndmask_b32_e64 v2, 0, v3, s[2:3]
	v_ldexp_f32 v3, v6, v7
	v_cmp_ngt_f32_e64 s[2:3], s81, v5
	v_add_f32_e32 v2, v4, v2
	s_nop 0
	v_cndmask_b32_e64 v3, 0, v3, s[2:3]
	v_cmp_nlt_f32_e64 s[2:3], s79, v5
	s_nop 1
	v_cndmask_b32_e64 v3, v112, v3, s[2:3]
	v_fma_f32 v2, v3, v2, v3
	v_cmp_class_f32_e64 s[2:3], v3, s77
	s_nop 1
	v_cndmask_b32_e64 v2, v2, v3, s[2:3]
	v_cmp_neq_f32_e64 s[2:3], v17, |v17|
	s_nop 1
	v_cndmask_b32_e64 v3, v112, 0, s[2:3]
	v_cndmask_b32_e64 v3, v3, 1.0, vcc
	v_cmp_class_f32_e64 s[2:3], v17, s77
	s_nop 1
	v_cndmask_b32_e64 v2, |v2|, v3, s[2:3]
	v_mul_f32_e32 v1, v2, v1
	s_brev_b32 s2, 18
	v_and_b32_e32 v2, 0x7fffffff, v1
	v_cmp_nlt_f32_e64 s[2:3], |v1|, s2
	s_and_saveexec_b64 s[4:5], s[2:3]
	s_xor_b64 s[12:13], exec, s[4:5]
	s_cbranch_execz .LBB0_220
	v_lshrrev_b32_e32 v3, 23, v2
	v_add_u32_e32 v3, 0xffffff88, v3
	v_cmp_lt_u32_e32 vcc, 63, v3
	s_mov_b32 s6, 0xfe5163ab
	s_nop 0
	v_cndmask_b32_e32 v4, 0, v113, vcc
	v_add_u32_e32 v3, v4, v3
	v_cmp_lt_u32_e64 s[2:3], 31, v3
	s_nop 1
	v_cndmask_b32_e64 v4, 0, v114, s[2:3]
	v_add_u32_e32 v3, v4, v3
	v_cmp_lt_u32_e64 s[4:5], 31, v3
	s_nop 1
	v_cndmask_b32_e64 v4, 0, v114, s[4:5]
	v_add_u32_e32 v3, v4, v3
	v_and_b32_e32 v4, 0x7fffff, v2
	v_or_b32_e32 v17, 0x800000, v4
	v_mad_u64_u32 v[4:5], s[6:7], v17, s6, 0
	v_mov_b32_e32 v64, v5
	s_mov_b32 s6, 0x3c439041
	v_mad_u64_u32 v[6:7], s[6:7], v17, s6, v[64:65]
	v_mov_b32_e32 v64, v7
	s_mov_b32 s6, 0xdb629599
	v_mad_u64_u32 v[8:9], s[6:7], v17, s6, v[64:65]
	v_mov_b32_e32 v64, v9
	s_mov_b32 s6, 0xf534ddc0
	v_mad_u64_u32 v[10:11], s[6:7], v17, s6, v[64:65]
	v_mov_b32_e32 v64, v11
	s_mov_b32 s6, 0xfc2757d1
	v_mad_u64_u32 v[12:13], s[6:7], v17, s6, v[64:65]
	v_mov_b32_e32 v64, v13
	s_mov_b32 s6, 0x4e441529
	v_mad_u64_u32 v[14:15], s[6:7], v17, s6, v[64:65]
	v_mov_b32_e32 v64, v15
	s_mov_b32 s6, 0xa2f9836e
	v_mad_u64_u32 v[18:19], s[6:7], v17, s6, v[64:65]
	v_cndmask_b32_e32 v5, v14, v10, vcc
	v_cndmask_b32_e32 v7, v18, v12, vcc
	v_cndmask_b32_e32 v11, v19, v14, vcc
	v_cndmask_b32_e64 v9, v7, v5, s[2:3]
	v_cndmask_b32_e64 v7, v11, v7, s[2:3]
	v_cndmask_b32_e32 v11, v12, v8, vcc
	v_cndmask_b32_e64 v5, v5, v11, s[2:3]
	v_sub_u32_e32 v12, 32, v3
	v_cmp_eq_u32_e64 s[6:7], 0, v3
	v_cndmask_b32_e32 v3, v10, v6, vcc
	v_cndmask_b32_e64 v7, v7, v9, s[4:5]
	v_cndmask_b32_e64 v9, v9, v5, s[4:5]
	v_cndmask_b32_e64 v6, v11, v3, s[2:3]
	v_alignbit_b32 v13, v7, v9, v12
	v_cndmask_b32_e64 v5, v5, v6, s[4:5]
	v_cndmask_b32_e64 v7, v13, v7, s[6:7]
	v_alignbit_b32 v10, v9, v5, v12
	v_cndmask_b32_e32 v4, v8, v4, vcc
	v_cndmask_b32_e64 v9, v10, v9, s[6:7]
	v_bfe_u32 v13, v7, 29, 1
	v_cndmask_b32_e64 v3, v3, v4, s[2:3]
	v_alignbit_b32 v10, v7, v9, 30
	v_sub_u32_e32 v14, 0, v13
	v_cndmask_b32_e64 v3, v6, v3, s[4:5]
	v_xor_b32_e32 v10, v10, v14
	v_alignbit_b32 v4, v5, v3, v12
	v_cndmask_b32_e64 v4, v4, v5, s[6:7]
	v_ffbh_u32_e32 v6, v10
	v_alignbit_b32 v5, v9, v4, 30
	v_min_u32_e32 v6, 32, v6
	v_alignbit_b32 v3, v4, v3, 30
	v_xor_b32_e32 v5, v5, v14
	v_sub_u32_e32 v8, 31, v6
	v_xor_b32_e32 v3, v3, v14
	v_alignbit_b32 v9, v10, v5, v8
	v_alignbit_b32 v3, v5, v3, v8
	v_alignbit_b32 v4, v9, v3, 9
	v_ffbh_u32_e32 v5, v4
	v_min_u32_e32 v5, 32, v5
	v_lshrrev_b32_e32 v11, 29, v7
	v_not_b32_e32 v8, v5
	v_alignbit_b32 v3, v4, v3, v8
	v_lshlrev_b32_e32 v4, 31, v11
	v_or_b32_e32 v8, 0x33000000, v4
	v_add_lshl_u32 v5, v5, v6, 23
	v_lshrrev_b32_e32 v3, 9, v3
	v_sub_u32_e32 v5, v8, v5
	v_or_b32_e32 v4, 0.5, v4
	v_lshlrev_b32_e32 v6, 23, v6
	v_or_b32_e32 v3, v5, v3
	v_lshrrev_b32_e32 v5, 9, v9
	v_sub_u32_e32 v4, v4, v6
	v_or_b32_e32 v4, v5, v4
	v_mul_f32_e32 v5, 0x3fc90fda, v4
	s_mov_b32 s2, 0x3fc90fda
	v_fma_f32 v6, v4, s2, -v5
	v_fmac_f32_e32 v6, 0x33a22168, v4
	v_fmac_f32_e32 v6, 0x3fc90fda, v3
	v_lshrrev_b32_e32 v4, 30, v7
	v_add_f32_e32 v3, v5, v6
	v_add_u32_e32 v4, v13, v4

.LBB0_224:
	v_add_u32_e32 v16, 0xfffffd40, v124
	v_mul_hi_i32 v17, v16, s82
	v_lshrrev_b32_e32 v18, 31, v17
	v_ashrrev_i32_e32 v17, 2, v17
	v_add_u32_e32 v137, v17, v18
	v_mul_lo_u32 v17, v137, 24
	v_sub_u32_e32 v18, v16, v17
	v_mul_lo_u16_e32 v16, 43, v18
	v_lshrrev_b16_e32 v17, 15, v16
	v_ashrrev_i16_e32 v16, 9, v16
	v_add_u16_e32 v16, v16, v17
	v_mul_lo_u16_e32 v16, 12, v16
	v_mov_b64_e32 v[22:23], s[52:53]
	v_cmp_lt_i32_e64 s[28:29], 11, v18
	v_sub_u16_e32 v20, v18, v16
	v_mad_i64_i32 v[16:17], s[6:7], v137, s73, v[22:23]
	v_cndmask_b32_e64 v18, v116, v117, s[28:29]
	v_mov_b32_e32 v19, v65
	v_lshl_add_u64 v[16:17], v[16:17], 0, v[18:19]
	v_add_u32_e32 v18, 0xfffffd80, v124
	v_mul_hi_i32 v19, v18, s82
	v_lshlrev_b32_sdwa v86, v118, sext(v20) dst_sel:DWORD dst_unused:UNUSED_PAD src0_sel:DWORD src1_sel:BYTE_0
	v_lshrrev_b32_e32 v20, 31, v19
	v_ashrrev_i32_e32 v19, 2, v19
	v_add_u32_e32 v136, v19, v20
	v_mul_lo_u32 v19, v136, 24
	v_sub_u32_e32 v20, v18, v19
	v_mul_lo_u16_e32 v18, 43, v20
	v_lshrrev_b16_e32 v19, 15, v18
	v_ashrrev_i16_e32 v18, 9, v18
	v_add_u16_e32 v18, v18, v19
	v_mul_lo_u16_e32 v18, 12, v18
	v_sub_u16_e32 v24, v20, v18
	v_cmp_lt_i32_e64 s[26:27], 11, v20
	v_mad_i64_i32 v[18:19], s[6:7], v136, s73, v[22:23]
	s_nop 0
	v_cndmask_b32_e64 v20, v116, v117, s[26:27]
	v_mov_b32_e32 v21, v65
	v_lshlrev_b32_sdwa v84, v118, sext(v24) dst_sel:DWORD dst_unused:UNUSED_PAD src0_sel:DWORD src1_sel:BYTE_0
	v_ashrrev_i32_e32 v87, 31, v86
	v_lshl_add_u64 v[18:19], v[18:19], 0, v[20:21]
	v_ashrrev_i32_e32 v85, 31, v84
	v_lshl_add_u64 v[16:17], v[86:87], 1, v[16:17]
	v_lshl_add_u64 v[18:19], v[84:85], 1, v[18:19]
	v_lshl_add_u64 v[16:17], v[16:17], 0, v[64:65]
	v_lshl_add_u64 v[20:21], v[18:19], 0, v[64:65]
	global_load_dwordx4 v[16:19], v[16:17], off nt
	s_nop 0
	global_load_dwordx4 v[48:51], v[20:21], off nt
	v_add_u32_e32 v20, 0xfffffdc0, v124
	v_mul_hi_i32 v21, v20, s82
	v_lshrrev_b32_e32 v24, 31, v21
	v_ashrrev_i32_e32 v21, 2, v21
	v_add_u32_e32 v135, v21, v24
	v_mul_lo_u32 v21, v135, 24
	v_sub_u32_e32 v24, v20, v21
	v_mul_lo_u16_e32 v20, 43, v24
	v_lshrrev_b16_e32 v21, 15, v20
	v_ashrrev_i16_e32 v20, 9, v20
	v_add_u16_e32 v20, v20, v21
	v_mul_lo_u16_e32 v20, 12, v20
	v_cmp_lt_i32_e64 s[24:25], 11, v24
	v_sub_u16_e32 v26, v24, v20
	v_mad_i64_i32 v[20:21], s[6:7], v135, s73, v[22:23]
	v_cndmask_b32_e64 v24, v116, v117, s[24:25]
	v_mov_b32_e32 v25, v65
	v_lshl_add_u64 v[20:21], v[20:21], 0, v[24:25]
	v_add_u32_e32 v24, 0xfffffe00, v124
	v_mul_hi_i32 v25, v24, s82
	v_lshlrev_b32_sdwa v82, v118, sext(v26) dst_sel:DWORD dst_unused:UNUSED_PAD src0_sel:DWORD src1_sel:BYTE_0
	v_lshrrev_b32_e32 v26, 31, v25
	v_ashrrev_i32_e32 v25, 2, v25
	v_add_u32_e32 v134, v25, v26
	v_mul_lo_u32 v25, v134, 24
	v_sub_u32_e32 v26, v24, v25
	v_mul_lo_u16_e32 v24, 43, v26
	v_lshrrev_b16_e32 v25, 15, v24
	v_ashrrev_i16_e32 v24, 9, v24
	v_add_u16_e32 v24, v24, v25
	v_mul_lo_u16_e32 v24, 12, v24
	v_cmp_lt_i32_e64 s[22:23], 11, v26
	s_waitcnt lgkmcnt(1)
	v_sub_u16_e32 v28, v26, v24
	v_mad_i64_i32 v[24:25], s[6:7], v134, s73, v[22:23]
	v_cndmask_b32_e64 v26, v116, v117, s[22:23]
	v_mov_b32_e32 v27, v65
	v_lshl_add_u64 v[24:25], v[24:25], 0, v[26:27]
	v_add_u32_e32 v26, 0xfffffe40, v124
	v_mul_hi_i32 v27, v26, s82
	v_lshlrev_b32_sdwa v80, v118, sext(v28) dst_sel:DWORD dst_unused:UNUSED_PAD src0_sel:DWORD src1_sel:BYTE_0
	v_lshrrev_b32_e32 v28, 31, v27
	v_ashrrev_i32_e32 v27, 2, v27
	v_add_u32_e32 v133, v27, v28
	v_mul_lo_u32 v27, v133, 24
	v_sub_u32_e32 v28, v26, v27
	v_mul_lo_u16_e32 v26, 43, v28
	v_lshrrev_b16_e32 v27, 15, v26
	v_ashrrev_i16_e32 v26, 9, v26
	v_add_u16_e32 v26, v26, v27
	v_mul_lo_u16_e32 v26, 12, v26
	v_cmp_lt_i32_e64 s[20:21], 11, v28
	v_sub_u16_e32 v30, v28, v26
	v_mad_i64_i32 v[26:27], s[6:7], v133, s73, v[22:23]
	v_cndmask_b32_e64 v28, v116, v117, s[20:21]
	s_waitcnt lgkmcnt(0)
	v_mov_b32_e32 v29, v65
	v_lshl_add_u64 v[26:27], v[26:27], 0, v[28:29]
	v_add_u32_e32 v28, 0xfffffe80, v124
	v_mul_hi_i32 v29, v28, s82
	v_lshlrev_b32_sdwa v78, v118, sext(v30) dst_sel:DWORD dst_unused:UNUSED_PAD src0_sel:DWORD src1_sel:BYTE_0
	v_lshrrev_b32_e32 v30, 31, v29
	v_ashrrev_i32_e32 v29, 2, v29
	v_add_u32_e32 v132, v29, v30
	v_mul_lo_u32 v29, v132, 24
	v_sub_u32_e32 v30, v28, v29
	v_mul_lo_u16_e32 v28, 43, v30
	v_lshrrev_b16_e32 v29, 15, v28
	v_ashrrev_i16_e32 v28, 9, v28
	v_add_u16_e32 v28, v28, v29
	v_mul_lo_u16_e32 v28, 12, v28
	v_cmp_lt_i32_e64 s[18:19], 11, v30
	v_sub_u16_e32 v32, v30, v28
	v_mad_i64_i32 v[28:29], s[6:7], v132, s73, v[22:23]
	v_cndmask_b32_e64 v30, v116, v117, s[18:19]
	v_mov_b32_e32 v31, v65
	v_lshl_add_u64 v[28:29], v[28:29], 0, v[30:31]
	v_add_u32_e32 v30, 0xfffffec0, v124
	v_mul_hi_i32 v31, v30, s82
	v_lshlrev_b32_sdwa v74, v118, sext(v32) dst_sel:DWORD dst_unused:UNUSED_PAD src0_sel:DWORD src1_sel:BYTE_0
	v_lshrrev_b32_e32 v32, 31, v31
	v_ashrrev_i32_e32 v31, 2, v31
	v_add_u32_e32 v131, v31, v32
	v_mul_lo_u32 v31, v131, 24
	v_sub_u32_e32 v32, v30, v31
	v_mul_lo_u16_e32 v30, 43, v32
	v_lshrrev_b16_e32 v31, 15, v30
	v_ashrrev_i16_e32 v30, 9, v30
	v_add_u16_e32 v30, v30, v31
	v_mul_lo_u16_e32 v30, 12, v30
	v_cmp_lt_i32_e64 s[16:17], 11, v32
	v_sub_u16_e32 v54, v32, v30
	v_mad_i64_i32 v[30:31], s[6:7], v131, s73, v[22:23]
	v_cndmask_b32_e64 v32, v116, v117, s[16:17]
	v_mov_b32_e32 v33, v65
	v_lshl_add_u64 v[30:31], v[30:31], 0, v[32:33]
	v_add_u32_e32 v32, 0xffffff00, v124
	v_mul_hi_i32 v33, v32, s82
	v_lshrrev_b32_e32 v34, 31, v33
	v_ashrrev_i32_e32 v33, 2, v33
	v_add_u32_e32 v130, v33, v34
	v_mul_lo_u32 v33, v130, 24
	v_sub_u32_e32 v34, v32, v33
	v_mul_lo_u16_e32 v32, 43, v34
	v_lshrrev_b16_e32 v33, 15, v32
	v_ashrrev_i16_e32 v32, 9, v32
	v_add_u16_e32 v32, v32, v33
	v_mul_lo_u16_e32 v32, 12, v32
	v_cmp_lt_i32_e64 s[14:15], 11, v34
	v_sub_u16_e32 v55, v34, v32
	v_mad_i64_i32 v[32:33], s[6:7], v130, s73, v[22:23]
	v_cndmask_b32_e64 v34, v116, v117, s[14:15]
	v_mov_b32_e32 v35, v65
	v_lshl_add_u64 v[32:33], v[32:33], 0, v[34:35]
	v_add_u32_e32 v34, 0xffffff40, v124
	v_mul_hi_i32 v35, v34, s82
	v_lshrrev_b32_e32 v36, 31, v35
	v_ashrrev_i32_e32 v35, 2, v35
	v_add_u32_e32 v129, v35, v36
	v_mul_lo_u32 v35, v129, 24
	v_sub_u32_e32 v36, v34, v35
	v_mul_lo_u16_e32 v34, 43, v36
	v_lshrrev_b16_e32 v35, 15, v34
	v_ashrrev_i16_e32 v34, 9, v34
	v_add_u16_e32 v34, v34, v35
	v_mul_lo_u16_e32 v34, 12, v34
	v_cmp_lt_i32_e64 s[12:13], 11, v36
	v_sub_u16_e32 v56, v36, v34
	v_mad_i64_i32 v[34:35], s[6:7], v129, s73, v[22:23]
	v_cndmask_b32_e64 v36, v116, v117, s[12:13]
	v_mov_b32_e32 v37, v65
	v_lshl_add_u64 v[34:35], v[34:35], 0, v[36:37]
	v_add_u32_e32 v36, 0xffffff80, v124
	v_mul_hi_i32 v37, v36, s82
	v_lshrrev_b32_e32 v38, 31, v37
	v_ashrrev_i32_e32 v37, 2, v37
	v_add_u32_e32 v128, v37, v38
	v_mul_lo_u32 v37, v128, 24
	v_sub_u32_e32 v38, v36, v37
	v_mul_lo_u16_e32 v36, 43, v38
	v_lshrrev_b16_e32 v37, 15, v36
	v_ashrrev_i16_e32 v36, 9, v36
	v_add_u16_e32 v36, v36, v37
	v_mul_lo_u16_e32 v36, 12, v36
	v_cmp_lt_i32_e64 s[10:11], 11, v38
	s_waitcnt vmcnt(1)
	v_lshlrev_b32_e32 v42, 16, v16
	v_and_b32_e32 v43, 0xffff0000, v16
	v_sub_u16_e32 v57, v38, v36
	v_mad_i64_i32 v[36:37], s[6:7], v128, s73, v[22:23]
	v_cndmask_b32_e64 v38, v116, v117, s[10:11]
	v_mov_b32_e32 v39, v65
	v_subrev_u32_e32 v58, 64, v124
	v_pk_mul_f32 v[44:45], v[42:43], v[42:43]
	v_lshlrev_b32_e32 v16, 16, v17
	v_and_b32_e32 v17, 0xffff0000, v17
	v_lshl_add_u64 v[36:37], v[36:37], 0, v[38:39]
	v_mul_hi_i32 v38, v58, s82
	v_pk_mul_f32 v[46:47], v[16:17], v[16:17]
	v_add_f32_e32 v44, v44, v45
	v_lshrrev_b32_e32 v39, 31, v38
	v_ashrrev_i32_e32 v38, 2, v38
	v_lshlrev_b32_e32 v52, 16, v18
	v_and_b32_e32 v53, 0xffff0000, v18
	v_add_f32_e32 v44, v46, v44
	v_add_u32_e32 v126, v38, v39
	v_and_b32_e32 v38, 0xffff0000, v19
	v_lshlrev_b32_e32 v39, 16, v19
	v_pk_mul_f32 v[18:19], v[52:53], v[52:53]
	v_add_f32_e32 v44, v47, v44
	v_add_f32_e32 v18, v18, v44
	v_pk_mul_f32 v[40:41], v[38:39], v[38:39]
	v_add_f32_e32 v18, v19, v18
	v_add_f32_e32 v18, v41, v18
	v_add_f32_e32 v40, v40, v18
	ds_swizzle_b32 v41, v40 offset:swizzle(SWAP,1)
	v_mul_lo_u32 v18, v126, 24
	v_sub_u32_e32 v45, v58, v18
	v_cmp_lt_i32_e64 s[8:9], 11, v45
	v_mad_i64_i32 v[18:19], s[6:7], v126, s73, v[22:23]
	s_waitcnt lgkmcnt(0)
	v_add_f32_e32 v44, v40, v41
	ds_swizzle_b32 v46, v44 offset:swizzle(SWAP,2)
	v_cndmask_b32_e64 v40, v116, v117, s[8:9]
	v_mov_b32_e32 v41, v65
	v_lshl_add_u64 v[18:19], v[18:19], 0, v[40:41]
	v_mul_hi_i32 v40, v124, s82
	s_waitcnt lgkmcnt(0)
	v_add_f32_e32 v41, v44, v46
	ds_swizzle_b32 v44, v41 offset:swizzle(SWAP,4)
	v_lshrrev_b32_e32 v46, 31, v40
	v_ashrrev_i32_e32 v40, 2, v40
	v_add_u32_e32 v127, v40, v46
	v_mul_lo_u32 v40, v127, 24
	s_waitcnt lgkmcnt(0)
	v_add_f32_e32 v41, v41, v44
	v_fmamk_f32 v41, v41, 0x3c800000, v107
	v_mul_f32_e32 v44, 0x4f800000, v41
	v_cmp_gt_f32_e32 vcc, s84, v41
	v_sub_u32_e32 v46, v124, v40
	v_mad_i64_i32 v[22:23], s[6:7], v127, s73, v[22:23]
	v_cndmask_b32_e32 v41, v41, v44, vcc
	v_sqrt_f32_e32 v44, v41
	v_lshlrev_b32_sdwa v70, v118, sext(v56) dst_sel:DWORD dst_unused:UNUSED_PAD src0_sel:DWORD src1_sel:BYTE_0
	v_ashrrev_i32_e32 v71, 31, v70
	v_lshlrev_b32_sdwa v68, v118, sext(v57) dst_sel:DWORD dst_unused:UNUSED_PAD src0_sel:DWORD src1_sel:BYTE_0
	v_add_u32_e32 v40, -1, v44
	v_fma_f32 v47, -v40, v44, v41
	v_cmp_ge_f32_e64 s[6:7], 0, v47
	v_add_u32_e32 v47, 1, v44
	v_ashrrev_i32_e32 v69, 31, v68
	v_cndmask_b32_e64 v40, v44, v40, s[6:7]
	v_fma_f32 v44, -v47, v44, v41
	v_cmp_lt_f32_e64 s[6:7], 0, v44
	v_lshlrev_b32_sdwa v76, v118, sext(v54) dst_sel:DWORD dst_unused:UNUSED_PAD src0_sel:DWORD src1_sel:BYTE_0
	v_lshlrev_b32_sdwa v72, v118, sext(v55) dst_sel:DWORD dst_unused:UNUSED_PAD src0_sel:DWORD src1_sel:BYTE_0
	v_cndmask_b32_e64 v40, v40, v47, s[6:7]
	v_mul_f32_e32 v44, 0x37800000, v40
	v_cndmask_b32_e32 v40, v40, v44, vcc
	v_cmp_class_f32_e32 vcc, v41, v108
	v_ashrrev_i32_e32 v83, 31, v82
	v_ashrrev_i32_e32 v81, 31, v80
	v_cndmask_b32_e32 v44, v40, v41, vcc
	v_div_scale_f32 v47, s[6:7], v44, v44, 1.0
	v_rcp_f32_e32 v58, v47
	v_cmp_lt_i32_e64 s[6:7], 11, v46
	v_mov_b32_e32 v41, v65
	v_ashrrev_i32_e32 v79, 31, v78
	v_cndmask_b32_e64 v40, v116, v117, s[6:7]
	v_lshl_add_u64 v[22:23], v[22:23], 0, v[40:41]
	v_fma_f32 v40, -v47, v58, 1.0
	v_fmac_f32_e32 v58, v40, v58
	v_div_scale_f32 v40, vcc, 1.0, v44, 1.0
	v_mul_f32_e32 v41, v40, v58
	v_fma_f32 v59, -v47, v41, v40
	v_fmac_f32_e32 v41, v59, v58
	v_fma_f32 v40, -v47, v41, v40
	v_div_fmas_f32 v47, v40, v58, v41
	v_div_fixup_f32 v44, v47, v44, 1.0
	v_cndmask_b32_e64 v41, v9, v13, s[28:29]
	v_cndmask_b32_e64 v40, v8, v12, s[28:29]
	v_pk_mul_f32 v[42:43], v[44:45], v[42:43] op_sel_hi:[0,1]
	v_pk_mul_f32 v[88:89], v[40:41], v[42:43]
	v_cndmask_b32_e64 v41, v11, v15, s[28:29]
	v_cndmask_b32_e64 v40, v10, v14, s[28:29]
	v_pk_mul_f32 v[16:17], v[44:45], v[16:17] op_sel_hi:[0,1]
	v_pk_mul_f32 v[92:93], v[40:41], v[16:17]
	v_pk_mul_f32 v[16:17], v[44:45], v[52:53] op_sel_hi:[0,1]
	v_cndmask_b32_e64 v41, v1, v5, s[28:29]
	v_cndmask_b32_e64 v40, v0, v4, s[28:29]
	v_pk_mul_f32 v[90:91], v[40:41], v[16:17]
	v_mul_lo_u16_e32 v16, 43, v45
	v_lshrrev_b16_e32 v17, 15, v16
	v_ashrrev_i16_e32 v16, 9, v16
	v_add_u16_e32 v40, v16, v17
	v_lshl_add_u64 v[16:17], v[70:71], 1, v[34:35]
	v_mul_lo_u16_e32 v34, 12, v40
	v_sub_u16_e32 v40, v45, v34
	v_lshl_add_u64 v[34:35], v[68:69], 1, v[36:37]
	v_lshl_add_u64 v[138:139], v[34:35], 0, v[64:65]
	v_pk_mul_f32 v[34:35], v[44:45], v[38:39] op_sel_hi:[0,1]
	v_cndmask_b32_e64 v37, v3, v7, s[28:29]
	v_cndmask_b32_e64 v36, v2, v6, s[28:29]
	v_pk_mul_f32 v[94:95], v[36:37], v[34:35] op_sel:[0,1] op_sel_hi:[1,0]
	v_mul_lo_u16_e32 v34, 43, v46
	v_lshrrev_b16_e32 v35, 15, v34
	v_ashrrev_i16_e32 v34, 9, v34
	v_add_u16_e32 v34, v34, v35
	v_mul_lo_u16_e32 v34, 12, v34
	v_lshlrev_b32_sdwa v62, v118, sext(v40) dst_sel:DWORD dst_unused:UNUSED_PAD src0_sel:DWORD src1_sel:BYTE_0
	v_sub_u16_e32 v34, v46, v34
	v_ashrrev_i32_e32 v75, 31, v74
	v_ashrrev_i32_e32 v77, 31, v76
	v_ashrrev_i32_e32 v73, 31, v72
	v_ashrrev_i32_e32 v63, 31, v62
	v_lshlrev_b32_sdwa v60, v118, sext(v34) dst_sel:DWORD dst_unused:UNUSED_PAD src0_sel:DWORD src1_sel:BYTE_0
	v_lshl_add_u64 v[20:21], v[82:83], 1, v[20:21]
	v_lshl_add_u64 v[24:25], v[80:81], 1, v[24:25]
	v_lshl_add_u64 v[26:27], v[78:79], 1, v[26:27]
	v_lshl_add_u64 v[28:29], v[74:75], 1, v[28:29]
	v_lshl_add_u64 v[30:31], v[76:77], 1, v[30:31]
	v_lshl_add_u64 v[32:33], v[72:73], 1, v[32:33]
	v_lshl_add_u64 v[18:19], v[62:63], 1, v[18:19]
	v_ashrrev_i32_e32 v61, 31, v60
	v_lshl_add_u64 v[20:21], v[20:21], 0, v[64:65]
	v_lshl_add_u64 v[24:25], v[24:25], 0, v[64:65]
	v_lshl_add_u64 v[26:27], v[26:27], 0, v[64:65]
	v_lshl_add_u64 v[28:29], v[28:29], 0, v[64:65]
	v_lshl_add_u64 v[30:31], v[30:31], 0, v[64:65]
	v_lshl_add_u64 v[32:33], v[32:33], 0, v[64:65]
	v_lshl_add_u64 v[16:17], v[16:17], 0, v[64:65]
	v_lshl_add_u64 v[18:19], v[18:19], 0, v[64:65]
	v_lshl_add_u64 v[22:23], v[60:61], 1, v[22:23]
	v_lshl_add_u64 v[140:141], v[22:23], 0, v[64:65]
	global_load_dwordx4 v[56:59], v[20:21], off nt
	global_load_dwordx4 v[52:55], v[24:25], off nt
	global_load_dwordx4 v[44:47], v[26:27], off nt
	global_load_dwordx4 v[40:43], v[28:29], off nt
	global_load_dwordx4 v[36:39], v[30:31], off nt
	s_nop 0
	global_load_dwordx4 v[32:35], v[32:33], off nt
	s_nop 0
	global_load_dwordx4 v[28:31], v[16:17], off nt
	global_load_dwordx4 v[24:27], v[138:139], off nt
	global_load_dwordx4 v[20:23], v[18:19], off nt
	s_nop 0
	global_load_dwordx4 v[16:19], v[140:141], off nt
	ds_swizzle_b32 v98, v88 offset:swizzle(SWAP,1)
	ds_swizzle_b32 v99, v89 offset:swizzle(SWAP,1)
	ds_swizzle_b32 v100, v92 offset:swizzle(SWAP,1)
	ds_swizzle_b32 v101, v93 offset:swizzle(SWAP,1)
	ds_swizzle_b32 v102, v90 offset:swizzle(SWAP,1)
	ds_swizzle_b32 v103, v91 offset:swizzle(SWAP,1)
	ds_swizzle_b32 v96, v94 offset:swizzle(SWAP,1)
	ds_swizzle_b32 v97, v95 offset:swizzle(SWAP,1)
	s_and_saveexec_b64 s[56:57], s[2:3]
	s_cbranch_execz .LBB0_226
	v_lshl_add_u32 v146, v137, 6, s60
	ds_read2_b32 v[138:139], v146 offset0:8 offset1:9
	ds_read2_b32 v[140:141], v146 offset0:10 offset1:11
	ds_read2_b32 v[142:143], v146 offset0:12 offset1:13
	ds_read2_b32 v[144:145], v146 offset0:14 offset1:15
	s_waitcnt lgkmcnt(3)
	v_pk_mul_f32 v[98:99], v[138:139], v[98:99]
	s_waitcnt lgkmcnt(2)
	v_pk_mul_f32 v[100:101], v[140:141], v[100:101]
	s_waitcnt lgkmcnt(1)
	v_pk_mul_f32 v[102:103], v[142:143], v[102:103]
	ds_read2_b32 v[138:139], v146 offset1:1
	ds_read2_b32 v[140:141], v146 offset0:2 offset1:3
	ds_read2_b32 v[142:143], v146 offset0:4 offset1:5
	ds_read2_b32 v[146:147], v146 offset0:6 offset1:7
	s_waitcnt lgkmcnt(4)
	v_pk_mul_f32 v[96:97], v[144:145], v[96:97]
	v_cndmask_b32_e64 v99, v99, -v99, s[4:5]
	v_cndmask_b32_e64 v98, v98, -v98, s[4:5]
	v_cndmask_b32_e64 v101, v101, -v101, s[4:5]
	v_cndmask_b32_e64 v100, v100, -v100, s[4:5]
	v_cndmask_b32_e64 v102, v102, -v102, s[4:5]
	v_cndmask_b32_e64 v103, v103, -v103, s[4:5]
	v_cndmask_b32_e64 v96, v96, -v96, s[4:5]
	v_cndmask_b32_e64 v97, v97, -v97, s[4:5]
	s_waitcnt lgkmcnt(0)
	v_pk_fma_f32 v[94:95], v[94:95], v[146:147], v[96:97]
	v_pk_fma_f32 v[90:91], v[90:91], v[142:143], v[102:103]
	v_pk_fma_f32 v[92:93], v[92:93], v[140:141], v[100:101]
	v_pk_fma_f32 v[88:89], v[88:89], v[138:139], v[98:99]

.LBB0_248:
	s_add_i32 s54, s54, s96
	s_cmpk_lt_u32 s54, 0x1000
	s_cselect_b64 s[2:3], -1, 0
	s_and_b64 s[2:3], s[2:3], exec
	s_cselect_b32 s6, 7, 0
	s_or_b32 s4, s46, 6
	s_cmpk_lt_u32 s54, 0x1000
	s_cselect_b64 s[2:3], -1, 0
	s_and_b64 s[2:3], s[2:3], exec
	s_cselect_b32 s8, s4, s46
	s_or_b32 s4, s46, 5
	s_cmpk_lt_u32 s54, 0x1000
	s_cselect_b64 s[2:3], -1, 0
	s_and_b64 s[2:3], s[2:3], exec
	s_cselect_b32 s9, s4, s46
	s_or_b32 s4, s46, 4
	s_cmpk_lt_u32 s54, 0x1000
	s_cselect_b64 s[2:3], -1, 0
	s_and_b64 s[2:3], s[2:3], exec
	s_cselect_b32 s10, s4, s46
	s_or_b32 s4, s46, 3
	s_cmpk_lt_u32 s54, 0x1000
	s_cselect_b64 s[2:3], -1, 0
	s_and_b64 s[2:3], s[2:3], exec
	s_cselect_b32 s11, s4, s46
	s_or_b32 s4, s46, 2
	s_cmpk_lt_u32 s54, 0x1000
	v_lshlrev_b32_e32 v64, 2, v67
	v_lshl_add_u64 v[0:1], s[52:53], 0, v[64:65]
	s_mov_b64 s[2:3], 0x1e00
	s_cselect_b64 vcc, -1, 0
	v_lshl_add_u64 v[2:3], v[0:1], 0, s[2:3]
	s_and_b64 s[2:3], vcc, exec
	s_cselect_b32 s12, s4, s46
	s_add_i32 s7, s46, -1
	s_add_i32 s2, s7, s96
	s_cmpk_lt_u32 s2, 0x1000
	s_cselect_b64 s[2:3], -1, 0
	s_and_b64 s[4:5], s[2:3], exec
	v_cndmask_b32_e64 v8, 0, 1, vcc
	s_cselect_b32 s13, s7, s46
	v_mad_i64_i32 v[4:5], s[4:5], s13, v121, v[2:3]
	v_or_b32_e32 v20, s46, v8
	s_or_b32 s14, s6, s46
	s_waitcnt lgkmcnt(0)
	s_barrier
	v_mad_i64_i32 v[6:7], s[4:5], s46, v121, v[2:3]
	v_mad_i64_i32 v[8:9], s[4:5], v20, s73, v[2:3]
	v_mad_i64_i32 v[10:11], s[4:5], s12, v121, v[2:3]
	v_mad_i64_i32 v[12:13], s[4:5], s11, v121, v[2:3]
	v_mad_i64_i32 v[14:15], s[4:5], s10, v121, v[2:3]
	v_mad_i64_i32 v[16:17], s[4:5], s9, v121, v[2:3]
	v_mad_i64_i32 v[18:19], s[4:5], s8, v121, v[2:3]
	global_load_dword v21, v[4:5], off nt
	global_load_dword v22, v[6:7], off nt
	global_load_dword v23, v[8:9], off nt
	global_load_dword v24, v[10:11], off nt
	global_load_dword v25, v[12:13], off nt
	global_load_dword v26, v[14:15], off nt
	global_load_dword v27, v[16:17], off nt
	global_load_dword v28, v[18:19], off nt
	v_mad_i64_i32 v[4:5], s[4:5], s14, v121, v[2:3]
	s_add_i32 s15, s46, 8
	s_add_i32 s4, s15, s96
	s_cmpk_lt_u32 s4, 0x1000
	s_cselect_b64 s[4:5], -1, 0
	s_and_b64 s[6:7], s[4:5], exec
	s_cselect_b32 s15, s15, s46
	v_mad_i64_i32 v[2:3], s[6:7], s15, v121, v[2:3]
	s_mov_b64 s[6:7], 0x2400
	s_nop 0
	v_lshl_add_u64 v[6:7], v[0:1], 0, s[6:7]
	v_mad_i64_i32 v[8:9], s[6:7], s13, v121, v[6:7]
	v_mad_i64_i32 v[18:19], s[6:7], s10, v121, v[6:7]
	v_mad_i64_i32 v[10:11], s[6:7], s46, v121, v[6:7]
	v_mad_i64_i32 v[12:13], s[6:7], v20, s73, v[6:7]
	v_mad_i64_i32 v[14:15], s[6:7], s12, v121, v[6:7]
	v_mad_i64_i32 v[16:17], s[6:7], s11, v121, v[6:7]
	global_load_dword v29, v[4:5], off nt
	global_load_dword v30, v[2:3], off nt
	global_load_dword v31, v[8:9], off nt
	global_load_dword v32, v[10:11], off nt
	global_load_dword v33, v[12:13], off nt
	global_load_dword v34, v[14:15], off nt
	global_load_dword v35, v[16:17], off nt
	s_nop 0
	global_load_dword v18, v[18:19], off nt
	v_mad_i64_i32 v[2:3], s[6:7], s9, v121, v[6:7]
	v_mad_i64_i32 v[4:5], s[6:7], s8, v121, v[6:7]
	v_mad_i64_i32 v[8:9], s[6:7], s14, v121, v[6:7]
	v_mad_i64_i32 v[6:7], s[6:7], s15, v121, v[6:7]
	s_mov_b64 s[6:7], 0x2a00
	s_nop 0
	v_lshl_add_u64 v[0:1], v[0:1], 0, s[6:7]
	v_mad_i64_i32 v[10:11], s[6:7], s13, v121, v[0:1]
	v_mad_i64_i32 v[12:13], s[6:7], s46, v121, v[0:1]
	v_mad_i64_i32 v[14:15], s[6:7], v20, s73, v[0:1]
	v_mad_i64_i32 v[16:17], s[6:7], s12, v121, v[0:1]
	global_load_dword v19, v[2:3], off nt
	global_load_dword v20, v[4:5], off nt
	global_load_dword v36, v[8:9], off nt
	global_load_dword v37, v[6:7], off nt
	global_load_dword v38, v[10:11], off nt
	s_nop 0
	global_load_dword v12, v[12:13], off nt
	s_nop 0
	global_load_dword v13, v[14:15], off nt
	s_nop 0
	global_load_dword v14, v[16:17], off nt
	v_mad_i64_i32 v[2:3], s[6:7], s11, v121, v[0:1]
	v_mad_i64_i32 v[4:5], s[6:7], s10, v121, v[0:1]
	v_mad_i64_i32 v[6:7], s[6:7], s9, v121, v[0:1]
	v_mad_i64_i32 v[8:9], s[6:7], s8, v121, v[0:1]
	v_mad_i64_i32 v[10:11], s[6:7], s14, v121, v[0:1]
	v_mad_i64_i32 v[0:1], s[6:7], s15, v121, v[0:1]
	global_load_dword v2, v[2:3], off nt
	s_nop 0
	global_load_dword v3, v[4:5], off nt
	s_nop 0
	global_load_dword v4, v[6:7], off nt
	global_load_dword v5, v[8:9], off nt
	s_nop 0
	global_load_dword v6, v[10:11], off nt
	s_nop 0
	global_load_dword v0, v[0:1], off nt
	s_mov_b32 s46, 0
	s_mul_i32 s18, s65, 6
	s_xor_b32 s19, s95, 63
	s_mul_i32 s20, s65, 12
	s_waitcnt vmcnt(29)
	v_cndmask_b32_e64 v68, 0, v21, s[2:3]
	s_waitcnt vmcnt(28)
	v_cndmask_b32_e32 v69, 0, v22, vcc
	s_waitcnt vmcnt(27)
	v_cndmask_b32_e32 v70, 0, v23, vcc
	s_waitcnt vmcnt(26)
	v_cndmask_b32_e32 v71, 0, v24, vcc
	s_waitcnt vmcnt(25)
	v_cndmask_b32_e32 v72, 0, v25, vcc
	s_waitcnt vmcnt(24)
	v_cndmask_b32_e32 v73, 0, v26, vcc
	s_waitcnt vmcnt(23)
	v_cndmask_b32_e32 v74, 0, v27, vcc
	s_waitcnt vmcnt(22)
	v_cndmask_b32_e32 v75, 0, v28, vcc
	s_waitcnt vmcnt(21)
	v_cndmask_b32_e32 v76, 0, v29, vcc
	s_waitcnt vmcnt(20)
	v_cndmask_b32_e64 v77, 0, v30, s[4:5]
	s_waitcnt vmcnt(19)
	v_cndmask_b32_e64 v78, 0, v31, s[2:3]
	s_waitcnt vmcnt(18)
	v_cndmask_b32_e32 v79, 0, v32, vcc
	s_waitcnt vmcnt(17)
	v_cndmask_b32_e32 v80, 0, v33, vcc
	s_waitcnt vmcnt(16)
	v_cndmask_b32_e32 v81, 0, v34, vcc
	s_waitcnt vmcnt(15)
	v_cndmask_b32_e32 v82, 0, v35, vcc
	s_waitcnt vmcnt(14)
	v_cndmask_b32_e32 v83, 0, v18, vcc
	s_waitcnt vmcnt(13)
	v_cndmask_b32_e32 v84, 0, v19, vcc
	s_waitcnt vmcnt(12)
	v_cndmask_b32_e32 v85, 0, v20, vcc
	s_waitcnt vmcnt(11)
	v_cndmask_b32_e32 v86, 0, v36, vcc
	s_waitcnt vmcnt(10)
	v_cndmask_b32_e64 v87, 0, v37, s[4:5]
	s_waitcnt vmcnt(9)
	v_cndmask_b32_e64 v88, 0, v38, s[2:3]
	s_waitcnt vmcnt(8)
	v_cndmask_b32_e32 v89, 0, v12, vcc
	s_waitcnt vmcnt(7)
	v_cndmask_b32_e32 v90, 0, v13, vcc
	s_waitcnt vmcnt(6)
	v_cndmask_b32_e32 v91, 0, v14, vcc
	s_waitcnt vmcnt(5)
	v_cndmask_b32_e32 v92, 0, v2, vcc
	s_waitcnt vmcnt(4)
	v_cndmask_b32_e32 v93, 0, v3, vcc
	s_waitcnt vmcnt(3)
	v_cndmask_b32_e32 v94, 0, v4, vcc
	s_waitcnt vmcnt(2)
	v_cndmask_b32_e32 v95, 0, v5, vcc
	s_waitcnt vmcnt(1)
	v_cndmask_b32_e32 v96, 0, v6, vcc
	s_waitcnt vmcnt(0)
	v_cndmask_b32_e64 v97, 0, v0, s[4:5]
	s_branch .LBB0_250

.LBB0_250:
	s_waitcnt lgkmcnt(0)
	s_barrier
	v_lshlrev_b32_e32 v32, 16, v69
	v_and_b32_e32 v38, 63, v123
	v_lshlrev_b32_e32 v39, 1, v38
	v_lshl_or_b32 v64, s46, 7, v39
	v_lshlrev_b64 v[0:1], 2, v[64:65]
	v_lshl_add_u64 v[28:29], s[42:43], 0, v[0:1]
	global_load_dwordx2 v[2:3], v[28:29], off
	v_lshl_add_u64 v[30:31], s[34:35], 0, v[0:1]
	global_load_dwordx2 v[4:5], v[30:31], off
	v_lshl_add_u64 v[0:1], s[44:45], 0, v[0:1]
	global_load_dwordx2 v[6:7], v[0:1], off
	global_load_dwordx2 v[18:19], v[28:29], off offset:3072
	global_load_dwordx2 v[16:17], v[30:31], off offset:3072
	v_add_co_u32_e32 v30, vcc, s74, v30
	v_and_b32_e32 v33, 0xffff0000, v69
	s_nop 0
	v_addc_co_u32_e32 v31, vcc, 0, v31, vcc
	v_add_co_u32_e32 v40, vcc, s74, v28
	v_lshlrev_b32_e32 v26, 16, v70
	s_nop 0
	v_addc_co_u32_e32 v41, vcc, 0, v29, vcc
	v_and_b32_e32 v27, 0xffff0000, v70
	v_lshlrev_b32_e32 v34, 16, v68
	v_and_b32_e32 v35, 0xffff0000, v68
	global_load_dwordx2 v[36:37], v[0:1], off offset:3072
	global_load_dwordx2 v[28:29], v[30:31], off offset:2048
	s_nop 0
	global_load_dwordx2 v[30:31], v[40:41], off offset:2048
	v_lshlrev_b32_e32 v24, 16, v71
	v_and_b32_e32 v25, 0xffff0000, v71
	v_readfirstlane_b32 s6, v123
	s_ashr_i32 s7, s6, 6
	s_lshl_b32 s2, s7, 11
	s_lshl_b32 s3, s7, 1
	s_add_i32 s9, s64, s2
	s_and_b32 s10, s3, 2
	v_lshlrev_b32_e32 v22, 16, v72
	v_and_b32_e32 v23, 0xffff0000, v72
	v_lshlrev_b32_e32 v20, 16, v73
	v_and_b32_e32 v21, 0xffff0000, v73
	v_lshlrev_b32_e32 v14, 16, v74
	v_and_b32_e32 v15, 0xffff0000, v74
	v_lshlrev_b32_e32 v8, 16, v75
	v_and_b32_e32 v9, 0xffff0000, v75
	s_lshl_b32 s8, s7, 3
	v_lshlrev_b32_e32 v12, 16, v76
	v_and_b32_e32 v13, 0xffff0000, v76
	v_lshlrev_b32_e32 v10, 16, v77
	v_and_b32_e32 v11, 0xffff0000, v77
	s_add_i32 s21, s46, 1
	s_waitcnt vmcnt(7)
	v_pk_mul_f32 v[40:41], v[2:3], v[32:33]
	v_pk_mul_f32 v[42:43], v[2:3], v[26:27]
	s_waitcnt vmcnt(6)
	v_pk_fma_f32 v[34:35], v[4:5], v[34:35], v[40:41]
	v_pk_fma_f32 v[32:33], v[4:5], v[32:33], v[42:43]
	s_waitcnt vmcnt(5)
	v_pk_fma_f32 v[34:35], v[6:7], v[26:27], v[34:35]
	v_pk_fma_f32 v[42:43], v[6:7], v[24:25], v[32:33]
	v_mul_f32_e32 v32, 0xbfb8aa3b, v35
	v_mul_f32_e32 v33, 0xbfb8aa3b, v34
	v_exp_f32_e32 v32, v32
	v_exp_f32_e32 v33, v33
	v_mul_f32_e32 v40, 0xbfb8aa3b, v43
	v_mul_f32_e32 v41, 0xbfb8aa3b, v42
	v_add_f32_e32 v32, 1.0, v32
	v_add_f32_e32 v33, 1.0, v33
	v_exp_f32_e32 v40, v40
	v_exp_f32_e32 v41, v41
	v_rcp_f32_e32 v45, v32
	v_rcp_f32_e32 v44, v33
	v_add_f32_e32 v40, 1.0, v40
	v_add_f32_e32 v41, 1.0, v41
	v_rcp_f32_e32 v47, v40
	v_pk_mul_f32 v[34:35], v[34:35], v[44:45]
	v_rcp_f32_e32 v46, v41
	v_pk_mul_f32 v[44:45], v[34:35], v[34:35]
	v_bfe_u32 v40, v123, 2, 4
	v_add_f32_e32 v33, v44, v45
	ds_swizzle_b32 v44, v33 offset:swizzle(SWAP,1)
	v_pk_mul_f32 v[42:43], v[42:43], v[46:47]
	v_lshlrev_b32_e32 v32, 2, v123
	v_pk_mul_f32 v[46:47], v[42:43], v[42:43]
	v_and_b32_e32 v48, 12, v32
	v_add_f32_e32 v41, v46, v47
	ds_swizzle_b32 v45, v41 offset:swizzle(SWAP,1)
	s_waitcnt lgkmcnt(1)
	v_add_f32_e32 v33, v33, v44
	ds_swizzle_b32 v44, v33 offset:swizzle(SWAP,2)
	v_bitop3_b32 v46, s3, v40, 2 bitop3:0x6c
	v_lshlrev_b32_e32 v46, 4, v46
	s_waitcnt lgkmcnt(1)
	v_add_f32_e32 v41, v41, v45
	ds_swizzle_b32 v45, v41 offset:swizzle(SWAP,2)
	s_waitcnt lgkmcnt(1)
	v_add_f32_e32 v33, v33, v44
	ds_swizzle_b32 v44, v33 offset:swizzle(SWAP,4)
	s_waitcnt lgkmcnt(1)
	v_add_f32_e32 v41, v41, v45
	ds_swizzle_b32 v45, v41 offset:swizzle(SWAP,4)
	s_waitcnt lgkmcnt(1)
	v_add_f32_e32 v33, v33, v44
	ds_swizzle_b32 v47, v33 offset:swizzle(SWAP,8)
	s_waitcnt lgkmcnt(1)
	v_add_f32_e32 v41, v41, v45
	ds_swizzle_b32 v49, v41 offset:swizzle(SWAP,8)
	v_pk_mul_f32 v[44:45], v[2:3], v[24:25]
	s_waitcnt lgkmcnt(1)
	v_add_f32_e32 v33, v33, v47
	v_pk_fma_f32 v[26:27], v[4:5], v[26:27], v[44:45]
	ds_swizzle_b32 v44, v33 offset:swizzle(SWAP,16)
	s_waitcnt lgkmcnt(1)
	v_add_f32_e32 v41, v41, v49
	ds_swizzle_b32 v45, v41 offset:swizzle(SWAP,16)
	v_pk_fma_f32 v[26:27], v[6:7], v[22:23], v[26:27]
	s_waitcnt lgkmcnt(1)
	v_add_f32_e32 v33, v33, v44
	v_mov_b32_e32 v44, v33
	s_nop 1
	v_permlane32_swap_b32_e32 v33, v44
	v_add_f32_e32 v33, v33, v44
	v_add_f32_e32 v33, 0x358637bd, v33
	s_waitcnt lgkmcnt(0)
	v_add_f32_e32 v41, v41, v45
	v_mul_f32_e32 v44, 0x4f800000, v33
	v_cmp_gt_f32_e32 vcc, s84, v33
	v_mov_b32_e32 v45, v41
	s_nop 1
	v_permlane32_swap_b32_e32 v41, v45
	v_cndmask_b32_e32 v33, v33, v44, vcc
	v_sqrt_f32_e32 v44, v33
	v_add_f32_e32 v41, v41, v45
	v_add_f32_e32 v41, 0x358637bd, v41
	v_mul_f32_e32 v45, 0x4f800000, v41
	v_cmp_gt_f32_e64 s[2:3], s84, v41
	v_add_u32_e32 v51, 1, v44
	v_fma_f32 v54, -v51, v44, v33
	v_cndmask_b32_e64 v41, v41, v45, s[2:3]
	v_add_u32_e32 v45, -1, v44
	v_fma_f32 v53, -v45, v44, v33
	v_cmp_ge_f32_e64 s[4:5], 0, v53
	v_sqrt_f32_e32 v50, v41
	v_mul_f32_e32 v47, 0xbfb8aa3b, v27
	v_cndmask_b32_e64 v44, v44, v45, s[4:5]
	v_cmp_lt_f32_e64 s[4:5], 0, v54
	v_add_u32_e32 v52, -1, v50
	v_fma_f32 v55, -v52, v50, v41
	v_cndmask_b32_e64 v44, v44, v51, s[4:5]
	v_mul_f32_e32 v45, 0x37800000, v44
	v_cndmask_b32_e32 v44, v44, v45, vcc
	v_cmp_class_f32_e32 vcc, v33, v108
	v_mul_f32_e32 v49, 0xbfb8aa3b, v26
	v_exp_f32_e32 v47, v47
	v_cndmask_b32_e32 v33, v44, v33, vcc
	v_div_scale_f32 v44, s[4:5], v33, v33, 1.0
	v_rcp_f32_e32 v45, v44
	v_cmp_ge_f32_e32 vcc, 0, v55
	v_exp_f32_e32 v49, v49
	s_or_b32 s4, s8, 4
	v_fma_f32 v53, -v44, v45, 1.0
	v_cndmask_b32_e32 v51, v50, v52, vcc
	v_div_scale_f32 v52, vcc, 1.0, v33, 1.0
	v_fmac_f32_e32 v45, v53, v45
	v_mul_f32_e32 v53, v52, v45
	v_fma_f32 v54, -v44, v53, v52
	v_fmac_f32_e32 v53, v54, v45
	v_fma_f32 v44, -v44, v53, v52
	v_div_fmas_f32 v44, v44, v45, v53
	v_div_fixup_f32 v33, v44, v33, 1.0
	v_mul_f32_e32 v44, 0x3db504f3, v33
	v_pk_mul_f32 v[34:35], v[34:35], v[44:45] op_sel_hi:[1,0]
	v_add_u32_e32 v33, 1, v50
	v_cvt_pk_bf16_f32 v34, v34, v35
	v_add_f32_e32 v35, 1.0, v47
	v_rcp_f32_e32 v45, v35
	v_add_f32_e32 v35, 1.0, v49
	v_rcp_f32_e32 v44, v35
	v_fma_f32 v35, -v33, v50, v41
	v_cmp_lt_f32_e32 vcc, 0, v35
	s_or_b32 s5, s8, 5
	v_pk_mul_f32 v[44:45], v[26:27], v[44:45]
	v_cndmask_b32_e32 v33, v51, v33, vcc
	v_pk_mul_f32 v[26:27], v[44:45], v[44:45]
	v_mul_f32_e32 v35, 0x37800000, v33
	v_add_f32_e32 v26, v26, v27
	ds_swizzle_b32 v27, v26 offset:swizzle(SWAP,1)
	v_cndmask_b32_e64 v33, v33, v35, s[2:3]
	v_cmp_class_f32_e32 vcc, v41, v108
	s_waitcnt lgkmcnt(0)
	v_add_f32_e32 v27, v26, v27
	ds_swizzle_b32 v35, v27 offset:swizzle(SWAP,2)
	v_cndmask_b32_e32 v33, v33, v41, vcc
	v_div_scale_f32 v41, s[2:3], v33, v33, 1.0
	v_rcp_f32_e32 v47, v41
	s_waitcnt lgkmcnt(0)
	v_add_f32_e32 v27, v27, v35
	ds_swizzle_b32 v35, v27 offset:swizzle(SWAP,4)
	v_add3_u32 v26, s9, v46, v48
	v_fma_f32 v46, -v41, v47, 1.0
	v_fmac_f32_e32 v47, v46, v47
	v_div_scale_f32 v46, vcc, 1.0, v33, 1.0
	s_waitcnt lgkmcnt(0)
	v_add_f32_e32 v27, v27, v35
	ds_swizzle_b32 v35, v27 offset:swizzle(SWAP,8)
	v_mul_f32_e32 v49, v46, v47
	v_fma_f32 v50, -v41, v49, v46
	v_fmac_f32_e32 v49, v50, v47
	v_fma_f32 v41, -v41, v49, v46
	s_waitcnt lgkmcnt(0)
	v_add_f32_e32 v27, v27, v35
	ds_swizzle_b32 v35, v27 offset:swizzle(SWAP,16)
	v_div_fmas_f32 v41, v41, v47, v49
	v_div_fixup_f32 v33, v41, v33, 1.0
	v_mul_f32_e32 v46, 0x3db504f3, v33
	v_pk_mul_f32 v[42:43], v[42:43], v[46:47] op_sel_hi:[1,0]
	s_waitcnt lgkmcnt(0)
	v_add_f32_e32 v27, v27, v35
	v_mov_b32_e32 v33, v27
	s_nop 1
	v_permlane32_swap_b32_e32 v27, v33
	v_add_f32_e32 v27, v27, v33
	v_add_f32_e32 v27, 0x358637bd, v27
	v_mul_f32_e32 v33, 0x4f800000, v27
	v_cmp_gt_f32_e32 vcc, s84, v27
	v_bitop3_b32 v41, s10, v40, 4 bitop3:0x36
	v_lshlrev_b32_e32 v41, 4, v41
	v_cndmask_b32_e32 v33, v27, v33, vcc
	v_sqrt_f32_e32 v35, v33
	v_cvt_pk_bf16_f32 v27, v42, v43
	v_add_u32_e32 v42, -1, v35
	v_fma_f32 v43, -v42, v35, v33
	v_cmp_ge_f32_e64 s[2:3], 0, v43
	v_add_u32_e32 v49, 1, v35
	s_nop 0
	v_cndmask_b32_e64 v46, v35, v42, s[2:3]
	v_pk_mul_f32 v[42:43], v[2:3], v[22:23]
	v_fma_f32 v35, -v49, v35, v33
	v_pk_fma_f32 v[24:25], v[4:5], v[24:25], v[42:43]
	v_cmp_lt_f32_e64 s[2:3], 0, v35
	v_pk_fma_f32 v[24:25], v[6:7], v[20:21], v[24:25]
	s_nop 0
	v_mul_f32_e32 v42, 0xbfb8aa3b, v25
	v_exp_f32_e32 v42, v42
	v_mul_f32_e32 v43, 0xbfb8aa3b, v24
	v_exp_f32_e32 v47, v43
	v_cndmask_b32_e64 v35, v46, v49, s[2:3]
	v_add_f32_e32 v42, 1.0, v42
	v_rcp_f32_e32 v43, v42
	v_add_f32_e32 v42, 1.0, v47
	v_rcp_f32_e32 v42, v42
	v_mul_f32_e32 v46, 0x37800000, v35
	v_cndmask_b32_e32 v35, v35, v46, vcc
	v_cmp_class_f32_e32 vcc, v33, v108
	v_pk_mul_f32 v[42:43], v[24:25], v[42:43]
	s_nop 0
	v_pk_mul_f32 v[24:25], v[42:43], v[42:43]
	v_cndmask_b32_e32 v33, v35, v33, vcc
	v_add_f32_e32 v24, v24, v25
	ds_swizzle_b32 v25, v24 offset:swizzle(SWAP,1)
	v_div_scale_f32 v46, s[2:3], v33, v33, 1.0
	v_rcp_f32_e32 v47, v46
	s_waitcnt lgkmcnt(0)
	v_add_f32_e32 v25, v24, v25
	ds_swizzle_b32 v35, v25 offset:swizzle(SWAP,2)
	v_add3_u32 v24, s9, v41, v48
	v_fma_f32 v41, -v46, v47, 1.0
	v_fmac_f32_e32 v47, v41, v47
	v_div_scale_f32 v41, vcc, 1.0, v33, 1.0
	s_waitcnt lgkmcnt(0)
	v_add_f32_e32 v25, v25, v35
	ds_swizzle_b32 v35, v25 offset:swizzle(SWAP,4)
	v_mul_f32_e32 v49, v41, v47
	v_fma_f32 v50, -v46, v49, v41
	v_fmac_f32_e32 v49, v50, v47
	v_fma_f32 v41, -v46, v49, v41
	s_waitcnt lgkmcnt(0)
	v_add_f32_e32 v25, v25, v35
	ds_swizzle_b32 v35, v25 offset:swizzle(SWAP,8)
	v_div_fmas_f32 v41, v41, v47, v49
	v_div_fixup_f32 v33, v41, v33, 1.0
	v_mul_f32_e32 v46, 0x3db504f3, v33
	v_pk_mul_f32 v[44:45], v[44:45], v[46:47] op_sel_hi:[1,0]
	s_waitcnt lgkmcnt(0)
	v_add_f32_e32 v25, v25, v35
	ds_swizzle_b32 v35, v25 offset:swizzle(SWAP,16)
	v_bitop3_b32 v41, s10, v40, 8 bitop3:0x36
	s_waitcnt lgkmcnt(0)
	v_add_f32_e32 v25, v25, v35
	v_mov_b32_e32 v33, v25
	s_nop 1
	v_permlane32_swap_b32_e32 v25, v33
	v_add_f32_e32 v25, v25, v33
	v_add_f32_e32 v25, 0x358637bd, v25
	v_mul_f32_e32 v33, 0x4f800000, v25
	v_cmp_gt_f32_e32 vcc, s84, v25
	s_nop 1
	v_cndmask_b32_e32 v25, v25, v33, vcc
	v_sqrt_f32_e32 v35, v25
	v_cvt_pk_bf16_f32 v33, v44, v45
	v_add_u32_e32 v44, -1, v35
	v_fma_f32 v45, -v44, v35, v25
	v_cmp_ge_f32_e64 s[2:3], 0, v45
	v_add_u32_e32 v47, 1, v35
	s_nop 0
	v_cndmask_b32_e64 v46, v35, v44, s[2:3]
	v_pk_mul_f32 v[44:45], v[2:3], v[20:21]
	v_fma_f32 v35, -v47, v35, v25
	v_pk_fma_f32 v[22:23], v[4:5], v[22:23], v[44:45]
	v_cmp_lt_f32_e64 s[2:3], 0, v35
	v_pk_fma_f32 v[22:23], v[6:7], v[14:15], v[22:23]
	s_nop 0
	v_mul_f32_e32 v44, 0xbfb8aa3b, v23
	v_exp_f32_e32 v44, v44
	v_mul_f32_e32 v45, 0xbfb8aa3b, v22
	v_exp_f32_e32 v49, v45
	v_cndmask_b32_e64 v35, v46, v47, s[2:3]
	v_add_f32_e32 v44, 1.0, v44
	v_rcp_f32_e32 v45, v44
	v_add_f32_e32 v44, 1.0, v49
	v_rcp_f32_e32 v44, v44
	v_mul_f32_e32 v46, 0x37800000, v35
	v_cndmask_b32_e32 v35, v35, v46, vcc
	v_cmp_class_f32_e32 vcc, v25, v108
	v_pk_mul_f32 v[44:45], v[22:23], v[44:45]
	s_nop 0
	v_pk_mul_f32 v[22:23], v[44:45], v[44:45]
	v_cndmask_b32_e32 v25, v35, v25, vcc
	v_add_f32_e32 v22, v22, v23
	ds_swizzle_b32 v23, v22 offset:swizzle(SWAP,1)
	v_div_scale_f32 v35, s[2:3], v25, v25, 1.0
	v_rcp_f32_e32 v46, v35
	s_waitcnt lgkmcnt(0)
	v_add_f32_e32 v23, v22, v23
	ds_swizzle_b32 v47, v23 offset:swizzle(SWAP,2)
	v_lshlrev_b32_e32 v22, 4, v41
	v_fma_f32 v41, -v35, v46, 1.0
	v_fmac_f32_e32 v46, v41, v46
	v_add3_u32 v22, s9, v22, v48
	s_waitcnt lgkmcnt(0)
	v_add_f32_e32 v23, v23, v47
	ds_swizzle_b32 v41, v23 offset:swizzle(SWAP,4)
	v_div_scale_f32 v47, vcc, 1.0, v25, 1.0
	v_mul_f32_e32 v49, v47, v46
	v_fma_f32 v50, -v35, v49, v47
	s_waitcnt lgkmcnt(0)
	v_add_f32_e32 v23, v23, v41
	ds_swizzle_b32 v41, v23 offset:swizzle(SWAP,8)
	v_fmac_f32_e32 v49, v50, v46
	v_fma_f32 v35, -v35, v49, v47
	v_div_fmas_f32 v35, v35, v46, v49
	v_div_fixup_f32 v25, v35, v25, 1.0
	s_waitcnt lgkmcnt(0)
	v_add_f32_e32 v23, v23, v41
	ds_swizzle_b32 v41, v23 offset:swizzle(SWAP,16)
	v_mul_f32_e32 v46, 0x3db504f3, v25
	v_pk_mul_f32 v[42:43], v[42:43], v[46:47] op_sel_hi:[1,0]
	s_waitcnt lgkmcnt(0)
	v_add_f32_e32 v23, v23, v41
	v_mov_b32_e32 v35, v23
	s_nop 1
	v_permlane32_swap_b32_e32 v23, v35
	v_add_f32_e32 v23, v23, v35
	v_add_f32_e32 v23, 0x358637bd, v23
	v_mul_f32_e32 v35, 0x4f800000, v23
	v_cmp_gt_f32_e32 vcc, s84, v23
	v_cvt_pk_bf16_f32 v25, v42, v43
	s_nop 0
	v_cndmask_b32_e32 v35, v23, v35, vcc
	v_sqrt_f32_e32 v41, v35
	v_bitop3_b32 v23, s10, v40, 12 bitop3:0x36
	v_lshlrev_b32_e32 v23, 4, v23
	v_add3_u32 v23, s9, v23, v48
	v_add_u32_e32 v42, -1, v41
	v_fma_f32 v43, -v42, v41, v35
	v_cmp_ge_f32_e64 s[2:3], 0, v43
	v_add_u32_e32 v43, 1, v41
	s_nop 0
	v_cndmask_b32_e64 v42, v41, v42, s[2:3]
	v_fma_f32 v41, -v43, v41, v35
	v_cmp_lt_f32_e64 s[2:3], 0, v41
	s_nop 1
	v_cndmask_b32_e64 v41, v42, v43, s[2:3]
	v_pk_mul_f32 v[42:43], v[2:3], v[14:15]
	v_mul_f32_e32 v47, 0x37800000, v41
	v_pk_fma_f32 v[20:21], v[4:5], v[20:21], v[42:43]
	v_cndmask_b32_e32 v41, v41, v47, vcc
	v_pk_fma_f32 v[20:21], v[6:7], v[8:9], v[20:21]
	v_cmp_class_f32_e32 vcc, v35, v108
	v_mul_f32_e32 v42, 0xbfb8aa3b, v21
	v_exp_f32_e32 v42, v42
	v_mul_f32_e32 v43, 0xbfb8aa3b, v20
	v_exp_f32_e32 v46, v43
	v_cndmask_b32_e32 v35, v41, v35, vcc
	v_add_f32_e32 v42, 1.0, v42
	v_rcp_f32_e32 v43, v42
	v_add_f32_e32 v42, 1.0, v46
	v_rcp_f32_e32 v42, v42
	v_div_scale_f32 v41, s[2:3], v35, v35, 1.0
	v_rcp_f32_e32 v46, v41
	v_pk_mul_f32 v[42:43], v[20:21], v[42:43]
	s_lshr_b32 s3, s4, 2
	v_pk_mul_f32 v[20:21], v[42:43], v[42:43]
	v_fma_f32 v47, -v41, v46, 1.0
	v_add_f32_e32 v20, v20, v21
	ds_swizzle_b32 v21, v20 offset:swizzle(SWAP,1)
	v_fmac_f32_e32 v46, v47, v46
	v_div_scale_f32 v47, vcc, 1.0, v35, 1.0
	v_mul_f32_e32 v49, v47, v46
	s_waitcnt lgkmcnt(0)
	v_add_f32_e32 v20, v20, v21
	ds_swizzle_b32 v21, v20 offset:swizzle(SWAP,2)
	v_fma_f32 v50, -v41, v49, v47
	v_fmac_f32_e32 v49, v50, v46
	v_fma_f32 v41, -v41, v49, v47
	s_lshl_b32 s2, s4, 8
	s_waitcnt lgkmcnt(0)
	v_add_f32_e32 v20, v20, v21
	ds_swizzle_b32 v21, v20 offset:swizzle(SWAP,4)
	s_add_i32 s2, s64, s2
	s_waitcnt lgkmcnt(0)
	v_add_f32_e32 v47, v20, v21
	ds_swizzle_b32 v50, v47 offset:swizzle(SWAP,8)
	v_div_fmas_f32 v20, v41, v46, v49
	v_div_fixup_f32 v20, v20, v35, 1.0
	v_mul_f32_e32 v20, 0x3db504f3, v20
	v_pk_mul_f32 v[20:21], v[44:45], v[20:21] op_sel_hi:[1,0]
	s_waitcnt lgkmcnt(0)
	v_add_f32_e32 v35, v47, v50
	ds_swizzle_b32 v41, v35 offset:swizzle(SWAP,16)
	v_cvt_pk_bf16_f32 v21, v20, v21
	s_waitcnt lgkmcnt(0)
	v_add_f32_e32 v20, v35, v41
	v_mov_b32_e32 v35, v20
	s_nop 1
	v_permlane32_swap_b32_e32 v20, v35
	v_add_f32_e32 v20, v20, v35
	v_add_f32_e32 v20, 0x358637bd, v20
	v_mul_f32_e32 v35, 0x4f800000, v20
	v_cmp_gt_f32_e32 vcc, s84, v20
	s_nop 1
	v_cndmask_b32_e32 v35, v20, v35, vcc
	v_sqrt_f32_e32 v41, v35
	v_bitop3_b32 v20, s3, v40, 3 bitop3:0x6c
	v_lshlrev_b32_e32 v20, 4, v20
	v_add3_u32 v20, s2, v20, v48
	v_add_u32_e32 v44, -1, v41
	v_fma_f32 v45, -v44, v41, v35
	v_cmp_ge_f32_e64 s[2:3], 0, v45
	v_add_u32_e32 v45, 1, v41
	s_nop 0
	v_cndmask_b32_e64 v44, v41, v44, s[2:3]
	v_fma_f32 v41, -v45, v41, v35
	v_cmp_lt_f32_e64 s[2:3], 0, v41
	s_nop 1
	v_cndmask_b32_e64 v41, v44, v45, s[2:3]
	v_pk_mul_f32 v[44:45], v[2:3], v[8:9]
	v_mul_f32_e32 v47, 0x37800000, v41
	v_pk_fma_f32 v[14:15], v[4:5], v[14:15], v[44:45]
	v_cndmask_b32_e32 v41, v41, v47, vcc
	v_pk_fma_f32 v[14:15], v[6:7], v[12:13], v[14:15]
	v_cmp_class_f32_e32 vcc, v35, v108
	v_mul_f32_e32 v44, 0xbfb8aa3b, v15
	v_exp_f32_e32 v44, v44
	v_mul_f32_e32 v45, 0xbfb8aa3b, v14
	v_exp_f32_e32 v46, v45
	v_cndmask_b32_e32 v35, v41, v35, vcc
	v_add_f32_e32 v44, 1.0, v44
	v_rcp_f32_e32 v45, v44
	v_add_f32_e32 v44, 1.0, v46
	v_rcp_f32_e32 v44, v44
	v_div_scale_f32 v41, s[2:3], v35, v35, 1.0
	v_rcp_f32_e32 v46, v41
	v_pk_mul_f32 v[44:45], v[14:15], v[44:45]
	v_pk_mul_f32 v[2:3], v[2:3], v[12:13]
	v_pk_mul_f32 v[14:15], v[44:45], v[44:45]
	v_fma_f32 v47, -v41, v46, 1.0
	v_add_f32_e32 v14, v14, v15
	ds_swizzle_b32 v15, v14 offset:swizzle(SWAP,1)
	v_fmac_f32_e32 v46, v47, v46
	v_div_scale_f32 v47, vcc, 1.0, v35, 1.0
	v_mul_f32_e32 v49, v47, v46
	s_waitcnt lgkmcnt(0)
	v_add_f32_e32 v14, v14, v15
	ds_swizzle_b32 v15, v14 offset:swizzle(SWAP,2)
	v_fma_f32 v50, -v41, v49, v47
	v_fmac_f32_e32 v49, v50, v46
	v_fma_f32 v41, -v41, v49, v47
	v_pk_fma_f32 v[2:3], v[4:5], v[8:9], v[2:3]
	s_waitcnt lgkmcnt(0)
	v_add_f32_e32 v14, v14, v15
	ds_swizzle_b32 v15, v14 offset:swizzle(SWAP,4)
	v_pk_fma_f32 v[2:3], v[6:7], v[10:11], v[2:3]
	s_lshl_b32 s2, s5, 8
	v_mul_f32_e32 v4, 0xbfb8aa3b, v3
	v_exp_f32_e32 v4, v4
	s_waitcnt lgkmcnt(0)
	v_add_f32_e32 v15, v14, v15
	ds_swizzle_b32 v47, v15 offset:swizzle(SWAP,8)
	v_div_fmas_f32 v14, v41, v46, v49
	v_div_fixup_f32 v14, v14, v35, 1.0
	v_mul_f32_e32 v5, 0xbfb8aa3b, v2
	v_exp_f32_e32 v6, v5
	s_waitcnt lgkmcnt(0)
	v_add_f32_e32 v35, v15, v47
	ds_swizzle_b32 v41, v35 offset:swizzle(SWAP,16)
	v_mul_f32_e32 v14, 0x3db504f3, v14
	v_pk_mul_f32 v[14:15], v[42:43], v[14:15] op_sel_hi:[1,0]
	v_add_f32_e32 v4, 1.0, v4
	v_cvt_pk_bf16_f32 v15, v14, v15
	s_waitcnt lgkmcnt(0)
	v_add_f32_e32 v14, v35, v41
	v_mov_b32_e32 v35, v14
	v_rcp_f32_e32 v5, v4
	v_add_f32_e32 v4, 1.0, v6
	v_permlane32_swap_b32_e32 v14, v35
	v_rcp_f32_e32 v4, v4
	v_add_f32_e32 v14, v14, v35
	v_add_f32_e32 v14, 0x358637bd, v14
	v_mul_f32_e32 v35, 0x4f800000, v14
	v_cmp_gt_f32_e32 vcc, s84, v14
	v_pk_mul_f32 v[2:3], v[2:3], v[4:5]
	s_add_i32 s9, s64, s2
	v_cndmask_b32_e32 v14, v14, v35, vcc
	v_sqrt_f32_e32 v35, v14
	v_pk_mul_f32 v[4:5], v[2:3], v[2:3]
	s_bfe_u32 s2, s5, 0x20002
	v_add_f32_e32 v4, v4, v5
	ds_swizzle_b32 v5, v4 offset:swizzle(SWAP,1)
	v_add_u32_e32 v42, -1, v35
	v_fma_f32 v43, -v42, v35, v14
	v_bitop3_b32 v41, s2, v40, 4 bitop3:0x36
	v_cmp_ge_f32_e64 s[2:3], 0, v43
	v_add_u32_e32 v43, 1, v35
	v_fma_f32 v7, -v43, v35, v14
	s_waitcnt lgkmcnt(0)
	v_add_f32_e32 v4, v4, v5
	v_cndmask_b32_e64 v42, v35, v42, s[2:3]
	v_cmp_lt_f32_e64 s[2:3], 0, v7
	ds_swizzle_b32 v5, v4 offset:swizzle(SWAP,2)
	v_lshlrev_b32_e32 v41, 4, v41
	v_cndmask_b32_e64 v6, v42, v43, s[2:3]
	v_mul_f32_e32 v7, 0x37800000, v6
	v_cndmask_b32_e32 v6, v6, v7, vcc
	v_cmp_class_f32_e32 vcc, v14, v108
	s_waitcnt lgkmcnt(0)
	v_add_f32_e32 v4, v4, v5
	ds_swizzle_b32 v5, v4 offset:swizzle(SWAP,4)
	v_cndmask_b32_e32 v6, v6, v14, vcc
	v_div_scale_f32 v7, s[2:3], v6, v6, 1.0
	v_rcp_f32_e32 v8, v7
	s_waitcnt lgkmcnt(0)
	v_add_f32_e32 v4, v4, v5
	ds_swizzle_b32 v5, v4 offset:swizzle(SWAP,8)
	v_add3_u32 v12, s9, v41, v48
	v_fma_f32 v9, -v7, v8, 1.0
	v_fmac_f32_e32 v8, v9, v8
	v_div_scale_f32 v9, vcc, 1.0, v6, 1.0
	v_mul_f32_e32 v10, v9, v8
	v_fma_f32 v11, -v7, v10, v9
	v_fmac_f32_e32 v10, v11, v8
	v_fma_f32 v7, -v7, v10, v9
	v_div_fmas_f32 v7, v7, v8, v10
	v_div_fixup_f32 v6, v7, v6, 1.0
	s_waitcnt lgkmcnt(0)
	v_add_f32_e32 v7, v4, v5
	ds_swizzle_b32 v8, v7 offset:swizzle(SWAP,16)
	v_mul_f32_e32 v4, 0x3db504f3, v6
	v_pk_mul_f32 v[4:5], v[44:45], v[4:5] op_sel_hi:[1,0]
	s_or_b32 s9, s8, 6
	v_cvt_pk_bf16_f32 v35, v4, v5
	s_waitcnt lgkmcnt(0)
	v_add_f32_e32 v4, v7, v8
	v_mov_b32_e32 v5, v4
	s_nop 1
	v_permlane32_swap_b32_e32 v4, v5
	v_add_f32_e32 v4, v4, v5
	v_add_f32_e32 v4, 0x358637bd, v4
	v_mul_f32_e32 v5, 0x4f800000, v4
	v_cmp_gt_f32_e32 vcc, s84, v4
	s_lshl_b32 s2, s9, 8
	s_add_i32 s10, s64, s2
	v_cndmask_b32_e32 v4, v4, v5, vcc
	v_sqrt_f32_e32 v5, v4
	s_bfe_u32 s2, s9, 0x20002
	v_bitop3_b32 v6, s2, v40, 8 bitop3:0x36
	v_lshlrev_b32_e32 v42, 16, v79
	v_add_u32_e32 v7, -1, v5
	v_fma_f32 v8, -v7, v5, v4
	v_cmp_ge_f32_e64 s[2:3], 0, v8
	v_add_u32_e32 v8, 1, v5
	v_and_b32_e32 v43, 0xffff0000, v79
	v_cndmask_b32_e64 v7, v5, v7, s[2:3]
	v_fma_f32 v5, -v8, v5, v4
	v_cmp_lt_f32_e64 s[2:3], 0, v5
	v_lshlrev_b32_e32 v44, 16, v80
	v_and_b32_e32 v45, 0xffff0000, v80
	v_cndmask_b32_e64 v5, v7, v8, s[2:3]
	v_mul_f32_e32 v7, 0x37800000, v5
	v_cndmask_b32_e32 v5, v5, v7, vcc
	v_cmp_class_f32_e32 vcc, v4, v108
	v_and_b32_e32 v41, 0xffff0000, v81
	v_and_b32_e32 v49, 0xffff0000, v82
	v_cndmask_b32_e32 v8, v5, v4, vcc
	v_div_scale_f32 v4, s[2:3], v8, v8, 1.0
	v_rcp_f32_e32 v9, v4
	v_lshlrev_b32_e32 v5, 4, v6
	v_add3_u32 v13, s10, v5, v48
	s_or_b32 s10, s8, 7
	v_fma_f32 v5, -v4, v9, 1.0
	v_fmac_f32_e32 v9, v5, v9
	v_div_scale_f32 v5, vcc, 1.0, v8, 1.0
	v_mul_f32_e32 v10, v5, v9
	v_fma_f32 v6, -v4, v10, v5
	v_fmac_f32_e32 v10, v6, v9
	v_fma_f32 v11, -v4, v10, v5
	v_lshlrev_b32_e32 v4, 16, v78
	v_and_b32_e32 v5, 0xffff0000, v78
	s_waitcnt vmcnt(4)
	v_pk_mul_f32 v[6:7], v[18:19], v[42:43]
	v_div_fmas_f32 v9, v11, v9, v10
	s_waitcnt vmcnt(3)
	v_pk_fma_f32 v[4:5], v[16:17], v[4:5], v[6:7]
	v_div_fixup_f32 v8, v9, v8, 1.0
	s_waitcnt vmcnt(2)
	v_pk_fma_f32 v[4:5], v[36:37], v[44:45], v[4:5]
	v_mul_f32_e32 v8, 0x3db504f3, v8
	v_mul_f32_e32 v6, 0xbfb8aa3b, v5
	v_exp_f32_e32 v6, v6
	v_mul_f32_e32 v7, 0xbfb8aa3b, v4
	v_exp_f32_e32 v14, v7
	v_pk_mul_f32 v[2:3], v[2:3], v[8:9] op_sel_hi:[1,0]
	v_add_f32_e32 v6, 1.0, v6
	v_rcp_f32_e32 v7, v6
	v_add_f32_e32 v6, 1.0, v14
	v_rcp_f32_e32 v6, v6
	v_cvt_pk_bf16_f32 v52, v2, v3
	s_bfe_u32 s3, s10, 0x20002
	s_lshl_b32 s2, s10, 8
	v_pk_mul_f32 v[46:47], v[4:5], v[6:7]
	s_add_i32 s2, s64, s2
	v_pk_mul_f32 v[4:5], v[46:47], v[46:47]
	v_lshlrev_b32_e32 v10, 16, v83
	v_add_f32_e32 v4, v4, v5
	ds_swizzle_b32 v5, v4 offset:swizzle(SWAP,1)
	v_and_b32_e32 v11, 0xffff0000, v83
	v_lshlrev_b32_e32 v8, 16, v84
	v_and_b32_e32 v9, 0xffff0000, v84
	v_lshlrev_b32_e32 v6, 16, v86
	s_waitcnt lgkmcnt(0)
	v_add_f32_e32 v2, v4, v5
	ds_swizzle_b32 v3, v2 offset:swizzle(SWAP,2)
	v_bitop3_b32 v4, s3, v40, 12 bitop3:0x36
	v_lshlrev_b32_e32 v4, 4, v4
	v_add3_u32 v14, s2, v4, v48
	v_lshlrev_b32_e32 v40, 16, v81
	s_waitcnt lgkmcnt(0)
	v_add_f32_e32 v2, v2, v3
	ds_swizzle_b32 v3, v2 offset:swizzle(SWAP,4)
	v_lshlrev_b32_e32 v48, 16, v82
	v_and_b32_e32 v7, 0xffff0000, v86
	s_cmp_eq_u32 s46, 5
	s_waitcnt lgkmcnt(0)
	v_add_f32_e32 v3, v2, v3
	ds_swizzle_b32 v4, v3 offset:swizzle(SWAP,8)
	v_lshlrev_b32_e32 v2, 16, v85
	s_waitcnt lgkmcnt(0)
	v_add_f32_e32 v5, v3, v4
	ds_swizzle_b32 v50, v5 offset:swizzle(SWAP,16)
	v_and_b32_e32 v3, 0xffff0000, v85
	v_lshlrev_b32_e32 v4, 16, v87
	s_waitcnt lgkmcnt(0)
	v_add_f32_e32 v5, v5, v50
	v_mov_b32_e32 v50, v5
	s_nop 1
	v_permlane32_swap_b32_e32 v5, v50
	v_add_f32_e32 v5, v5, v50
	v_add_f32_e32 v5, 0x358637bd, v5
	v_mul_f32_e32 v50, 0x4f800000, v5
	v_cmp_gt_f32_e32 vcc, s84, v5
	s_nop 1
	v_cndmask_b32_e32 v5, v5, v50, vcc
	v_pk_mul_f32 v[50:51], v[18:19], v[44:45]
	v_sqrt_f32_e32 v53, v5
	v_pk_fma_f32 v[42:43], v[16:17], v[42:43], v[50:51]
	v_add_u32_e32 v55, -1, v53
	v_pk_fma_f32 v[42:43], v[36:37], v[40:41], v[42:43]
	s_nop 0
	v_mul_f32_e32 v50, 0xbfb8aa3b, v43
	v_exp_f32_e32 v50, v50
	v_mul_f32_e32 v51, 0xbfb8aa3b, v42
	v_exp_f32_e32 v54, v51
	v_add_f32_e32 v50, 1.0, v50
	v_rcp_f32_e32 v51, v50
	v_add_f32_e32 v50, 1.0, v54
	v_rcp_f32_e32 v50, v50
	v_fma_f32 v54, -v55, v53, v5
	v_cmp_ge_f32_e64 s[2:3], 0, v54
	v_pk_mul_f32 v[42:43], v[42:43], v[50:51]
	s_nop 0
	v_pk_mul_f32 v[50:51], v[42:43], v[42:43]
	v_cndmask_b32_e64 v54, v53, v55, s[2:3]
	v_add_f32_e32 v50, v50, v51
	ds_swizzle_b32 v51, v50 offset:swizzle(SWAP,1)
	v_add_u32_e32 v55, 1, v53
	v_fma_f32 v53, -v55, v53, v5
	v_cmp_lt_f32_e64 s[2:3], 0, v53
	s_waitcnt lgkmcnt(0)
	v_add_f32_e32 v50, v50, v51
	ds_swizzle_b32 v51, v50 offset:swizzle(SWAP,2)
	v_cndmask_b32_e64 v53, v54, v55, s[2:3]
	v_mul_f32_e32 v54, 0x37800000, v53
	v_cndmask_b32_e32 v53, v53, v54, vcc
	v_cmp_class_f32_e32 vcc, v5, v108
	s_waitcnt lgkmcnt(0)
	v_add_f32_e32 v50, v50, v51
	ds_swizzle_b32 v51, v50 offset:swizzle(SWAP,4)
	v_cndmask_b32_e32 v53, v53, v5, vcc
	v_div_scale_f32 v54, s[2:3], v53, v53, 1.0
	v_rcp_f32_e32 v55, v54
	s_waitcnt lgkmcnt(0)
	v_add_f32_e32 v50, v50, v51
	ds_swizzle_b32 v51, v50 offset:swizzle(SWAP,8)
	v_and_b32_e32 v5, 0xffff0000, v87
	v_fma_f32 v56, -v54, v55, 1.0
	v_fmac_f32_e32 v55, v56, v55
	v_div_scale_f32 v56, vcc, 1.0, v53, 1.0
	s_waitcnt lgkmcnt(0)
	v_add_f32_e32 v50, v50, v51
	ds_swizzle_b32 v51, v50 offset:swizzle(SWAP,16)
	v_mul_f32_e32 v57, v56, v55
	v_fma_f32 v58, -v54, v57, v56
	v_fmac_f32_e32 v57, v58, v55
	v_fma_f32 v54, -v54, v57, v56
	s_waitcnt lgkmcnt(0)
	v_add_f32_e32 v50, v50, v51
	v_mov_b32_e32 v51, v50
	s_nop 1
	v_permlane32_swap_b32_e32 v50, v51
	v_add_f32_e32 v50, v50, v51
	v_add_f32_e32 v50, 0x358637bd, v50
	v_mul_f32_e32 v51, 0x4f800000, v50
	v_cmp_gt_f32_e64 s[2:3], s84, v50
	s_nop 1
	v_cndmask_b32_e64 v56, v50, v51, s[2:3]
	v_div_fmas_f32 v50, v54, v55, v57
	v_div_fixup_f32 v50, v50, v53, 1.0
	v_pk_mul_f32 v[46:47], v[46:47], v[50:51] op_sel_hi:[1,0]
	v_pk_mul_f32 v[50:51], v[18:19], v[40:41]
	v_sqrt_f32_e32 v58, v56
	v_pk_fma_f32 v[44:45], v[16:17], v[44:45], v[50:51]
	v_cvt_pk_bf16_f32 v46, v46, v47
	v_pk_fma_f32 v[44:45], v[36:37], v[48:49], v[44:45]
	v_add_u32_e32 v53, -1, v58
	v_mul_f32_e32 v50, 0xbfb8aa3b, v45
	v_exp_f32_e32 v50, v50
	v_mul_f32_e32 v51, 0xbfb8aa3b, v44
	v_exp_f32_e32 v54, v51
	v_fma_f32 v55, -v53, v58, v56
	v_add_f32_e32 v50, 1.0, v50
	v_rcp_f32_e32 v51, v50
	v_add_f32_e32 v50, 1.0, v54
	v_rcp_f32_e32 v50, v50
	v_add_u32_e32 v54, 1, v58
	v_cmp_ge_f32_e32 vcc, 0, v55
	v_fma_f32 v55, -v54, v58, v56
	v_pk_mul_f32 v[44:45], v[44:45], v[50:51]
	v_cndmask_b32_e32 v53, v58, v53, vcc
	v_pk_mul_f32 v[50:51], v[44:45], v[44:45]
	v_cmp_lt_f32_e32 vcc, 0, v55
	v_add_f32_e32 v50, v50, v51
	ds_swizzle_b32 v51, v50 offset:swizzle(SWAP,1)
	v_cndmask_b32_e32 v53, v53, v54, vcc
	v_mul_f32_e32 v54, 0x37800000, v53
	v_cndmask_b32_e64 v53, v53, v54, s[2:3]
	v_cmp_class_f32_e32 vcc, v56, v108
	s_waitcnt lgkmcnt(0)
	v_add_f32_e32 v50, v50, v51
	ds_swizzle_b32 v51, v50 offset:swizzle(SWAP,2)
	v_cndmask_b32_e32 v53, v53, v56, vcc
	v_div_scale_f32 v54, s[2:3], v53, v53, 1.0
	v_rcp_f32_e32 v55, v54
	s_waitcnt lgkmcnt(0)
	v_add_f32_e32 v50, v50, v51
	ds_swizzle_b32 v51, v50 offset:swizzle(SWAP,4)
	ds_write2st64_b32 v26, v46, v34 offset1:64
	v_fma_f32 v34, -v54, v55, 1.0
	v_fmac_f32_e32 v55, v34, v55
	v_div_scale_f32 v47, vcc, 1.0, v53, 1.0
	s_waitcnt lgkmcnt(1)
	v_add_f32_e32 v34, v50, v51
	ds_swizzle_b32 v46, v34 offset:swizzle(SWAP,8)
	v_mul_f32_e32 v50, v47, v55
	v_fma_f32 v51, -v54, v50, v47
	v_fmac_f32_e32 v50, v51, v55
	v_fma_f32 v47, -v54, v50, v47
	s_waitcnt lgkmcnt(0)
	v_add_f32_e32 v34, v34, v46
	ds_swizzle_b32 v46, v34 offset:swizzle(SWAP,16)
	v_div_fmas_f32 v47, v47, v55, v50
	s_waitcnt lgkmcnt(0)
	v_add_f32_e32 v34, v34, v46
	v_mov_b32_e32 v46, v34
	s_nop 1
	v_permlane32_swap_b32_e32 v34, v46
	v_add_f32_e32 v34, v34, v46
	v_add_f32_e32 v34, 0x358637bd, v34
	v_mul_f32_e32 v46, 0x4f800000, v34
	v_cmp_gt_f32_e32 vcc, s84, v34
	s_nop 1
	v_cndmask_b32_e32 v46, v34, v46, vcc
	v_sqrt_f32_e32 v50, v46
	v_div_fixup_f32 v34, v47, v53, 1.0
	v_pk_mul_f32 v[42:43], v[42:43], v[34:35] op_sel_hi:[1,0]
	v_add_u32_e32 v53, 1, v50
	v_cvt_pk_bf16_f32 v34, v42, v43
	v_add_u32_e32 v42, -1, v50
	v_fma_f32 v43, -v42, v50, v46
	v_cmp_ge_f32_e64 s[2:3], 0, v43
	ds_write2st64_b32 v24, v34, v27 offset0:1 offset1:65
	s_nop 0
	v_cndmask_b32_e64 v47, v50, v42, s[2:3]
	v_pk_mul_f32 v[42:43], v[18:19], v[48:49]
	v_fma_f32 v50, -v53, v50, v46
	v_pk_fma_f32 v[40:41], v[16:17], v[40:41], v[42:43]
	v_cmp_lt_f32_e64 s[2:3], 0, v50
	v_pk_fma_f32 v[40:41], v[36:37], v[10:11], v[40:41]
	s_nop 0
	v_mul_f32_e32 v42, 0xbfb8aa3b, v41
	v_exp_f32_e32 v42, v42
	v_mul_f32_e32 v43, 0xbfb8aa3b, v40
	v_exp_f32_e32 v51, v43
	v_cndmask_b32_e64 v47, v47, v53, s[2:3]
	v_add_f32_e32 v42, 1.0, v42
	v_rcp_f32_e32 v43, v42
	v_add_f32_e32 v42, 1.0, v51
	v_rcp_f32_e32 v42, v42
	v_mul_f32_e32 v50, 0x37800000, v47
	v_cndmask_b32_e32 v47, v47, v50, vcc
	v_cmp_class_f32_e32 vcc, v46, v108
	v_pk_mul_f32 v[40:41], v[40:41], v[42:43]
	s_nop 0
	v_pk_mul_f32 v[42:43], v[40:41], v[40:41]
	v_cndmask_b32_e32 v46, v47, v46, vcc
	v_add_f32_e32 v42, v42, v43
	ds_swizzle_b32 v43, v42 offset:swizzle(SWAP,1)
	v_div_scale_f32 v47, s[2:3], v46, v46, 1.0
	v_rcp_f32_e32 v50, v47
	s_waitcnt lgkmcnt(0)
	v_add_f32_e32 v42, v42, v43
	ds_swizzle_b32 v43, v42 offset:swizzle(SWAP,2)
	s_waitcnt lgkmcnt(0)
	v_add_f32_e32 v27, v42, v43
	ds_swizzle_b32 v34, v27 offset:swizzle(SWAP,4)
	v_fma_f32 v42, -v47, v50, 1.0
	v_fmac_f32_e32 v50, v42, v50
	v_div_scale_f32 v42, vcc, 1.0, v46, 1.0
	s_waitcnt lgkmcnt(0)
	v_add_f32_e32 v27, v27, v34
	ds_swizzle_b32 v34, v27 offset:swizzle(SWAP,8)
	v_mul_f32_e32 v43, v42, v50
	v_fma_f32 v51, -v47, v43, v42
	v_fmac_f32_e32 v43, v51, v50
	v_fma_f32 v42, -v47, v43, v42
	s_waitcnt lgkmcnt(0)
	v_add_f32_e32 v27, v27, v34
	ds_swizzle_b32 v47, v27 offset:swizzle(SWAP,16)
	v_div_fmas_f32 v34, v42, v50, v43
	v_div_fixup_f32 v34, v34, v46, 1.0
	v_pk_mul_f32 v[42:43], v[44:45], v[34:35] op_sel_hi:[1,0]
	s_waitcnt lgkmcnt(0)
	v_add_f32_e32 v27, v27, v47
	v_cvt_pk_bf16_f32 v34, v42, v43
	v_mov_b32_e32 v42, v27
	s_nop 1
	v_permlane32_swap_b32_e32 v27, v42
	v_add_f32_e32 v27, v27, v42
	v_add_f32_e32 v27, 0x358637bd, v27
	v_mul_f32_e32 v42, 0x4f800000, v27
	v_cmp_gt_f32_e32 vcc, s84, v27
	ds_write2st64_b32 v22, v34, v33 offset0:2 offset1:66
	s_nop 0
	v_cndmask_b32_e32 v27, v27, v42, vcc
	v_pk_mul_f32 v[42:43], v[18:19], v[10:11]
	v_sqrt_f32_e32 v46, v27
	v_pk_fma_f32 v[42:43], v[16:17], v[48:49], v[42:43]
	v_add_u32_e32 v48, -1, v46
	v_pk_fma_f32 v[42:43], v[36:37], v[8:9], v[42:43]
	s_nop 0
	v_mul_f32_e32 v44, 0xbfb8aa3b, v43
	v_exp_f32_e32 v44, v44
	v_mul_f32_e32 v45, 0xbfb8aa3b, v42
	v_exp_f32_e32 v47, v45
	v_add_f32_e32 v44, 1.0, v44
	v_rcp_f32_e32 v45, v44
	v_add_f32_e32 v44, 1.0, v47
	v_rcp_f32_e32 v44, v44
	v_fma_f32 v47, -v48, v46, v27
	v_cmp_ge_f32_e64 s[2:3], 0, v47
	v_pk_mul_f32 v[42:43], v[42:43], v[44:45]
	s_nop 0
	v_pk_mul_f32 v[44:45], v[42:43], v[42:43]
	v_cndmask_b32_e64 v47, v46, v48, s[2:3]
	v_add_f32_e32 v44, v44, v45
	ds_swizzle_b32 v45, v44 offset:swizzle(SWAP,1)
	v_add_u32_e32 v48, 1, v46
	v_fma_f32 v46, -v48, v46, v27
	v_cmp_lt_f32_e64 s[2:3], 0, v46
	s_waitcnt lgkmcnt(0)
	v_add_f32_e32 v44, v44, v45
	ds_swizzle_b32 v45, v44 offset:swizzle(SWAP,2)
	v_cndmask_b32_e64 v46, v47, v48, s[2:3]
	v_mul_f32_e32 v47, 0x37800000, v46
	v_cndmask_b32_e32 v46, v46, v47, vcc
	v_cmp_class_f32_e32 vcc, v27, v108
	s_waitcnt lgkmcnt(0)
	v_add_f32_e32 v44, v44, v45
	ds_swizzle_b32 v45, v44 offset:swizzle(SWAP,4)
	v_cndmask_b32_e32 v27, v46, v27, vcc
	v_div_scale_f32 v46, s[2:3], v27, v27, 1.0
	v_rcp_f32_e32 v47, v46
	s_waitcnt lgkmcnt(0)
	v_add_f32_e32 v33, v44, v45
	ds_swizzle_b32 v34, v33 offset:swizzle(SWAP,8)
	v_fma_f32 v44, -v46, v47, 1.0
	v_fmac_f32_e32 v47, v44, v47
	v_div_scale_f32 v44, vcc, 1.0, v27, 1.0
	s_waitcnt lgkmcnt(0)
	v_add_f32_e32 v33, v33, v34
	ds_swizzle_b32 v34, v33 offset:swizzle(SWAP,16)
	v_mul_f32_e32 v45, v44, v47
	v_fma_f32 v48, -v46, v45, v44
	v_fmac_f32_e32 v45, v48, v47
	v_fma_f32 v44, -v46, v45, v44
	s_waitcnt lgkmcnt(0)
	v_add_f32_e32 v33, v33, v34
	v_mov_b32_e32 v34, v33
	s_nop 1
	v_permlane32_swap_b32_e32 v33, v34
	v_add_f32_e32 v33, v33, v34
	v_add_f32_e32 v33, 0x358637bd, v33
	v_mul_f32_e32 v34, 0x4f800000, v33
	v_cmp_gt_f32_e64 s[2:3], s84, v33
	s_nop 1
	v_cndmask_b32_e64 v33, v33, v34, s[2:3]
	v_div_fmas_f32 v34, v44, v47, v45
	v_pk_mul_f32 v[44:45], v[18:19], v[8:9]
	v_div_fixup_f32 v34, v34, v27, 1.0
	v_pk_fma_f32 v[10:11], v[16:17], v[10:11], v[44:45]
	v_pk_mul_f32 v[40:41], v[40:41], v[34:35] op_sel_hi:[1,0]
	v_pk_fma_f32 v[10:11], v[36:37], v[2:3], v[10:11]
	v_sqrt_f32_e32 v46, v33
	v_mul_f32_e32 v34, 0xbfb8aa3b, v11
	v_exp_f32_e32 v34, v34
	v_mul_f32_e32 v44, 0xbfb8aa3b, v10
	v_exp_f32_e32 v44, v44
	v_add_u32_e32 v27, -1, v46
	v_add_f32_e32 v34, 1.0, v34
	v_rcp_f32_e32 v45, v34
	v_add_f32_e32 v34, 1.0, v44
	v_rcp_f32_e32 v44, v34
	v_fma_f32 v47, -v27, v46, v33
	v_cmp_ge_f32_e32 vcc, 0, v47
	v_add_u32_e32 v34, 1, v46
	v_pk_mul_f32 v[10:11], v[10:11], v[44:45]
	v_cndmask_b32_e32 v27, v46, v27, vcc
	v_pk_mul_f32 v[44:45], v[10:11], v[10:11]
	v_fma_f32 v46, -v34, v46, v33
	v_add_f32_e32 v44, v44, v45
	ds_swizzle_b32 v45, v44 offset:swizzle(SWAP,1)
	v_cmp_lt_f32_e32 vcc, 0, v46
	v_cvt_pk_bf16_f32 v40, v40, v41
	ds_write2st64_b32 v23, v40, v25 offset0:3 offset1:67
	v_cndmask_b32_e32 v27, v27, v34, vcc
	v_mul_f32_e32 v34, 0x37800000, v27
	v_cndmask_b32_e64 v27, v27, v34, s[2:3]
	s_waitcnt lgkmcnt(1)
	v_add_f32_e32 v34, v44, v45
	ds_swizzle_b32 v44, v34 offset:swizzle(SWAP,2)
	v_cmp_class_f32_e32 vcc, v33, v108
	s_waitcnt lgkmcnt(0)
	v_add_f32_e32 v34, v34, v44
	v_cndmask_b32_e32 v27, v27, v33, vcc
	v_div_scale_f32 v33, s[2:3], v27, v27, 1.0
	v_rcp_f32_e32 v45, v33
	ds_swizzle_b32 v44, v34 offset:swizzle(SWAP,4)
	v_div_scale_f32 v40, vcc, 1.0, v27, 1.0
	v_fma_f32 v25, -v33, v45, 1.0
	v_fmac_f32_e32 v45, v25, v45
	s_waitcnt lgkmcnt(0)
	v_add_f32_e32 v25, v34, v44
	ds_swizzle_b32 v34, v25 offset:swizzle(SWAP,8)
	v_mul_f32_e32 v41, v40, v45
	v_fma_f32 v44, -v33, v41, v40
	v_fmac_f32_e32 v41, v44, v45
	v_fma_f32 v33, -v33, v41, v40
	s_waitcnt lgkmcnt(0)
	v_add_f32_e32 v25, v25, v34
	ds_swizzle_b32 v34, v25 offset:swizzle(SWAP,16)
	v_div_fmas_f32 v33, v33, v45, v41
	s_waitcnt lgkmcnt(0)
	v_add_f32_e32 v25, v25, v34
	v_mov_b32_e32 v34, v25
	s_nop 1
	v_permlane32_swap_b32_e32 v25, v34
	v_add_f32_e32 v25, v25, v34
	v_add_f32_e32 v25, 0x358637bd, v25
	v_mul_f32_e32 v34, 0x4f800000, v25
	v_cmp_gt_f32_e32 vcc, s84, v25
	s_nop 1
	v_cndmask_b32_e32 v25, v25, v34, vcc
	v_sqrt_f32_e32 v44, v25
	v_div_fixup_f32 v34, v33, v27, 1.0
	v_pk_mul_f32 v[40:41], v[42:43], v[34:35] op_sel_hi:[1,0]
	v_and_b32_e32 v43, 0xffff0000, v91
	v_cvt_pk_bf16_f32 v27, v40, v41
	v_pk_mul_f32 v[40:41], v[18:19], v[2:3]
	v_add_u32_e32 v33, -1, v44
	v_pk_fma_f32 v[8:9], v[16:17], v[8:9], v[40:41]
	v_fma_f32 v34, -v33, v44, v25
	v_pk_fma_f32 v[8:9], v[36:37], v[6:7], v[8:9]
	v_cmp_ge_f32_e64 s[2:3], 0, v34
	v_mul_f32_e32 v34, 0xbfb8aa3b, v9
	v_exp_f32_e32 v34, v34
	v_mul_f32_e32 v40, 0xbfb8aa3b, v8
	v_exp_f32_e32 v40, v40
	v_add_u32_e32 v42, 1, v44
	v_add_f32_e32 v34, 1.0, v34
	v_rcp_f32_e32 v41, v34
	v_add_f32_e32 v34, 1.0, v40
	v_rcp_f32_e32 v40, v34
	v_fma_f32 v34, -v42, v44, v25
	v_cndmask_b32_e64 v33, v44, v33, s[2:3]
	v_cmp_lt_f32_e64 s[2:3], 0, v34
	v_pk_mul_f32 v[8:9], v[8:9], v[40:41]
	ds_write2st64_b32 v20, v27, v21 offset1:64
	v_pk_mul_f32 v[40:41], v[8:9], v[8:9]
	v_cndmask_b32_e64 v33, v33, v42, s[2:3]
	v_add_f32_e32 v34, v40, v41
	ds_swizzle_b32 v40, v34 offset:swizzle(SWAP,1)
	v_mul_f32_e32 v41, 0x37800000, v33
	v_cndmask_b32_e32 v33, v33, v41, vcc
	v_cmp_class_f32_e32 vcc, v25, v108
	v_pk_mul_f32 v[6:7], v[18:19], v[6:7]
	v_lshlrev_b32_e32 v18, 16, v97
	v_cndmask_b32_e32 v25, v33, v25, vcc
	s_waitcnt lgkmcnt(0)
	v_add_f32_e32 v33, v34, v40
	ds_swizzle_b32 v34, v33 offset:swizzle(SWAP,2)
	v_div_scale_f32 v40, s[2:3], v25, v25, 1.0
	v_rcp_f32_e32 v41, v40
	v_pk_fma_f32 v[2:3], v[16:17], v[2:3], v[6:7]
	s_waitcnt lgkmcnt(0)
	v_add_f32_e32 v21, v33, v34
	ds_swizzle_b32 v27, v21 offset:swizzle(SWAP,4)
	v_fma_f32 v33, -v40, v41, 1.0
	v_fmac_f32_e32 v41, v33, v41
	v_div_scale_f32 v33, vcc, 1.0, v25, 1.0
	s_waitcnt lgkmcnt(0)
	v_add_f32_e32 v21, v21, v27
	ds_swizzle_b32 v27, v21 offset:swizzle(SWAP,8)
	v_mul_f32_e32 v34, v33, v41
	v_fma_f32 v42, -v40, v34, v33
	v_fmac_f32_e32 v34, v42, v41
	v_fma_f32 v33, -v40, v34, v33
	s_waitcnt lgkmcnt(0)
	v_add_f32_e32 v21, v21, v27
	ds_swizzle_b32 v27, v21 offset:swizzle(SWAP,16)
	v_div_fmas_f32 v33, v33, v41, v34
	v_div_fixup_f32 v34, v33, v25, 1.0
	v_pk_mul_f32 v[10:11], v[10:11], v[34:35] op_sel_hi:[1,0]
	v_pk_fma_f32 v[2:3], v[36:37], v[4:5], v[2:3]
	v_cvt_pk_bf16_f32 v10, v10, v11
	s_waitcnt lgkmcnt(0)
	v_add_f32_e32 v11, v21, v27
	v_mov_b32_e32 v21, v11
	s_nop 1
	v_permlane32_swap_b32_e32 v11, v21
	v_add_f32_e32 v11, v11, v21
	v_add_f32_e32 v11, 0x358637bd, v11
	v_mul_f32_e32 v21, 0x4f800000, v11
	v_cmp_gt_f32_e32 vcc, s84, v11
	v_mul_f32_e32 v4, 0xbfb8aa3b, v3
	v_exp_f32_e32 v4, v4
	v_cndmask_b32_e32 v11, v11, v21, vcc
	v_sqrt_f32_e32 v21, v11
	v_mul_f32_e32 v5, 0xbfb8aa3b, v2
	v_exp_f32_e32 v6, v5
	v_add_f32_e32 v4, 1.0, v4
	v_add_u32_e32 v7, -1, v21
	v_rcp_f32_e32 v5, v4
	v_add_f32_e32 v4, 1.0, v6
	v_fma_f32 v6, -v7, v21, v11
	v_cmp_ge_f32_e64 s[2:3], 0, v6
	v_rcp_f32_e32 v4, v4
	ds_write2st64_b32 v12, v10, v15 offset1:64
	v_cndmask_b32_e64 v6, v21, v7, s[2:3]
	v_add_u32_e32 v7, 1, v21
	v_fma_f32 v16, -v7, v21, v11
	v_cmp_lt_f32_e64 s[2:3], 0, v16
	v_pk_mul_f32 v[2:3], v[2:3], v[4:5]
	v_lshlrev_b32_e32 v36, 16, v89
	v_cndmask_b32_e64 v6, v6, v7, s[2:3]
	v_mul_f32_e32 v7, 0x37800000, v6
	v_cndmask_b32_e32 v6, v6, v7, vcc
	v_cmp_class_f32_e32 vcc, v11, v108
	v_pk_mul_f32 v[4:5], v[2:3], v[2:3]
	v_and_b32_e32 v37, 0xffff0000, v89
	v_cndmask_b32_e32 v6, v6, v11, vcc
	v_add_co_u32_e32 v0, vcc, s74, v0
	v_add_f32_e32 v4, v4, v5
	s_nop 0
	v_addc_co_u32_e32 v1, vcc, 0, v1, vcc
	global_load_dwordx2 v[0:1], v[0:1], off offset:2048
	ds_swizzle_b32 v5, v4 offset:swizzle(SWAP,1)
	v_div_scale_f32 v7, s[2:3], v6, v6, 1.0
	v_rcp_f32_e32 v11, v7
	v_lshlrev_b32_e32 v34, 16, v88
	s_waitcnt lgkmcnt(0)
	v_add_f32_e32 v4, v4, v5
	ds_swizzle_b32 v5, v4 offset:swizzle(SWAP,2)
	v_fma_f32 v10, -v7, v11, 1.0
	v_fmac_f32_e32 v11, v10, v11
	v_div_scale_f32 v10, vcc, 1.0, v6, 1.0
	s_waitcnt lgkmcnt(0)
	v_add_f32_e32 v4, v4, v5
	ds_swizzle_b32 v5, v4 offset:swizzle(SWAP,4)
	v_mul_f32_e32 v15, v10, v11
	v_fma_f32 v16, -v7, v15, v10
	v_fmac_f32_e32 v15, v16, v11
	v_fma_f32 v7, -v7, v15, v10
	s_waitcnt lgkmcnt(0)
	v_add_f32_e32 v4, v4, v5
	ds_swizzle_b32 v5, v4 offset:swizzle(SWAP,8)
	s_waitcnt vmcnt(1)
	v_pk_mul_f32 v[40:41], v[30:31], v[36:37]
	v_lshlrev_b32_e32 v42, 16, v91
	v_lshlrev_b32_e32 v16, 16, v96
	v_and_b32_e32 v17, 0xffff0000, v96
	s_waitcnt lgkmcnt(0)
	v_add_f32_e32 v4, v4, v5
	ds_swizzle_b32 v5, v4 offset:swizzle(SWAP,16)
	s_waitcnt lgkmcnt(0)
	v_add_f32_e32 v4, v4, v5
	v_mov_b32_e32 v5, v4
	s_nop 1
	v_permlane32_swap_b32_e32 v4, v5
	v_add_f32_e32 v4, v4, v5
	v_add_f32_e32 v4, 0x358637bd, v4
	v_mul_f32_e32 v5, 0x4f800000, v4
	v_cmp_gt_f32_e64 s[2:3], s84, v4
	s_nop 1
	v_cndmask_b32_e64 v5, v4, v5, s[2:3]
	v_sqrt_f32_e32 v10, v5
	v_div_fmas_f32 v4, v7, v11, v15
	v_div_fixup_f32 v4, v4, v6, 1.0
	v_and_b32_e32 v11, 0xffff0000, v95
	v_add_u32_e32 v6, -1, v10
	v_fma_f32 v7, -v6, v10, v5
	v_cmp_ge_f32_e32 vcc, 0, v7
	v_add_u32_e32 v7, 1, v10
	s_nop 0
	v_cndmask_b32_e32 v6, v10, v6, vcc
	v_fma_f32 v10, -v7, v10, v5
	v_cmp_lt_f32_e32 vcc, 0, v10
	s_nop 1
	v_cndmask_b32_e32 v6, v6, v7, vcc
	v_mul_f32_e32 v7, 0x37800000, v6
	v_cndmask_b32_e64 v6, v6, v7, s[2:3]
	v_cmp_class_f32_e32 vcc, v5, v108
	s_nop 1
	v_cndmask_b32_e32 v6, v6, v5, vcc
	v_div_scale_f32 v7, s[2:3], v6, v6, 1.0
	v_rcp_f32_e32 v10, v7
	v_pk_mul_f32 v[4:5], v[8:9], v[4:5] op_sel_hi:[1,0]
	v_and_b32_e32 v9, 0xffff0000, v94
	v_cvt_pk_bf16_f32 v4, v4, v5
	ds_write2st64_b32 v13, v4, v35 offset1:64
	v_fma_f32 v4, -v7, v10, 1.0
	v_fmac_f32_e32 v10, v4, v10
	v_div_scale_f32 v4, vcc, 1.0, v6, 1.0
	v_mul_f32_e32 v5, v4, v10
	v_fma_f32 v8, -v7, v5, v4
	v_fmac_f32_e32 v5, v8, v10
	v_fma_f32 v4, -v7, v5, v4
	v_div_fmas_f32 v4, v4, v10, v5
	v_div_fixup_f32 v4, v4, v6, 1.0
	v_pk_mul_f32 v[2:3], v[2:3], v[4:5] op_sel_hi:[1,0]
	v_and_b32_e32 v35, 0xffff0000, v88
	v_cvt_pk_bf16_f32 v2, v2, v3
	ds_write2st64_b32 v14, v2, v52 offset1:64
	v_lshlrev_b32_e32 v2, 16, v90
	v_and_b32_e32 v3, 0xffff0000, v90
	v_pk_fma_f32 v[34:35], v[28:29], v[34:35], v[40:41]
	v_pk_mul_f32 v[44:45], v[30:31], v[2:3]
	s_waitcnt vmcnt(0)
	v_pk_fma_f32 v[34:35], v[0:1], v[2:3], v[34:35]
	v_pk_fma_f32 v[36:37], v[28:29], v[36:37], v[44:45]
	v_mul_f32_e32 v15, 0xbfb8aa3b, v34
	v_exp_f32_e32 v15, v15
	v_mul_f32_e32 v19, 0xbfb8aa3b, v35
	v_exp_f32_e32 v21, v19
	v_pk_fma_f32 v[36:37], v[0:1], v[42:43], v[36:37]
	v_add_f32_e32 v15, 1.0, v15
	v_rcp_f32_e32 v40, v15
	v_add_f32_e32 v15, 1.0, v21
	v_mul_f32_e32 v21, 0xbfb8aa3b, v36
	v_exp_f32_e32 v21, v21
	v_mul_f32_e32 v25, 0xbfb8aa3b, v37
	v_exp_f32_e32 v25, v25
	v_rcp_f32_e32 v41, v15
	v_add_f32_e32 v15, 1.0, v21
	v_rcp_f32_e32 v44, v15
	v_add_f32_e32 v15, 1.0, v25
	v_rcp_f32_e32 v45, v15
	v_pk_mul_f32 v[34:35], v[34:35], v[40:41]
	v_lshlrev_b32_e32 v4, 16, v92
	v_cvt_pk_bf16_f32 v15, v34, v35
	ds_write_b32 v26, v15 offset:32768
	v_pk_mul_f32 v[26:27], v[36:37], v[44:45]
	v_and_b32_e32 v5, 0xffff0000, v92
	v_cvt_pk_bf16_f32 v15, v26, v27
	v_pk_mul_f32 v[26:27], v[30:31], v[42:43]
	v_lshlrev_b32_e32 v6, 16, v93
	v_pk_fma_f32 v[2:3], v[28:29], v[2:3], v[26:27]
	v_pk_mul_f32 v[26:27], v[30:31], v[4:5]
	v_pk_fma_f32 v[2:3], v[0:1], v[4:5], v[2:3]
	v_and_b32_e32 v7, 0xffff0000, v93
	v_mul_f32_e32 v21, 0xbfb8aa3b, v2
	v_exp_f32_e32 v21, v21
	v_mul_f32_e32 v25, 0xbfb8aa3b, v3
	v_exp_f32_e32 v25, v25
	v_pk_fma_f32 v[26:27], v[28:29], v[42:43], v[26:27]
	ds_write_b32 v24, v15 offset:33024
	v_pk_fma_f32 v[26:27], v[0:1], v[6:7], v[26:27]
	v_add_f32_e32 v15, 1.0, v21
	v_mul_f32_e32 v21, 0xbfb8aa3b, v26
	v_rcp_f32_e32 v24, v15
	v_add_f32_e32 v15, 1.0, v25
	v_exp_f32_e32 v21, v21
	v_mul_f32_e32 v25, 0xbfb8aa3b, v27
	v_exp_f32_e32 v33, v25
	v_rcp_f32_e32 v25, v15
	v_add_f32_e32 v15, 1.0, v21
	v_rcp_f32_e32 v34, v15
	v_add_f32_e32 v15, 1.0, v33
	v_rcp_f32_e32 v35, v15
	v_pk_mul_f32 v[2:3], v[2:3], v[24:25]
	v_lshlrev_b32_e32 v8, 16, v94
	v_cvt_pk_bf16_f32 v2, v2, v3
	ds_write_b32 v22, v2 offset:33280
	v_pk_mul_f32 v[2:3], v[26:27], v[34:35]
	v_lshlrev_b32_e32 v10, 16, v95
	v_cvt_pk_bf16_f32 v15, v2, v3
	v_pk_mul_f32 v[2:3], v[30:31], v[6:7]
	ds_write_b32 v23, v15 offset:33536
	v_pk_fma_f32 v[2:3], v[28:29], v[4:5], v[2:3]
	v_pk_mul_f32 v[22:23], v[30:31], v[8:9]
	v_pk_fma_f32 v[2:3], v[0:1], v[8:9], v[2:3]
	v_pk_fma_f32 v[6:7], v[28:29], v[6:7], v[22:23]
	v_mul_f32_e32 v4, 0xbfb8aa3b, v2
	v_mul_f32_e32 v5, 0xbfb8aa3b, v3
	v_pk_fma_f32 v[6:7], v[0:1], v[10:11], v[6:7]
	v_exp_f32_e32 v4, v4
	v_exp_f32_e32 v5, v5
	v_mul_f32_e32 v15, 0xbfb8aa3b, v6
	v_exp_f32_e32 v15, v15
	v_mul_f32_e32 v21, 0xbfb8aa3b, v7
	v_exp_f32_e32 v21, v21
	v_add_f32_e32 v4, 1.0, v4
	v_add_f32_e32 v5, 1.0, v5
	v_rcp_f32_e32 v4, v4
	v_rcp_f32_e32 v5, v5
	v_add_f32_e32 v15, 1.0, v15
	v_rcp_f32_e32 v22, v15
	v_add_f32_e32 v15, 1.0, v21
	v_rcp_f32_e32 v23, v15
	v_pk_mul_f32 v[2:3], v[2:3], v[4:5]
	v_and_b32_e32 v19, 0xffff0000, v97
	v_cvt_pk_bf16_f32 v2, v2, v3
	ds_write_b32 v20, v2 offset:32768
	v_pk_mul_f32 v[2:3], v[6:7], v[22:23]
	s_nop 0
	v_cvt_pk_bf16_f32 v4, v2, v3
	v_pk_mul_f32 v[2:3], v[30:31], v[10:11]
	ds_write_b32 v12, v4 offset:32768
	v_pk_fma_f32 v[2:3], v[28:29], v[8:9], v[2:3]
	s_nop 0
	v_pk_fma_f32 v[2:3], v[0:1], v[16:17], v[2:3]
	s_nop 0
	v_mul_f32_e32 v5, 0xbfb8aa3b, v2
	v_mul_f32_e32 v6, 0xbfb8aa3b, v3
	v_exp_f32_e32 v5, v5
	v_exp_f32_e32 v6, v6
	v_add_f32_e32 v4, 1.0, v5
	v_add_f32_e32 v5, 1.0, v6
	v_pk_mul_f32 v[6:7], v[30:31], v[16:17]
	v_rcp_f32_e32 v4, v4
	v_pk_fma_f32 v[6:7], v[28:29], v[10:11], v[6:7]
	v_rcp_f32_e32 v5, v5
	v_pk_fma_f32 v[0:1], v[0:1], v[18:19], v[6:7]
	v_pk_mul_f32 v[2:3], v[2:3], v[4:5]
	v_mul_f32_e32 v6, 0xbfb8aa3b, v0
	v_mul_f32_e32 v7, 0xbfb8aa3b, v1
	v_exp_f32_e32 v6, v6
	v_exp_f32_e32 v7, v7
	v_cvt_pk_bf16_f32 v2, v2, v3
	ds_write_b32 v13, v2 offset:32768
	v_add_f32_e32 v6, 1.0, v6
	v_add_f32_e32 v7, 1.0, v7
	v_rcp_f32_e32 v6, v6
	v_rcp_f32_e32 v7, v7
	s_nop 0
	v_pk_mul_f32 v[0:1], v[0:1], v[6:7]
	s_nop 0
	v_cvt_pk_bf16_f32 v0, v0, v1
	ds_write_b32 v14, v0 offset:32768
	s_cbranch_scc1 .LBB0_252
	s_add_i32 s11, s8, s96
	s_cmpk_lt_u32 s11, 0x1000
	s_cselect_b64 s[2:3], -1, 0
	s_and_b64 s[2:3], s[2:3], exec
	s_cselect_b32 s12, s4, s8
	s_cselect_b32 s13, s5, s8
	s_cselect_b32 s14, s9, s8
	s_cselect_b32 s15, s10, s8
	s_or_b32 s4, s8, 3
	s_cmpk_lt_u32 s11, 0x1000
	s_cselect_b64 s[2:3], -1, 0
	s_and_b64 s[2:3], s[2:3], exec
	s_cselect_b32 s16, s4, s8
	s_or_b32 s4, s8, 2
	s_cmpk_lt_u32 s11, 0x1000
	s_cselect_b64 vcc, -1, 0
	s_and_b64 s[2:3], vcc, exec
	s_cselect_b32 s17, s4, s8
	s_lshl_b32 s9, s21, 7
	s_add_i32 s2, s9, 0xf00
	s_add_i32 s10, s8, -1
	v_or_b32_e32 v0, s2, v39
	s_add_i32 s2, s10, s96
	s_cmpk_lt_u32 s2, 0x1000
	s_cselect_b64 s[2:3], -1, 0
	v_lshlrev_b32_e32 v64, 1, v0
	s_and_b64 s[4:5], s[2:3], exec
	v_cndmask_b32_e64 v6, 0, 1, vcc
	v_lshl_add_u64 v[0:1], s[52:53], 0, v[64:65]
	s_cselect_b32 s22, s10, s8
	v_mad_i64_i32 v[2:3], s[4:5], s22, v121, v[0:1]
	v_or_b32_e32 v18, s8, v6
	v_mad_i64_i32 v[4:5], s[4:5], s8, v121, v[0:1]
	v_mad_i64_i32 v[6:7], s[4:5], v18, s73, v[0:1]
	v_mad_i64_i32 v[8:9], s[4:5], s17, v121, v[0:1]
	v_mad_i64_i32 v[10:11], s[4:5], s16, v121, v[0:1]
	v_mad_i64_i32 v[12:13], s[4:5], s12, v121, v[0:1]
	v_mad_i64_i32 v[14:15], s[4:5], s13, v121, v[0:1]
	v_mad_i64_i32 v[16:17], s[4:5], s14, v121, v[0:1]
	global_load_dword v19, v[2:3], off nt
	global_load_dword v20, v[4:5], off nt
	global_load_dword v21, v[6:7], off nt
	global_load_dword v22, v[8:9], off nt
	global_load_dword v23, v[10:11], off nt
	global_load_dword v24, v[12:13], off nt
	global_load_dword v25, v[14:15], off nt
	global_load_dword v26, v[16:17], off nt
	v_mad_i64_i32 v[2:3], s[4:5], s15, v121, v[0:1]
	s_add_i32 s23, s8, 8
	s_add_i32 s4, s23, s96
	s_cmpk_lt_u32 s4, 0x1000
	s_cselect_b64 s[4:5], -1, 0
	s_and_b64 s[10:11], s[4:5], exec
	s_cselect_b32 s23, s23, s8
	v_mad_i64_i32 v[0:1], s[10:11], s23, v121, v[0:1]
	s_add_i32 s10, s9, 0x1200
	s_nop 0
	v_or_b32_e32 v4, s10, v39
	v_lshlrev_b32_e32 v64, 1, v4
	v_lshl_add_u64 v[4:5], s[52:53], 0, v[64:65]
	v_mad_i64_i32 v[8:9], s[10:11], s8, v121, v[4:5]
	s_addk_i32 s9, 0x1500
	v_mad_i64_i32 v[6:7], s[10:11], s22, v121, v[4:5]
	v_mad_i64_i32 v[10:11], s[10:11], v18, s73, v[4:5]
	v_mad_i64_i32 v[12:13], s[10:11], s17, v121, v[4:5]
	v_mad_i64_i32 v[14:15], s[10:11], s16, v121, v[4:5]
	v_mad_i64_i32 v[16:17], s[10:11], s12, v121, v[4:5]
	global_load_dword v27, v[2:3], off nt
	global_load_dword v28, v[0:1], off nt
	global_load_dword v29, v[6:7], off nt
	global_load_dword v30, v[8:9], off nt
	global_load_dword v31, v[10:11], off nt
	global_load_dword v33, v[12:13], off nt
	global_load_dword v34, v[14:15], off nt
	global_load_dword v35, v[16:17], off nt
	v_or_b32_e32 v8, s9, v39
	v_lshlrev_b32_e32 v64, 1, v8
	v_lshl_add_u64 v[8:9], s[52:53], 0, v[64:65]
	v_mad_i64_i32 v[0:1], s[10:11], s13, v121, v[4:5]
	v_mad_i64_i32 v[2:3], s[10:11], s14, v121, v[4:5]
	v_mad_i64_i32 v[6:7], s[10:11], s15, v121, v[4:5]
	v_mad_i64_i32 v[4:5], s[10:11], s23, v121, v[4:5]
	v_mad_i64_i32 v[12:13], s[8:9], s8, v121, v[8:9]
	v_mad_i64_i32 v[14:15], s[8:9], v18, s73, v[8:9]
	v_mad_i64_i32 v[10:11], s[10:11], s22, v121, v[8:9]
	v_mad_i64_i32 v[16:17], s[8:9], s17, v121, v[8:9]
	global_load_dword v18, v[0:1], off nt
	global_load_dword v36, v[2:3], off nt
	global_load_dword v37, v[6:7], off nt
	global_load_dword v39, v[4:5], off nt
	global_load_dword v40, v[10:11], off nt
	s_nop 0
	global_load_dword v12, v[12:13], off nt
	s_nop 0
	global_load_dword v13, v[14:15], off nt
	s_nop 0
	global_load_dword v14, v[16:17], off nt
	v_mad_i64_i32 v[0:1], s[8:9], s16, v121, v[8:9]
	v_mad_i64_i32 v[2:3], s[8:9], s12, v121, v[8:9]
	v_mad_i64_i32 v[4:5], s[8:9], s13, v121, v[8:9]
	v_mad_i64_i32 v[6:7], s[8:9], s14, v121, v[8:9]
	v_mad_i64_i32 v[10:11], s[8:9], s15, v121, v[8:9]
	v_mad_i64_i32 v[8:9], s[8:9], s23, v121, v[8:9]
	global_load_dword v0, v[0:1], off nt
	s_nop 0
	global_load_dword v1, v[2:3], off nt
	s_nop 0
	global_load_dword v2, v[4:5], off nt
	global_load_dword v3, v[6:7], off nt
	s_nop 0
	global_load_dword v4, v[10:11], off nt
	global_load_dword v5, v[8:9], off nt
	s_waitcnt vmcnt(29)
	v_cndmask_b32_e64 v68, 0, v19, s[2:3]
	s_waitcnt vmcnt(28)
	v_cndmask_b32_e32 v69, 0, v20, vcc
	s_waitcnt vmcnt(27)
	v_cndmask_b32_e32 v70, 0, v21, vcc
	s_waitcnt vmcnt(26)
	v_cndmask_b32_e32 v71, 0, v22, vcc
	s_waitcnt vmcnt(25)
	v_cndmask_b32_e32 v72, 0, v23, vcc
	s_waitcnt vmcnt(24)
	v_cndmask_b32_e32 v73, 0, v24, vcc
	s_waitcnt vmcnt(23)
	v_cndmask_b32_e32 v74, 0, v25, vcc
	s_waitcnt vmcnt(22)
	v_cndmask_b32_e32 v75, 0, v26, vcc
	s_waitcnt vmcnt(21)
	v_cndmask_b32_e32 v76, 0, v27, vcc
	s_waitcnt vmcnt(20)
	v_cndmask_b32_e64 v77, 0, v28, s[4:5]
	s_waitcnt vmcnt(19)
	v_cndmask_b32_e64 v78, 0, v29, s[2:3]
	s_waitcnt vmcnt(18)
	v_cndmask_b32_e32 v79, 0, v30, vcc
	s_waitcnt vmcnt(17)
	v_cndmask_b32_e32 v80, 0, v31, vcc
	s_waitcnt vmcnt(16)
	v_cndmask_b32_e32 v81, 0, v33, vcc
	s_waitcnt vmcnt(15)
	v_cndmask_b32_e32 v82, 0, v34, vcc
	s_waitcnt vmcnt(14)
	v_cndmask_b32_e32 v83, 0, v35, vcc
	s_waitcnt vmcnt(13)
	v_cndmask_b32_e32 v84, 0, v18, vcc
	s_waitcnt vmcnt(12)
	v_cndmask_b32_e32 v85, 0, v36, vcc
	s_waitcnt vmcnt(11)
	v_cndmask_b32_e32 v86, 0, v37, vcc
	s_waitcnt vmcnt(10)
	v_cndmask_b32_e64 v87, 0, v39, s[4:5]
	s_waitcnt vmcnt(9)
	v_cndmask_b32_e64 v88, 0, v40, s[2:3]
	s_waitcnt vmcnt(8)
	v_cndmask_b32_e32 v89, 0, v12, vcc
	s_waitcnt vmcnt(7)
	v_cndmask_b32_e32 v90, 0, v13, vcc
	s_waitcnt vmcnt(6)
	v_cndmask_b32_e32 v91, 0, v14, vcc
	s_waitcnt vmcnt(5)
	v_cndmask_b32_e32 v92, 0, v0, vcc
	s_waitcnt vmcnt(4)
	v_cndmask_b32_e32 v93, 0, v1, vcc
	s_waitcnt vmcnt(3)
	v_cndmask_b32_e32 v94, 0, v2, vcc
	s_waitcnt vmcnt(2)
	v_cndmask_b32_e32 v95, 0, v3, vcc
	s_waitcnt vmcnt(1)
	v_cndmask_b32_e32 v96, 0, v4, vcc
	s_waitcnt vmcnt(0)
	v_cndmask_b32_e64 v97, 0, v5, s[4:5]
.LBB0_252:
	s_cmp_gt_i32 s7, 1
	s_cbranch_scc1 .LBB0_256
	s_mul_i32 s2, s7, 6
	s_add_i32 s2, s2, s46
	s_add_i32 s4, s2, 12
	s_ashr_i32 s3, s2, 31
	s_ashr_i32 s5, s4, 31
	s_cmp_lt_u32 s6, 64
	s_cselect_b64 vcc, -1, 0
	s_and_b64 s[8:9], vcc, exec
	s_cselect_b32 s6, s85, 0x70
	s_cselect_b32 s12, s87, 0x80
	s_add_u32 s8, s30, s6
	s_addc_u32 s9, s31, 0
	s_load_dwordx2 s[8:9], s[8:9], 0x0
	s_lshl_b64 s[10:11], s[46:47], 2
	v_xor_b32_e32 v0, 63, v38
	v_cndmask_b32_e32 v0, v0, v38, vcc
	v_or_b32_e32 v0, s97, v0
	s_waitcnt lgkmcnt(0)
	s_add_u32 s8, s8, s10
	s_addc_u32 s9, s9, s11
	s_add_u32 s12, s30, s12
	s_addc_u32 s13, s31, 0
	s_load_dwordx2 s[12:13], s[12:13], 0x0
	v_ashrrev_i32_e32 v1, 31, v0
	v_lshlrev_b64 v[0:1], 7, v[0:1]
	v_lshl_add_u64 v[0:1], s[40:41], 0, v[0:1]
	v_lshl_add_u64 v[2:3], s[2:3], 2, v[0:1]
	s_waitcnt lgkmcnt(0)
	s_add_u32 s2, s12, s10
	v_lshl_add_u64 v[0:1], s[4:5], 2, v[0:1]
	s_addc_u32 s3, s13, s11
	global_load_dword v4, v65, s[2:3]
	global_load_dword v5, v[0:1], off nt
	s_nop 0
	global_load_dword v0, v[2:3], off nt
	global_load_dword v1, v65, s[8:9]
	s_waitcnt vmcnt(2)
	v_add_f32_e32 v2, v5, v4
	v_cmp_nlt_f32_e32 vcc, s88, v2
	s_and_saveexec_b64 s[2:3], vcc
	s_cbranch_execz .LBB0_255
	v_mul_f32_e32 v3, 0x3fb8aa3b, v2
	v_rndne_f32_e32 v4, v3
	v_sub_f32_e32 v5, v3, v4
	v_fma_f32 v3, v2, s80, -v3
	v_fmac_f32_e32 v3, 0x32a5705f, v2
	v_add_f32_e32 v3, v5, v3
	v_cvt_i32_f32_e32 v4, v4
	v_exp_f32_e32 v3, v3
	v_cmp_ngt_f32_e32 vcc, s81, v2
	v_ldexp_f32 v3, v3, v4
	s_nop 0
	v_cndmask_b32_e32 v3, 0, v3, vcc
	v_cmp_nlt_f32_e32 vcc, s79, v2
	s_nop 1
	v_cndmask_b32_e32 v16, v112, v3, vcc
	v_add_f32_e32 v4, 1.0, v16
	v_add_f32_e32 v2, -1.0, v4
	v_sub_f32_e32 v3, v2, v4
	v_add_f32_e32 v3, 1.0, v3
	v_sub_f32_e32 v2, v16, v2
	v_add_f32_e32 v5, v2, v3
	v_frexp_mant_f32_e32 v6, v4
	v_cvt_f64_f32_e32 v[2:3], v4
	v_frexp_exp_i32_f64_e32 v2, v[2:3]
	v_cmp_gt_f32_e32 vcc, s75, v6
	s_nop 1
	v_subbrev_co_u32_e32 v10, vcc, 0, v2, vcc
	v_sub_u32_e32 v2, 0, v10
	v_ldexp_f32 v3, v4, v2
	v_add_f32_e32 v4, -1.0, v3
	v_add_f32_e32 v6, 1.0, v3
	v_ldexp_f32 v2, v5, v2
	v_add_f32_e32 v5, 1.0, v4
	v_add_f32_e32 v7, -1.0, v6
	v_sub_f32_e32 v5, v3, v5
	v_sub_f32_e32 v3, v3, v7
	v_add_f32_e32 v5, v2, v5
	v_add_f32_e32 v2, v2, v3
	v_add_f32_e32 v11, v6, v2
	v_rcp_f32_e32 v13, v11
	v_sub_f32_e32 v3, v6, v11
	v_add_f32_e32 v12, v2, v3
	v_add_f32_e32 v3, v4, v5
	v_mul_f32_e32 v15, v3, v13
	v_sub_f32_e32 v2, v4, v3
	v_mul_f32_e32 v4, v11, v15
	v_fma_f32 v6, v15, v11, -v4
	v_fmac_f32_e32 v6, v15, v12
	v_add_f32_e32 v14, v5, v2
	v_add_f32_e32 v2, v4, v6
	v_sub_f32_e32 v5, v3, v2
	v_pk_add_f32 v[8:9], v[2:3], v[4:5] neg_lo:[0,1] neg_hi:[0,1]
	v_mov_b32_e32 v7, v2
	v_pk_add_f32 v[2:3], v[8:9], v[6:7] neg_lo:[0,1] neg_hi:[0,1]
	v_cmp_neq_f32_e32 vcc, s78, v16
	v_add_f32_e32 v3, v14, v3
	v_add_f32_e32 v2, v2, v3
	v_add_f32_e32 v3, v5, v2
	v_mul_f32_e32 v14, v13, v3
	v_mul_f32_e32 v4, v11, v14
	v_fma_f32 v6, v14, v11, -v4
	v_fmac_f32_e32 v6, v14, v12
	v_sub_f32_e32 v5, v5, v3
	v_add_f32_e32 v11, v2, v5
	v_add_f32_e32 v2, v4, v6
	v_sub_f32_e32 v5, v3, v2
	v_pk_add_f32 v[8:9], v[2:3], v[4:5] neg_lo:[0,1] neg_hi:[0,1]
	v_mov_b32_e32 v7, v2
	v_pk_add_f32 v[2:3], v[8:9], v[6:7] neg_lo:[0,1] neg_hi:[0,1]
	s_nop 0
	v_add_f32_e32 v3, v11, v3
	v_add_f32_e32 v2, v2, v3
	v_add_f32_e32 v3, v15, v14
	v_add_f32_e32 v2, v5, v2
	v_sub_f32_e32 v4, v3, v15
	v_mul_f32_e32 v2, v13, v2
	v_sub_f32_e32 v4, v14, v4
	v_add_f32_e32 v4, v4, v2
	v_add_f32_e32 v6, v3, v4
	v_mul_f32_e32 v7, v6, v6
	v_fmamk_f32 v2, v7, 0x3e9b6dac, v109
	v_fmaak_f32 v67, v7, v2, 0x3f2aaada
	v_cvt_f32_i32_e32 v2, v10
	v_sub_f32_e32 v3, v6, v3
	v_sub_f32_e32 v3, v4, v3
	v_ldexp_f32 v8, v3, 1
	v_mul_f32_e32 v3, v6, v7
	v_ldexp_f32 v5, v6, 1
	v_pk_mul_f32 v[6:7], v[2:3], v[66:67]
	s_nop 0
	v_fma_f32 v4, v2, s76, -v6
	v_fmac_f32_e32 v4, 0xb102e308, v2
	v_pk_add_f32 v[2:3], v[6:7], v[4:5]
	s_nop 0
	v_sub_f32_e32 v5, v3, v5
	v_sub_f32_e32 v5, v7, v5
	v_add_f32_e32 v9, v8, v5
	v_mov_b32_e32 v8, v6
	v_pk_add_f32 v[6:7], v[2:3], v[6:7] neg_lo:[0,1] neg_hi:[0,1]
	v_pk_add_f32 v[10:11], v[2:3], v[8:9]
	v_mov_b32_e32 v5, v2
	v_mov_b32_e32 v7, v11
	v_pk_add_f32 v[12:13], v[4:5], v[6:7] neg_lo:[0,1] neg_hi:[0,1]
	v_pk_add_f32 v[4:5], v[4:5], v[6:7]
	v_mov_b32_e32 v8, v9
	v_pk_add_f32 v[6:7], v[4:5], v[2:3] op_sel:[1,0] op_sel_hi:[0,1] neg_lo:[0,1] neg_hi:[0,1]
	v_pk_add_f32 v[14:15], v[10:11], v[6:7] op_sel_hi:[1,0] neg_lo:[0,1] neg_hi:[0,1]
	v_mov_b32_e32 v10, v11
	v_mov_b32_e32 v11, v5
	v_pk_mov_b32 v[6:7], v[2:3], v[6:7] op_sel:[1,0]
	v_mov_b32_e32 v9, v2
	v_pk_add_f32 v[6:7], v[10:11], v[6:7] neg_lo:[0,1] neg_hi:[0,1]
	v_mov_b32_e32 v14, v12
	v_pk_add_f32 v[2:3], v[8:9], v[6:7] neg_lo:[0,1] neg_hi:[0,1]
	v_mov_b32_e32 v13, v5
	v_pk_add_f32 v[6:7], v[14:15], v[2:3]
	s_nop 0
	v_pk_add_f32 v[8:9], v[6:7], v[6:7] op_sel:[0,1] op_sel_hi:[1,0]
	s_nop 0
	v_pk_add_f32 v[4:5], v[4:5], v[8:9] op_sel:[1,0] op_sel_hi:[0,1]
	v_mov_b32_e32 v7, v4
	v_pk_add_f32 v[10:11], v[6:7], v[12:13] neg_lo:[0,1] neg_hi:[0,1]
	v_mov_b32_e32 v3, v8
	v_sub_f32_e32 v5, v6, v10
	v_pk_add_f32 v[2:3], v[2:3], v[10:11] neg_lo:[0,1] neg_hi:[0,1]
	v_sub_f32_e32 v5, v12, v5
	v_add_f32_e32 v2, v2, v5
	v_add_f32_e32 v2, v2, v3
	v_add_f32_e32 v2, v4, v2
	v_cndmask_b32_e32 v2, v112, v2, vcc
	v_cmp_lt_f32_e64 vcc, |v16|, s89
	s_nop 1
	v_cndmask_b32_e32 v2, v2, v16, vcc

.LBB0_1575:
	v_add_u32_e32 v16, s6, v67
	v_ashrrev_i32_e32 v16, 5, v16
	v_and_b32_e32 v52, -8, v16
	v_add_u32_e32 v21, s96, v16
	v_or_b32_e32 v18, 7, v16
	v_add_u32_e32 v35, -1, v52
	v_or_b32_e32 v37, 2, v52
	v_or_b32_e32 v39, 3, v52
	v_or_b32_e32 v41, 4, v52
	v_or_b32_e32 v43, 5, v52
	v_or_b32_e32 v45, 6, v52
	v_add_u32_e32 v47, 8, v52
	v_or_b32_e32 v22, 1, v52
	v_cmp_gt_u32_e32 vcc, s74, v21
	v_mad_i64_i32 v[16:17], s[2:3], v52, s73, v[6:7]
	v_mad_i64_i32 v[18:19], s[2:3], v18, s73, v[6:7]
	v_add_u32_e32 v20, s97, v52
	v_cndmask_b32_e64 v48, 0, 1, vcc
	v_add_u32_e32 v49, s96, v35
	v_add_u32_e32 v50, s96, v47
	v_mad_i64_i32 v[22:23], s[2:3], v22, s73, v[6:7]
	v_mad_i64_i32 v[24:25], s[2:3], v37, s73, v[6:7]
	v_mad_i64_i32 v[26:27], s[2:3], v39, s73, v[6:7]
	v_mad_i64_i32 v[28:29], s[2:3], v41, s73, v[6:7]
	v_mad_i64_i32 v[30:31], s[2:3], v43, s73, v[6:7]
	v_mad_i64_i32 v[32:33], s[2:3], v45, s73, v[6:7]
	v_ashrrev_i32_e32 v21, 31, v20
	v_cndmask_b32_e32 v51, v52, v37, vcc
	v_or_b32_e32 v48, v52, v48
	v_cndmask_b32_e32 v55, v52, v43, vcc
	v_cmp_gt_u32_e64 s[4:5], s74, v49
	v_cmp_gt_u32_e64 s[2:3], s74, v50
	global_load_dwordx2 v[12:13], v[0:1], off
	global_load_dwordx2 v[14:15], v[2:3], off
	global_load_dwordx2 v[10:11], v[4:5], off
	global_load_dword v56, v[16:17], off offset:1024 nt
	global_load_dword v57, v[16:17], off offset:2048 nt
	v_or_b32_e32 v34, 1, v20
	v_or_b32_e32 v36, 2, v20
	v_or_b32_e32 v38, 3, v20
	v_or_b32_e32 v40, 4, v20
	v_or_b32_e32 v42, 5, v20
	v_or_b32_e32 v44, 6, v20
	v_or_b32_e32 v46, 7, v20
	v_cndmask_b32_e32 v53, v52, v39, vcc
	v_cndmask_b32_e32 v54, v52, v41, vcc
	v_cndmask_b32_e32 v58, v52, v45, vcc
	v_cndmask_b32_e64 v59, 0, 7, vcc
	global_load_dword v60, v[28:29], off nt
	global_load_dword v61, v[30:31], off nt
	global_load_dword v62, v[32:33], off nt
	global_load_dword v63, v[18:19], off nt
	v_cndmask_b32_e64 v64, v52, v35, s[4:5]
	v_cndmask_b32_e64 v68, v52, v47, s[2:3]
	v_lshlrev_b64 v[18:19], 12, v[20:21]
	v_mad_i64_i32 v[20:21], s[8:9], v51, s73, v[6:7]
	v_mad_i64_i32 v[28:29], s[8:9], v48, s73, v[6:7]
	v_mad_i64_i32 v[48:49], s[8:9], v55, s73, v[6:7]
	v_mad_i64_i32 v[30:31], s[8:9], v53, s73, v[6:7]
	v_mad_i64_i32 v[32:33], s[8:9], v54, s73, v[6:7]
	v_mad_i64_i32 v[50:51], s[8:9], v58, s73, v[6:7]
	v_or_b32_e32 v58, v59, v52
	v_mad_i64_i32 v[52:53], s[8:9], v64, s73, v[6:7]
	v_mad_i64_i32 v[54:55], s[8:9], v68, s73, v[6:7]
	global_load_dword v59, v[20:21], off offset:2048 nt
	global_load_dword v64, v[28:29], off offset:1024 nt
	global_load_dword v68, v[28:29], off offset:2048 nt
	global_load_dword v69, v[20:21], off offset:1024 nt
	global_load_dword v70, v[30:31], off offset:1024 nt
	global_load_dword v71, v[30:31], off offset:2048 nt
	global_load_dword v72, v[32:33], off offset:1024 nt
	global_load_dword v73, v[32:33], off offset:2048 nt
	global_load_dword v74, v[48:49], off offset:1024 nt
	s_nop 0
	global_load_dword v48, v[48:49], off offset:2048 nt
	s_nop 0
	global_load_dword v49, v[50:51], off offset:1024 nt
	v_mad_i64_i32 v[20:21], s[8:9], v58, s73, v[6:7]
	global_load_dword v50, v[50:51], off offset:2048 nt
	s_nop 0
	global_load_dword v51, v[52:53], off offset:1024 nt
	s_nop 0
	global_load_dword v52, v[52:53], off offset:2048 nt
	s_nop 0
	global_load_dword v53, v[16:17], off nt
	global_load_dword v58, v[20:21], off offset:1024 nt
	global_load_dword v75, v[20:21], off offset:2048 nt
	global_load_dword v76, v[54:55], off offset:1024 nt
	s_nop 0
	global_load_dword v54, v[54:55], off offset:2048 nt
	s_nop 0
	global_load_dword v77, v[22:23], off nt
	global_load_dword v78, v[24:25], off nt
	global_load_dword v79, v[26:27], off nt
	v_ashrrev_i32_e32 v35, 31, v34
	v_ashrrev_i32_e32 v37, 31, v36
	v_ashrrev_i32_e32 v39, 31, v38
	v_ashrrev_i32_e32 v41, 31, v40
	v_ashrrev_i32_e32 v45, 31, v44
	v_ashrrev_i32_e32 v43, 31, v42
	v_ashrrev_i32_e32 v47, 31, v46
	v_lshlrev_b64 v[34:35], 12, v[34:35]
	v_lshlrev_b64 v[36:37], 12, v[36:37]
	v_lshlrev_b64 v[38:39], 12, v[38:39]
	v_lshlrev_b64 v[40:41], 12, v[40:41]
	v_lshlrev_b64 v[44:45], 12, v[44:45]
	v_lshlrev_b64 v[42:43], 12, v[42:43]
	v_lshlrev_b64 v[46:47], 12, v[46:47]
	v_lshl_add_u64 v[16:17], v[8:9], 0, v[34:35]
	v_lshl_add_u64 v[20:21], v[8:9], 0, v[36:37]
	v_lshl_add_u64 v[22:23], v[8:9], 0, v[38:39]
	v_lshl_add_u64 v[24:25], v[8:9], 0, v[40:41]
	v_lshl_add_u64 v[28:29], v[8:9], 0, v[44:45]
	v_lshl_add_u64 v[26:27], v[8:9], 0, v[42:43]
	v_lshl_add_u64 v[30:31], v[8:9], 0, v[46:47]
	s_addk_i32 s6, 0x200
	s_cmpk_eq_i32 s6, 0x800
	v_lshl_add_u64 v[18:19], v[8:9], 0, v[18:19]
	s_waitcnt vmcnt(27)
	v_cndmask_b32_e32 v33, 0, v56, vcc
	s_waitcnt vmcnt(26)
	v_cndmask_b32_e32 v35, 0, v57, vcc
	v_lshlrev_b32_e32 v32, 16, v33
	v_lshlrev_b32_e32 v34, 16, v35
	v_and_b32_e32 v33, 0xffff0000, v33
	v_and_b32_e32 v35, 0xffff0000, v35
	v_pk_mul_f32 v[32:33], v[32:33], v[34:35]
	s_waitcnt vmcnt(25)
	v_lshlrev_b32_e32 v36, 16, v60
	v_and_b32_e32 v37, 0xffff0000, v60
	s_waitcnt vmcnt(24)
	v_lshlrev_b32_e32 v38, 16, v61
	v_and_b32_e32 v39, 0xffff0000, v61
	s_waitcnt vmcnt(23)
	v_lshlrev_b32_e32 v40, 16, v62
	v_and_b32_e32 v41, 0xffff0000, v62
	s_waitcnt vmcnt(22)
	v_lshlrev_b32_e32 v42, 16, v63
	v_and_b32_e32 v43, 0xffff0000, v63
	v_pk_mul_f32 v[34:35], v[14:15], v[32:33]
	s_waitcnt vmcnt(21)
	v_cndmask_b32_e32 v45, 0, v59, vcc
	s_waitcnt vmcnt(20)
	v_cndmask_b32_e32 v55, 0, v64, vcc
	s_waitcnt vmcnt(19)
	v_cndmask_b32_e32 v56, 0, v68, vcc
	s_waitcnt vmcnt(18)
	v_cndmask_b32_e32 v57, 0, v69, vcc
	s_waitcnt vmcnt(17)
	v_cndmask_b32_e32 v59, 0, v70, vcc
	s_waitcnt vmcnt(16)
	v_cndmask_b32_e32 v60, 0, v71, vcc
	s_waitcnt vmcnt(15)
	v_cndmask_b32_e32 v61, 0, v72, vcc
	s_waitcnt vmcnt(14)
	v_cndmask_b32_e32 v62, 0, v73, vcc
	s_waitcnt vmcnt(13)
	v_cndmask_b32_e32 v63, 0, v74, vcc
	s_waitcnt vmcnt(12)
	v_cndmask_b32_e32 v64, 0, v48, vcc
	s_waitcnt vmcnt(11)
	v_cndmask_b32_e32 v71, 0, v49, vcc
	s_waitcnt vmcnt(10)
	v_cndmask_b32_e32 v73, 0, v50, vcc
	s_waitcnt vmcnt(9)
	v_cndmask_b32_e64 v81, 0, v51, s[4:5]
	s_waitcnt vmcnt(8)
	v_cndmask_b32_e64 v83, 0, v52, s[4:5]
	v_lshlrev_b32_e32 v44, 16, v45
	v_and_b32_e32 v45, 0xffff0000, v45
	s_waitcnt vmcnt(7)
	v_lshlrev_b32_e32 v46, 16, v53
	v_and_b32_e32 v47, 0xffff0000, v53
	v_lshlrev_b32_e32 v48, 16, v55
	v_lshlrev_b32_e32 v50, 16, v56
	v_and_b32_e32 v49, 0xffff0000, v55
	v_and_b32_e32 v51, 0xffff0000, v56
	v_lshlrev_b32_e32 v52, 16, v57
	v_and_b32_e32 v53, 0xffff0000, v57
	s_waitcnt vmcnt(6)
	v_cndmask_b32_e32 v84, 0, v58, vcc
	s_waitcnt vmcnt(5)
	v_cndmask_b32_e32 v85, 0, v75, vcc
	s_waitcnt vmcnt(3)
	v_cndmask_b32_e64 v87, 0, v54, s[2:3]
	v_lshlrev_b32_e32 v54, 16, v59
	v_lshlrev_b32_e32 v56, 16, v60
	v_and_b32_e32 v55, 0xffff0000, v59
	v_and_b32_e32 v57, 0xffff0000, v60
	v_lshlrev_b32_e32 v58, 16, v61
	v_lshlrev_b32_e32 v60, 16, v62
	v_and_b32_e32 v59, 0xffff0000, v61
	v_and_b32_e32 v61, 0xffff0000, v62
	v_cndmask_b32_e64 v86, 0, v76, s[2:3]
	v_lshlrev_b32_e32 v62, 16, v63
	v_lshlrev_b32_e32 v68, 16, v64
	v_and_b32_e32 v63, 0xffff0000, v63
	v_and_b32_e32 v69, 0xffff0000, v64
	v_lshlrev_b32_e32 v70, 16, v71
	v_lshlrev_b32_e32 v72, 16, v73
	v_and_b32_e32 v71, 0xffff0000, v71
	v_and_b32_e32 v73, 0xffff0000, v73
	v_pk_mul_f32 v[44:45], v[52:53], v[44:45]
	v_pk_mul_f32 v[52:53], v[58:59], v[60:61]
	v_lshlrev_b32_e32 v58, 16, v84
	v_lshlrev_b32_e32 v60, 16, v85
	v_and_b32_e32 v59, 0xffff0000, v84
	v_and_b32_e32 v61, 0xffff0000, v85
	v_lshlrev_b32_e32 v80, 16, v81
	v_lshlrev_b32_e32 v82, 16, v83
	v_and_b32_e32 v81, 0xffff0000, v81
	v_and_b32_e32 v83, 0xffff0000, v83
	v_pk_mul_f32 v[48:49], v[48:49], v[50:51]
	v_pk_mul_f32 v[50:51], v[54:55], v[56:57]
	v_pk_mul_f32 v[54:55], v[62:63], v[68:69]
	v_pk_mul_f32 v[56:57], v[70:71], v[72:73]
	v_lshlrev_b32_e32 v62, 16, v86
	v_lshlrev_b32_e32 v68, 16, v87
	v_and_b32_e32 v63, 0xffff0000, v86
	v_and_b32_e32 v69, 0xffff0000, v87
	v_pk_mul_f32 v[58:59], v[58:59], v[60:61]
	v_pk_mul_f32 v[70:71], v[80:81], v[82:83]
	v_pk_mul_f32 v[72:73], v[14:15], v[48:49]
	v_pk_mul_f32 v[80:81], v[14:15], v[44:45]
	v_pk_mul_f32 v[60:61], v[62:63], v[68:69]
	v_pk_mul_f32 v[62:63], v[14:15], v[50:51]
	v_pk_mul_f32 v[68:69], v[14:15], v[52:53]
	v_pk_mul_f32 v[82:83], v[14:15], v[54:55]
	v_pk_mul_f32 v[84:85], v[14:15], v[56:57]
	v_pk_mul_f32 v[14:15], v[14:15], v[58:59]
	v_pk_fma_f32 v[34:35], v[12:13], v[70:71], v[34:35]
	v_pk_fma_f32 v[32:33], v[12:13], v[32:33], v[72:73]
	v_pk_fma_f32 v[70:71], v[12:13], v[48:49], v[80:81]
	v_pk_fma_f32 v[62:63], v[12:13], v[44:45], v[62:63]
	v_pk_fma_f32 v[68:69], v[12:13], v[50:51], v[68:69]
	v_pk_fma_f32 v[72:73], v[12:13], v[52:53], v[82:83]
	v_pk_fma_f32 v[80:81], v[12:13], v[54:55], v[84:85]
	v_pk_fma_f32 v[12:13], v[12:13], v[56:57], v[14:15]
	v_pk_fma_f32 v[34:35], v[10:11], v[48:49], v[34:35]
	v_pk_fma_f32 v[32:33], v[10:11], v[44:45], v[32:33]
	v_pk_fma_f32 v[44:45], v[10:11], v[50:51], v[70:71]
	v_pk_fma_f32 v[48:49], v[10:11], v[52:53], v[62:63]
	v_pk_fma_f32 v[50:51], v[10:11], v[54:55], v[68:69]
	v_pk_fma_f32 v[52:53], v[10:11], v[56:57], v[72:73]
	v_pk_fma_f32 v[54:55], v[10:11], v[58:59], v[80:81]
	v_pk_fma_f32 v[10:11], v[10:11], v[60:61], v[12:13]
	s_waitcnt vmcnt(2)
	v_lshlrev_b32_e32 v74, 16, v77
	v_and_b32_e32 v75, 0xffff0000, v77
	s_waitcnt vmcnt(1)
	v_lshlrev_b32_e32 v76, 16, v78
	v_and_b32_e32 v77, 0xffff0000, v78
	s_waitcnt vmcnt(0)
	v_lshlrev_b32_e32 v78, 16, v79
	v_and_b32_e32 v79, 0xffff0000, v79
	v_pk_mul_f32 v[14:15], v[34:35], v[46:47]
	v_pk_mul_f32 v[10:11], v[10:11], v[42:43]
	v_pk_mul_f32 v[32:33], v[32:33], v[74:75]
	v_pk_mul_f32 v[34:35], v[44:45], v[76:77]
	v_pk_mul_f32 v[44:45], v[48:49], v[78:79]
	v_pk_mul_f32 v[36:37], v[50:51], v[36:37]
	v_pk_mul_f32 v[38:39], v[52:53], v[38:39]
	v_pk_mul_f32 v[40:41], v[54:55], v[40:41]
	v_cvt_pk_bf16_f32 v12, v14, v15
	v_cvt_pk_bf16_f32 v10, v10, v11
	v_cvt_pk_bf16_f32 v13, v32, v33
	v_cvt_pk_bf16_f32 v14, v34, v35
	v_cvt_pk_bf16_f32 v15, v44, v45
	v_cvt_pk_bf16_f32 v32, v36, v37
	v_cvt_pk_bf16_f32 v33, v38, v39
	v_cvt_pk_bf16_f32 v34, v40, v41
	global_store_dword v[18:19], v12, off
	global_store_dword v[16:17], v13, off
	global_store_dword v[20:21], v14, off
	global_store_dword v[22:23], v15, off
	global_store_dword v[24:25], v32, off
	global_store_dword v[26:27], v33, off
	global_store_dword v[28:29], v34, off
	global_store_dword v[30:31], v10, off
	s_cbranch_scc0 .LBB0_1575
	v_mov_b32_e32 v123, v67
	s_load_dwordx2 s[2:3], s[34:35], 0x8
	s_load_dwordx4 s[8:11], s[34:35], 0x28
	v_ashrrev_i32_e32 v0, 3, v123
	v_add_u32_e32 v2, s97, v0
	v_ashrrev_i32_e32 v3, 31, v2
	v_and_b32_e32 v16, 7, v123
	s_waitcnt lgkmcnt(0)
	v_lshl_add_u64 v[2:3], v[2:3], 2, s[2:3]
	global_load_dword v1, v[2:3], off nt
	v_lshlrev_b32_e32 v2, 1, v16
	v_cvt_f32_ubyte0_e32 v2, v2
	v_mul_f32_e32 v17, 0xbd800000, v2
	v_cmp_eq_f32_e32 vcc, 0, v17
	v_readfirstlane_b32 s14, v123
	s_waitcnt vmcnt(0)
	v_cvt_f32_i32_e32 v1, v1
	v_cndmask_b32_e64 v12, v110, 1.0, vcc
	v_frexp_mant_f32_e32 v2, v12
	v_cmp_gt_f32_e64 s[2:3], s75, v2
	s_nop 1
	v_cndmask_b32_e64 v3, 1.0, 2.0, s[2:3]
	v_mul_f32_e32 v2, v2, v3
	v_add_f32_e32 v5, 1.0, v2
	v_rcp_f32_e32 v10, v5
	v_add_f32_e32 v3, -1.0, v5
	v_sub_f32_e32 v7, v2, v3
	v_add_f32_e32 v3, -1.0, v2
	v_mul_f32_e32 v11, v3, v10
	v_mul_f32_e32 v4, v5, v11
	v_fma_f32 v6, v11, v5, -v4
	v_fmac_f32_e32 v6, v11, v7
	v_add_f32_e32 v2, v4, v6
	v_sub_f32_e32 v5, v3, v2
	v_pk_add_f32 v[8:9], v[2:3], v[4:5] neg_lo:[0,1] neg_hi:[0,1]
	v_mov_b32_e32 v7, v2
	v_pk_add_f32 v[2:3], v[8:9], v[6:7] neg_lo:[0,1] neg_hi:[0,1]
	s_nop 0
	v_add_f32_e32 v2, v2, v3
	v_add_f32_e32 v2, v5, v2
	v_mul_f32_e32 v3, v10, v2
	v_add_f32_e32 v2, v11, v3
	v_sub_f32_e32 v4, v2, v11
	v_sub_f32_e32 v13, v3, v4
	v_mul_f32_e32 v3, v2, v2
	v_fma_f32 v5, v2, v2, -v3
	v_add_f32_e32 v4, v13, v13
	v_fmac_f32_e32 v5, v2, v4
	v_add_f32_e32 v4, v3, v5
	v_fmamk_f32 v6, v4, 0x3e76c4e1, v104
	v_fmaak_f32 v6, v4, v6, 0x3ecccdef
	v_sub_f32_e32 v3, v4, v3
	v_sub_f32_e32 v14, v5, v3
	v_mul_f32_e32 v3, v4, v6
	v_fma_f32 v5, v4, v6, -v3
	v_fmac_f32_e32 v5, v14, v6
	v_add_f32_e32 v6, v3, v5
	v_add_f32_e32 v7, 0x3f2aaaaa, v6
	v_sub_f32_e32 v3, v6, v3
	v_sub_f32_e32 v3, v5, v3
	v_add_f32_e32 v5, 0xbf2aaaaa, v7
	v_add_f32_e32 v3, 0x31739010, v3
	v_sub_f32_e32 v5, v6, v5
	v_pk_mul_f32 v[8:9], v[2:3], v[4:5]
	v_pk_add_f32 v[10:11], v[2:3], v[4:5]
	v_fma_f32 v6, v4, v2, -v8
	v_fmac_f32_e32 v6, v4, v13
	v_mov_b32_e32 v9, v11
	v_fmac_f32_e32 v6, v14, v2
	v_pk_add_f32 v[4:5], v[8:9], v[6:7]
	v_ldexp_f32 v14, v13, 1
	v_sub_f32_e32 v3, v4, v8
	v_sub_f32_e32 v3, v6, v3
	v_sub_f32_e32 v6, v7, v5
	v_add_f32_e32 v10, v11, v6
	v_pk_mul_f32 v[6:7], v[4:5], v[4:5] op_sel:[0,1] op_sel_hi:[1,0]
	v_cvt_f64_f32_e32 v[8:9], v12
	v_frexp_exp_i32_f64_e32 v7, v[8:9]
	v_subbrev_co_u32_e64 v7, s[2:3], 0, v7, s[2:3]
	v_cvt_f32_i32_e32 v7, v7
	v_fma_f32 v8, v4, v5, -v6
	v_fmac_f32_e32 v8, v4, v10
	v_fmac_f32_e32 v8, v3, v5
	v_mul_f32_e32 v4, 0x3f317218, v7
	v_fma_f32 v10, v7, s76, -v4
	v_fmac_f32_e32 v10, 0xb102e308, v7
	v_ldexp_f32 v11, v2, 1
	v_add_f32_e32 v5, v6, v8
	v_pk_add_f32 v[2:3], v[4:5], v[10:11]
	v_mov_b32_e32 v12, v5
	v_mov_b32_e32 v13, v3
	v_mov_b32_e32 v7, v11
	v_pk_add_f32 v[6:7], v[12:13], v[6:7] neg_lo:[0,1] neg_hi:[0,1]
	v_mov_b32_e32 v9, v5
	v_pk_add_f32 v[6:7], v[8:9], v[6:7] neg_lo:[0,1] neg_hi:[0,1]
	v_mov_b32_e32 v11, v2
	v_add_f32_e32 v5, v14, v6
	v_add_f32_e32 v5, v5, v7
	v_pk_add_f32 v[6:7], v[2:3], v[4:5] neg_lo:[0,1] neg_hi:[0,1]
	v_pk_add_f32 v[8:9], v[2:3], v[4:5]
	v_mov_b32_e32 v4, v5
	v_mov_b32_e32 v7, v9
	v_pk_add_f32 v[12:13], v[10:11], v[6:7] neg_lo:[0,1] neg_hi:[0,1]
	v_pk_add_f32 v[6:7], v[10:11], v[6:7]
	v_mov_b32_e32 v5, v2
	v_pk_add_f32 v[10:11], v[6:7], v[2:3] op_sel:[1,0] op_sel_hi:[0,1] neg_lo:[0,1] neg_hi:[0,1]
	v_pk_add_f32 v[14:15], v[8:9], v[10:11] op_sel_hi:[1,0] neg_lo:[0,1] neg_hi:[0,1]
	v_mov_b32_e32 v8, v9
	v_mov_b32_e32 v9, v7
	v_pk_mov_b32 v[10:11], v[2:3], v[10:11] op_sel:[1,0]
	v_mov_b32_e32 v14, v12
	v_pk_add_f32 v[8:9], v[8:9], v[10:11] neg_lo:[0,1] neg_hi:[0,1]
	v_mov_b32_e32 v13, v7
	v_pk_add_f32 v[2:3], v[4:5], v[8:9] neg_lo:[0,1] neg_hi:[0,1]
	s_nop 0
	v_pk_add_f32 v[4:5], v[14:15], v[2:3]
	s_nop 0
	v_pk_add_f32 v[8:9], v[4:5], v[4:5] op_sel:[0,1] op_sel_hi:[1,0]
	s_nop 0
	v_pk_add_f32 v[6:7], v[6:7], v[8:9] op_sel:[1,0] op_sel_hi:[0,1]
	v_mov_b32_e32 v5, v6
	v_pk_add_f32 v[10:11], v[4:5], v[12:13] neg_lo:[0,1] neg_hi:[0,1]
	v_mov_b32_e32 v3, v8
	v_sub_f32_e32 v4, v4, v10
	v_pk_add_f32 v[2:3], v[2:3], v[10:11] neg_lo:[0,1] neg_hi:[0,1]
	v_sub_f32_e32 v4, v12, v4
	v_add_f32_e32 v2, v2, v4
	v_add_f32_e32 v2, v2, v3
	v_add_f32_e32 v3, v6, v2
	v_sub_f32_e32 v4, v3, v6
	v_sub_f32_e32 v2, v2, v4
	v_mul_f32_e32 v4, v17, v3
	v_fma_f32 v3, v17, v3, -v4
	v_fmac_f32_e32 v3, v17, v2
	v_add_f32_e32 v2, v4, v3
	v_cmp_class_f32_e64 s[2:3], v4, s77
	v_sub_f32_e32 v5, v2, v4
	v_sub_f32_e32 v3, v3, v5
	v_cndmask_b32_e64 v2, v2, v4, s[2:3]
	v_cmp_eq_f32_e64 s[2:3], s79, v2
	s_nop 1
	v_cndmask_b32_e64 v4, 0, v111, s[2:3]
	v_sub_f32_e32 v5, v2, v4
	v_mul_f32_e32 v6, 0x3fb8aa3b, v5
	v_fma_f32 v7, v5, s80, -v6
	v_rndne_f32_e32 v8, v6
	v_fmac_f32_e32 v7, 0x32a5705f, v5
	v_sub_f32_e32 v6, v6, v8
	v_add_f32_e32 v6, v6, v7
	v_exp_f32_e32 v6, v6
	v_cvt_i32_f32_e32 v7, v8
	v_cmp_neq_f32_e64 s[2:3], |v2|, s78
	s_nop 1
	v_cndmask_b32_e64 v2, 0, v3, s[2:3]
	v_ldexp_f32 v3, v6, v7
	v_cmp_ngt_f32_e64 s[2:3], s81, v5
	v_add_f32_e32 v2, v4, v2
	s_nop 0
	v_cndmask_b32_e64 v3, 0, v3, s[2:3]
	v_cmp_nlt_f32_e64 s[2:3], s79, v5
	s_nop 1
	v_cndmask_b32_e64 v3, v112, v3, s[2:3]
	v_fma_f32 v2, v3, v2, v3
	v_cmp_class_f32_e64 s[2:3], v3, s77
	s_nop 1
	v_cndmask_b32_e64 v2, v2, v3, s[2:3]
	v_cmp_neq_f32_e64 s[2:3], v17, |v17|
	s_nop 1
	v_cndmask_b32_e64 v3, v112, 0, s[2:3]
	v_cndmask_b32_e64 v3, v3, 1.0, vcc
	v_cmp_class_f32_e64 s[2:3], v17, s77
	s_nop 1
	v_cndmask_b32_e64 v2, |v2|, v3, s[2:3]
	v_mul_f32_e32 v1, v2, v1
	s_brev_b32 s2, 18
	v_and_b32_e32 v2, 0x7fffffff, v1
	v_cmp_nlt_f32_e64 s[2:3], |v1|, s2
	s_and_saveexec_b64 s[4:5], s[2:3]
	s_xor_b64 s[12:13], exec, s[4:5]
	s_cbranch_execz .LBB0_1578
	v_lshrrev_b32_e32 v3, 23, v2
	v_add_u32_e32 v3, 0xffffff88, v3
	v_cmp_lt_u32_e32 vcc, 63, v3
	s_mov_b32 s6, 0xfe5163ab
	s_nop 0
	v_cndmask_b32_e32 v4, 0, v113, vcc
	v_add_u32_e32 v3, v4, v3
	v_cmp_lt_u32_e64 s[2:3], 31, v3
	s_nop 1
	v_cndmask_b32_e64 v4, 0, v114, s[2:3]
	v_add_u32_e32 v3, v4, v3
	v_cmp_lt_u32_e64 s[4:5], 31, v3
	s_nop 1
	v_cndmask_b32_e64 v4, 0, v114, s[4:5]
	v_add_u32_e32 v3, v4, v3
	v_and_b32_e32 v4, 0x7fffff, v2
	v_or_b32_e32 v17, 0x800000, v4
	v_mad_u64_u32 v[4:5], s[6:7], v17, s6, 0
	v_mov_b32_e32 v64, v5
	s_mov_b32 s6, 0x3c439041
	v_mad_u64_u32 v[6:7], s[6:7], v17, s6, v[64:65]
	v_mov_b32_e32 v64, v7
	s_mov_b32 s6, 0xdb629599
	v_mad_u64_u32 v[8:9], s[6:7], v17, s6, v[64:65]
	v_mov_b32_e32 v64, v9
	s_mov_b32 s6, 0xf534ddc0
	v_mad_u64_u32 v[10:11], s[6:7], v17, s6, v[64:65]
	v_mov_b32_e32 v64, v11
	s_mov_b32 s6, 0xfc2757d1
	v_mad_u64_u32 v[12:13], s[6:7], v17, s6, v[64:65]
	v_mov_b32_e32 v64, v13
	s_mov_b32 s6, 0x4e441529
	v_mad_u64_u32 v[14:15], s[6:7], v17, s6, v[64:65]
	v_mov_b32_e32 v64, v15
	s_mov_b32 s6, 0xa2f9836e
	v_mad_u64_u32 v[18:19], s[6:7], v17, s6, v[64:65]
	v_cndmask_b32_e32 v5, v14, v10, vcc
	v_cndmask_b32_e32 v7, v18, v12, vcc
	v_cndmask_b32_e32 v11, v19, v14, vcc
	v_cndmask_b32_e64 v9, v7, v5, s[2:3]
	v_cndmask_b32_e64 v7, v11, v7, s[2:3]
	v_cndmask_b32_e32 v11, v12, v8, vcc
	v_cndmask_b32_e64 v5, v5, v11, s[2:3]
	v_sub_u32_e32 v12, 32, v3
	v_cmp_eq_u32_e64 s[6:7], 0, v3
	v_cndmask_b32_e32 v3, v10, v6, vcc
	v_cndmask_b32_e64 v7, v7, v9, s[4:5]
	v_cndmask_b32_e64 v9, v9, v5, s[4:5]
	v_cndmask_b32_e64 v6, v11, v3, s[2:3]
	v_alignbit_b32 v13, v7, v9, v12
	v_cndmask_b32_e64 v5, v5, v6, s[4:5]
	v_cndmask_b32_e64 v7, v13, v7, s[6:7]
	v_alignbit_b32 v10, v9, v5, v12
	v_cndmask_b32_e32 v4, v8, v4, vcc
	v_cndmask_b32_e64 v9, v10, v9, s[6:7]
	v_bfe_u32 v13, v7, 29, 1
	v_cndmask_b32_e64 v3, v3, v4, s[2:3]
	v_alignbit_b32 v10, v7, v9, 30
	v_sub_u32_e32 v14, 0, v13
	v_cndmask_b32_e64 v3, v6, v3, s[4:5]
	v_xor_b32_e32 v10, v10, v14
	v_alignbit_b32 v4, v5, v3, v12
	v_cndmask_b32_e64 v4, v4, v5, s[6:7]
	v_ffbh_u32_e32 v6, v10
	v_alignbit_b32 v5, v9, v4, 30
	v_min_u32_e32 v6, 32, v6
	v_alignbit_b32 v3, v4, v3, 30
	v_xor_b32_e32 v5, v5, v14
	v_sub_u32_e32 v8, 31, v6
	v_xor_b32_e32 v3, v3, v14
	v_alignbit_b32 v9, v10, v5, v8
	v_alignbit_b32 v3, v5, v3, v8
	v_alignbit_b32 v4, v9, v3, 9
	v_ffbh_u32_e32 v5, v4
	v_min_u32_e32 v5, 32, v5
	v_lshrrev_b32_e32 v11, 29, v7
	v_not_b32_e32 v8, v5
	v_alignbit_b32 v3, v4, v3, v8
	v_lshlrev_b32_e32 v4, 31, v11
	v_or_b32_e32 v8, 0x33000000, v4
	v_add_lshl_u32 v5, v5, v6, 23
	v_lshrrev_b32_e32 v3, 9, v3
	v_sub_u32_e32 v5, v8, v5
	v_or_b32_e32 v4, 0.5, v4
	v_lshlrev_b32_e32 v6, 23, v6
	v_or_b32_e32 v3, v5, v3
	v_lshrrev_b32_e32 v5, 9, v9
	v_sub_u32_e32 v4, v4, v6
	v_or_b32_e32 v4, v5, v4
	v_mul_f32_e32 v5, 0x3fc90fda, v4
	s_mov_b32 s2, 0x3fc90fda
	v_fma_f32 v6, v4, s2, -v5
	v_fmac_f32_e32 v6, 0x33a22168, v4
	v_fmac_f32_e32 v6, 0x3fc90fda, v3
	v_lshrrev_b32_e32 v4, 30, v7
	v_add_f32_e32 v3, v5, v6
	v_add_u32_e32 v4, v13, v4

.LBB0_1582:
	v_add_u32_e32 v16, 0xfffffd40, v124
	v_mul_hi_i32 v17, v16, s82
	v_lshrrev_b32_e32 v18, 31, v17
	v_ashrrev_i32_e32 v17, 2, v17
	v_add_u32_e32 v137, v17, v18
	v_mul_lo_u32 v17, v137, 24
	v_sub_u32_e32 v20, v16, v17
	v_mul_lo_u16_e32 v16, 43, v20
	v_lshrrev_b16_e32 v17, 15, v16
	v_ashrrev_i16_e32 v16, 9, v16
	v_add_u16_e32 v16, v16, v17
	v_mul_lo_u16_e32 v16, 12, v16
	v_sub_u16_e32 v22, v20, v16
	v_mov_b64_e32 v[16:17], s[56:57]
	v_cmp_lt_i32_e64 s[28:29], 11, v20
	v_mad_i64_i32 v[18:19], s[6:7], v137, s73, v[16:17]
	s_nop 0
	v_cndmask_b32_e64 v20, v116, v117, s[28:29]
	v_mov_b32_e32 v21, v65
	v_lshl_add_u64 v[18:19], v[18:19], 0, v[20:21]
	v_add_u32_e32 v20, 0xfffffd80, v124
	v_mul_hi_i32 v21, v20, s82
	v_lshlrev_b32_sdwa v90, v118, sext(v22) dst_sel:DWORD dst_unused:UNUSED_PAD src0_sel:DWORD src1_sel:BYTE_0
	v_lshrrev_b32_e32 v22, 31, v21
	v_ashrrev_i32_e32 v21, 2, v21
	v_add_u32_e32 v136, v21, v22
	v_mul_lo_u32 v21, v136, 24
	v_sub_u32_e32 v22, v20, v21
	v_mul_lo_u16_e32 v20, 43, v22
	v_lshrrev_b16_e32 v21, 15, v20
	v_ashrrev_i16_e32 v20, 9, v20
	v_add_u16_e32 v20, v20, v21
	v_mul_lo_u16_e32 v20, 12, v20
	v_sub_u16_e32 v24, v22, v20
	v_cmp_lt_i32_e64 s[26:27], 11, v22
	v_ashrrev_i32_e32 v91, 31, v90
	v_mad_i64_i32 v[20:21], s[6:7], v136, s73, v[16:17]
	v_cndmask_b32_e64 v22, v116, v117, s[26:27]
	v_mov_b32_e32 v23, v65
	v_lshlrev_b32_sdwa v88, v118, sext(v24) dst_sel:DWORD dst_unused:UNUSED_PAD src0_sel:DWORD src1_sel:BYTE_0
	v_lshl_add_u64 v[18:19], v[90:91], 1, v[18:19]
	v_lshl_add_u64 v[20:21], v[20:21], 0, v[22:23]
	v_ashrrev_i32_e32 v89, 31, v88
	v_lshl_add_u64 v[18:19], v[18:19], 0, v[64:65]
	v_lshl_add_u64 v[20:21], v[88:89], 1, v[20:21]
	v_lshl_add_u64 v[20:21], v[20:21], 0, v[64:65]
	global_load_dwordx4 v[60:63], v[18:19], off nt
	global_load_dwordx4 v[56:59], v[20:21], off nt
	v_add_u32_e32 v18, 0xfffffdc0, v124
	v_mul_hi_i32 v19, v18, s82
	v_lshrrev_b32_e32 v20, 31, v19
	v_ashrrev_i32_e32 v19, 2, v19
	v_add_u32_e32 v135, v19, v20
	v_mul_lo_u32 v19, v135, 24
	v_sub_u32_e32 v20, v18, v19
	v_mul_lo_u16_e32 v18, 43, v20
	v_lshrrev_b16_e32 v19, 15, v18
	v_ashrrev_i16_e32 v18, 9, v18
	v_add_u16_e32 v18, v18, v19
	v_mul_lo_u16_e32 v18, 12, v18
	v_cmp_lt_i32_e64 s[24:25], 11, v20
	v_sub_u16_e32 v22, v20, v18
	v_mad_i64_i32 v[18:19], s[6:7], v135, s73, v[16:17]
	v_cndmask_b32_e64 v20, v116, v117, s[24:25]
	v_mov_b32_e32 v21, v65
	v_lshl_add_u64 v[18:19], v[18:19], 0, v[20:21]
	v_add_u32_e32 v20, 0xfffffe00, v124
	v_mul_hi_i32 v21, v20, s82
	v_lshlrev_b32_sdwa v86, v118, sext(v22) dst_sel:DWORD dst_unused:UNUSED_PAD src0_sel:DWORD src1_sel:BYTE_0
	v_lshrrev_b32_e32 v22, 31, v21
	v_ashrrev_i32_e32 v21, 2, v21
	v_add_u32_e32 v134, v21, v22
	v_mul_lo_u32 v21, v134, 24
	v_sub_u32_e32 v22, v20, v21
	v_mul_lo_u16_e32 v20, 43, v22
	v_lshrrev_b16_e32 v21, 15, v20
	v_ashrrev_i16_e32 v20, 9, v20
	v_add_u16_e32 v20, v20, v21
	v_mul_lo_u16_e32 v20, 12, v20
	v_sub_u16_e32 v24, v22, v20
	v_cmp_lt_i32_e64 s[22:23], 11, v22
	v_ashrrev_i32_e32 v87, 31, v86
	v_mad_i64_i32 v[20:21], s[6:7], v134, s73, v[16:17]
	v_cndmask_b32_e64 v22, v116, v117, s[22:23]
	v_lshlrev_b32_sdwa v84, v118, sext(v24) dst_sel:DWORD dst_unused:UNUSED_PAD src0_sel:DWORD src1_sel:BYTE_0
	v_lshl_add_u64 v[18:19], v[86:87], 1, v[18:19]
	v_lshl_add_u64 v[20:21], v[20:21], 0, v[22:23]
	v_ashrrev_i32_e32 v85, 31, v84
	v_lshl_add_u64 v[18:19], v[18:19], 0, v[64:65]
	v_lshl_add_u64 v[20:21], v[84:85], 1, v[20:21]
	v_lshl_add_u64 v[20:21], v[20:21], 0, v[64:65]
	global_load_dwordx4 v[52:55], v[18:19], off nt
	global_load_dwordx4 v[48:51], v[20:21], off nt
	v_add_u32_e32 v18, 0xfffffe40, v124
	v_mul_hi_i32 v19, v18, s82
	v_lshrrev_b32_e32 v20, 31, v19
	v_ashrrev_i32_e32 v19, 2, v19
	v_add_u32_e32 v133, v19, v20
	v_mul_lo_u32 v19, v133, 24
	v_sub_u32_e32 v20, v18, v19
	v_mul_lo_u16_e32 v18, 43, v20
	v_lshrrev_b16_e32 v19, 15, v18
	v_ashrrev_i16_e32 v18, 9, v18
	v_add_u16_e32 v18, v18, v19
	v_mul_lo_u16_e32 v18, 12, v18
	v_cmp_lt_i32_e64 s[20:21], 11, v20
	v_sub_u16_e32 v22, v20, v18
	v_mad_i64_i32 v[18:19], s[6:7], v133, s73, v[16:17]
	v_cndmask_b32_e64 v20, v116, v117, s[20:21]
	v_mov_b32_e32 v21, v65
	v_lshl_add_u64 v[18:19], v[18:19], 0, v[20:21]
	v_add_u32_e32 v20, 0xfffffe80, v124
	v_mul_hi_i32 v21, v20, s82
	v_lshlrev_b32_sdwa v82, v118, sext(v22) dst_sel:DWORD dst_unused:UNUSED_PAD src0_sel:DWORD src1_sel:BYTE_0
	v_lshrrev_b32_e32 v22, 31, v21
	v_ashrrev_i32_e32 v21, 2, v21
	v_add_u32_e32 v132, v21, v22
	v_mul_lo_u32 v21, v132, 24
	v_sub_u32_e32 v22, v20, v21
	v_mul_lo_u16_e32 v20, 43, v22
	v_lshrrev_b16_e32 v21, 15, v20
	v_ashrrev_i16_e32 v20, 9, v20
	v_add_u16_e32 v20, v20, v21
	v_mul_lo_u16_e32 v20, 12, v20
	v_sub_u16_e32 v24, v22, v20
	v_cmp_lt_i32_e64 s[18:19], 11, v22
	v_ashrrev_i32_e32 v83, 31, v82
	v_mad_i64_i32 v[20:21], s[6:7], v132, s73, v[16:17]
	v_cndmask_b32_e64 v22, v116, v117, s[18:19]
	v_lshlrev_b32_sdwa v80, v118, sext(v24) dst_sel:DWORD dst_unused:UNUSED_PAD src0_sel:DWORD src1_sel:BYTE_0
	v_lshl_add_u64 v[18:19], v[82:83], 1, v[18:19]
	v_lshl_add_u64 v[20:21], v[20:21], 0, v[22:23]
	v_ashrrev_i32_e32 v81, 31, v80
	v_lshl_add_u64 v[18:19], v[18:19], 0, v[64:65]
	v_lshl_add_u64 v[20:21], v[80:81], 1, v[20:21]
	v_lshl_add_u64 v[20:21], v[20:21], 0, v[64:65]
	global_load_dwordx4 v[44:47], v[18:19], off nt
	global_load_dwordx4 v[40:43], v[20:21], off nt
	v_add_u32_e32 v18, 0xfffffec0, v124
	v_mul_hi_i32 v19, v18, s82
	v_lshrrev_b32_e32 v20, 31, v19
	v_ashrrev_i32_e32 v19, 2, v19
	v_add_u32_e32 v131, v19, v20
	v_mul_lo_u32 v19, v131, 24
	v_sub_u32_e32 v20, v18, v19
	v_mul_lo_u16_e32 v18, 43, v20
	v_lshrrev_b16_e32 v19, 15, v18
	v_ashrrev_i16_e32 v18, 9, v18
	v_add_u16_e32 v18, v18, v19
	v_mul_lo_u16_e32 v18, 12, v18
	v_cmp_lt_i32_e64 s[16:17], 11, v20
	v_sub_u16_e32 v22, v20, v18
	v_mad_i64_i32 v[18:19], s[6:7], v131, s73, v[16:17]
	v_cndmask_b32_e64 v20, v116, v117, s[16:17]
	v_mov_b32_e32 v21, v65
	v_lshl_add_u64 v[18:19], v[18:19], 0, v[20:21]
	v_add_u32_e32 v20, 0xffffff00, v124
	v_mul_hi_i32 v21, v20, s82
	v_lshlrev_b32_sdwa v78, v118, sext(v22) dst_sel:DWORD dst_unused:UNUSED_PAD src0_sel:DWORD src1_sel:BYTE_0
	v_lshrrev_b32_e32 v22, 31, v21
	v_ashrrev_i32_e32 v21, 2, v21
	v_add_u32_e32 v130, v21, v22
	v_mul_lo_u32 v21, v130, 24
	v_sub_u32_e32 v22, v20, v21
	v_mul_lo_u16_e32 v20, 43, v22
	v_lshrrev_b16_e32 v21, 15, v20
	v_ashrrev_i16_e32 v20, 9, v20
	v_add_u16_e32 v20, v20, v21
	v_mul_lo_u16_e32 v20, 12, v20
	v_sub_u16_e32 v24, v22, v20
	v_cmp_lt_i32_e64 s[14:15], 11, v22
	v_ashrrev_i32_e32 v79, 31, v78
	v_mad_i64_i32 v[20:21], s[6:7], v130, s73, v[16:17]
	v_cndmask_b32_e64 v22, v116, v117, s[14:15]
	v_lshlrev_b32_sdwa v76, v118, sext(v24) dst_sel:DWORD dst_unused:UNUSED_PAD src0_sel:DWORD src1_sel:BYTE_0
	v_lshl_add_u64 v[18:19], v[78:79], 1, v[18:19]
	v_lshl_add_u64 v[20:21], v[20:21], 0, v[22:23]
	v_ashrrev_i32_e32 v77, 31, v76
	v_lshl_add_u64 v[18:19], v[18:19], 0, v[64:65]
	v_lshl_add_u64 v[20:21], v[76:77], 1, v[20:21]
	v_lshl_add_u64 v[20:21], v[20:21], 0, v[64:65]
	global_load_dwordx4 v[36:39], v[18:19], off nt
	s_waitcnt lgkmcnt(0)
	global_load_dwordx4 v[32:35], v[20:21], off nt
	v_add_u32_e32 v18, 0xffffff40, v124
	v_mul_hi_i32 v19, v18, s82
	v_lshrrev_b32_e32 v20, 31, v19
	v_ashrrev_i32_e32 v19, 2, v19
	v_add_u32_e32 v129, v19, v20
	v_mul_lo_u32 v19, v129, 24
	v_sub_u32_e32 v20, v18, v19
	v_mul_lo_u16_e32 v18, 43, v20
	v_lshrrev_b16_e32 v19, 15, v18
	v_ashrrev_i16_e32 v18, 9, v18
	v_add_u16_e32 v18, v18, v19
	v_mul_lo_u16_e32 v18, 12, v18
	v_cmp_lt_i32_e64 s[12:13], 11, v20
	v_sub_u16_e32 v22, v20, v18
	v_mad_i64_i32 v[18:19], s[6:7], v129, s73, v[16:17]
	v_cndmask_b32_e64 v20, v116, v117, s[12:13]
	v_mov_b32_e32 v21, v65
	v_lshl_add_u64 v[18:19], v[18:19], 0, v[20:21]
	v_add_u32_e32 v20, 0xffffff80, v124
	v_mul_hi_i32 v21, v20, s82
	v_lshlrev_b32_sdwa v74, v118, sext(v22) dst_sel:DWORD dst_unused:UNUSED_PAD src0_sel:DWORD src1_sel:BYTE_0
	v_lshrrev_b32_e32 v22, 31, v21
	v_ashrrev_i32_e32 v21, 2, v21
	v_add_u32_e32 v128, v21, v22
	v_mul_lo_u32 v21, v128, 24
	v_sub_u32_e32 v22, v20, v21
	v_mul_lo_u16_e32 v20, 43, v22
	v_lshrrev_b16_e32 v21, 15, v20
	v_ashrrev_i16_e32 v20, 9, v20
	v_add_u16_e32 v20, v20, v21
	v_mul_lo_u16_e32 v20, 12, v20
	v_sub_u16_e32 v24, v22, v20
	v_cmp_lt_i32_e64 s[10:11], 11, v22
	v_ashrrev_i32_e32 v75, 31, v74
	v_mad_i64_i32 v[20:21], s[6:7], v128, s73, v[16:17]
	v_cndmask_b32_e64 v22, v116, v117, s[10:11]
	v_lshlrev_b32_sdwa v72, v118, sext(v24) dst_sel:DWORD dst_unused:UNUSED_PAD src0_sel:DWORD src1_sel:BYTE_0
	v_lshl_add_u64 v[18:19], v[74:75], 1, v[18:19]
	v_lshl_add_u64 v[20:21], v[20:21], 0, v[22:23]
	v_ashrrev_i32_e32 v73, 31, v72
	v_lshl_add_u64 v[18:19], v[18:19], 0, v[64:65]
	v_lshl_add_u64 v[20:21], v[72:73], 1, v[20:21]
	v_lshl_add_u64 v[20:21], v[20:21], 0, v[64:65]
	global_load_dwordx4 v[28:31], v[18:19], off nt
	global_load_dwordx4 v[24:27], v[20:21], off nt
	v_subrev_u32_e32 v18, 64, v124
	v_mul_hi_i32 v19, v18, s82
	v_lshrrev_b32_e32 v20, 31, v19
	v_ashrrev_i32_e32 v19, 2, v19
	v_add_u32_e32 v127, v19, v20
	v_mul_lo_u32 v19, v127, 24
	v_sub_u32_e32 v20, v18, v19
	v_mul_lo_u16_e32 v18, 43, v20
	v_lshrrev_b16_e32 v19, 15, v18
	v_ashrrev_i16_e32 v18, 9, v18
	v_add_u16_e32 v18, v18, v19
	v_mul_lo_u16_e32 v18, 12, v18
	v_cmp_lt_i32_e64 s[8:9], 11, v20
	v_sub_u16_e32 v22, v20, v18
	v_mad_i64_i32 v[18:19], s[6:7], v127, s73, v[16:17]
	v_cndmask_b32_e64 v20, v116, v117, s[8:9]
	v_mov_b32_e32 v21, v65
	v_lshl_add_u64 v[18:19], v[18:19], 0, v[20:21]
	v_mul_hi_i32 v20, v124, s82
	v_lshrrev_b32_e32 v21, 31, v20
	v_ashrrev_i32_e32 v20, 2, v20
	v_add_u32_e32 v126, v20, v21
	v_mul_lo_u32 v20, v126, 24
	v_sub_u32_e32 v20, v124, v20
	v_mul_lo_u16_e32 v21, 43, v20
	v_lshlrev_b32_sdwa v70, v118, sext(v22) dst_sel:DWORD dst_unused:UNUSED_PAD src0_sel:DWORD src1_sel:BYTE_0
	v_lshrrev_b16_e32 v22, 15, v21
	v_ashrrev_i16_e32 v21, 9, v21
	v_add_u16_e32 v21, v21, v22
	v_mul_lo_u16_e32 v21, 12, v21
	v_mad_i64_i32 v[16:17], s[6:7], v126, s73, v[16:17]
	v_sub_u16_e32 v22, v20, v21
	v_cmp_lt_i32_e64 s[6:7], 11, v20
	v_mov_b32_e32 v21, v65
	v_lshlrev_b32_sdwa v68, v118, sext(v22) dst_sel:DWORD dst_unused:UNUSED_PAD src0_sel:DWORD src1_sel:BYTE_0
	v_cndmask_b32_e64 v20, v116, v117, s[6:7]
	v_ashrrev_i32_e32 v71, 31, v70
	v_lshl_add_u64 v[16:17], v[16:17], 0, v[20:21]
	v_ashrrev_i32_e32 v69, 31, v68
	v_lshl_add_u64 v[18:19], v[70:71], 1, v[18:19]
	v_lshl_add_u64 v[16:17], v[68:69], 1, v[16:17]
	v_lshl_add_u64 v[18:19], v[18:19], 0, v[64:65]
	v_lshl_add_u64 v[16:17], v[16:17], 0, v[64:65]
	global_load_dwordx4 v[20:23], v[18:19], off nt
	s_nop 0
	global_load_dwordx4 v[16:19], v[16:17], off nt
	s_waitcnt vmcnt(11)
	v_lshlrev_b32_e32 v94, 16, v60
	v_and_b32_e32 v95, 0xffff0000, v60
	v_pk_mul_f32 v[98:99], v[94:95], v[94:95]
	v_lshlrev_b32_e32 v60, 16, v61
	v_and_b32_e32 v61, 0xffff0000, v61
	v_pk_mul_f32 v[100:101], v[60:61], v[60:61]
	v_add_f32_e32 v98, v98, v99
	v_lshlrev_b32_e32 v102, 16, v62
	v_and_b32_e32 v103, 0xffff0000, v62
	v_add_f32_e32 v98, v100, v98
	v_and_b32_e32 v96, 0xffff0000, v63
	v_lshlrev_b32_e32 v97, 16, v63
	v_pk_mul_f32 v[62:63], v[102:103], v[102:103]
	v_add_f32_e32 v98, v101, v98
	v_add_f32_e32 v62, v62, v98
	v_pk_mul_f32 v[92:93], v[96:97], v[96:97]
	v_add_f32_e32 v62, v63, v62
	v_add_f32_e32 v62, v93, v62
	v_add_f32_e32 v62, v92, v62
	ds_swizzle_b32 v63, v62 offset:swizzle(SWAP,1)
	s_waitcnt lgkmcnt(0)
	v_add_f32_e32 v62, v62, v63
	ds_swizzle_b32 v63, v62 offset:swizzle(SWAP,2)
	s_waitcnt lgkmcnt(0)
	v_add_f32_e32 v62, v62, v63
	ds_swizzle_b32 v63, v62 offset:swizzle(SWAP,4)
	s_waitcnt lgkmcnt(0)
	v_add_f32_e32 v62, v62, v63
	v_fmamk_f32 v62, v62, 0x3c800000, v107
	v_mul_f32_e32 v63, 0x4f800000, v62
	v_cmp_gt_f32_e32 vcc, s84, v62
	s_nop 1
	v_cndmask_b32_e32 v62, v62, v63, vcc
	v_sqrt_f32_e32 v92, v62
	v_cndmask_b32_e64 v63, v9, v13, s[28:29]
	v_add_u32_e32 v93, -1, v92
	v_fma_f32 v98, -v93, v92, v62
	v_cmp_ge_f32_e64 s[30:31], 0, v98
	v_add_u32_e32 v98, 1, v92
	s_nop 0
	v_cndmask_b32_e64 v93, v92, v93, s[30:31]
	v_fma_f32 v92, -v98, v92, v62
	v_cmp_lt_f32_e64 s[30:31], 0, v92
	s_nop 1
	v_cndmask_b32_e64 v92, v93, v98, s[30:31]
	v_mul_f32_e32 v93, 0x37800000, v92
	v_cndmask_b32_e32 v92, v92, v93, vcc
	v_cmp_class_f32_e32 vcc, v62, v108
	v_cndmask_b32_e64 v93, v11, v15, s[28:29]
	s_nop 0
	v_cndmask_b32_e32 v98, v92, v62, vcc
	v_div_scale_f32 v99, s[30:31], v98, v98, 1.0
	v_rcp_f32_e32 v100, v99
	v_cndmask_b32_e64 v62, v8, v12, s[28:29]
	v_cndmask_b32_e64 v92, v10, v14, s[28:29]
	v_fma_f32 v101, -v99, v100, 1.0
	v_fmac_f32_e32 v100, v101, v100
	v_div_scale_f32 v101, vcc, 1.0, v98, 1.0
	v_mul_f32_e32 v138, v101, v100
	v_fma_f32 v139, -v99, v138, v101
	v_fmac_f32_e32 v138, v139, v100
	v_fma_f32 v99, -v99, v138, v101
	v_div_fmas_f32 v99, v99, v100, v138
	v_div_fixup_f32 v98, v99, v98, 1.0
	v_pk_mul_f32 v[94:95], v[98:99], v[94:95] op_sel_hi:[0,1]
	v_pk_mul_f32 v[60:61], v[98:99], v[60:61] op_sel_hi:[0,1]
	v_pk_mul_f32 v[94:95], v[62:63], v[94:95]
	v_pk_mul_f32 v[92:93], v[92:93], v[60:61]
	v_pk_mul_f32 v[60:61], v[98:99], v[102:103] op_sel_hi:[0,1]
	v_cndmask_b32_e64 v63, v1, v5, s[28:29]
	v_cndmask_b32_e64 v62, v0, v4, s[28:29]
	v_pk_mul_f32 v[60:61], v[62:63], v[60:61]
	v_pk_mul_f32 v[62:63], v[98:99], v[96:97] op_sel_hi:[0,1]
	v_cndmask_b32_e64 v97, v3, v7, s[28:29]
	v_cndmask_b32_e64 v96, v2, v6, s[28:29]
	v_pk_mul_f32 v[62:63], v[96:97], v[62:63] op_sel:[0,1] op_sel_hi:[1,0]
	ds_swizzle_b32 v96, v94 offset:swizzle(SWAP,1)
	ds_swizzle_b32 v97, v95 offset:swizzle(SWAP,1)
	ds_swizzle_b32 v98, v92 offset:swizzle(SWAP,1)
	ds_swizzle_b32 v99, v93 offset:swizzle(SWAP,1)
	ds_swizzle_b32 v102, v60 offset:swizzle(SWAP,1)
	ds_swizzle_b32 v103, v61 offset:swizzle(SWAP,1)
	ds_swizzle_b32 v100, v62 offset:swizzle(SWAP,1)
	ds_swizzle_b32 v101, v63 offset:swizzle(SWAP,1)
	s_and_saveexec_b64 s[30:31], s[2:3]
	s_cbranch_execz .LBB0_1584
	v_lshl_add_u32 v146, v137, 6, s60
	ds_read2_b32 v[138:139], v146 offset0:8 offset1:9
	ds_read2_b32 v[140:141], v146 offset0:10 offset1:11
	ds_read2_b32 v[142:143], v146 offset0:12 offset1:13
	ds_read2_b32 v[144:145], v146 offset0:14 offset1:15
	s_waitcnt lgkmcnt(3)
	v_pk_mul_f32 v[96:97], v[138:139], v[96:97]
	s_waitcnt lgkmcnt(2)
	v_pk_mul_f32 v[98:99], v[140:141], v[98:99]
	s_waitcnt lgkmcnt(1)
	v_pk_mul_f32 v[102:103], v[142:143], v[102:103]
	ds_read2_b32 v[138:139], v146 offset1:1
	ds_read2_b32 v[140:141], v146 offset0:2 offset1:3
	ds_read2_b32 v[142:143], v146 offset0:4 offset1:5
	ds_read2_b32 v[146:147], v146 offset0:6 offset1:7
	s_waitcnt lgkmcnt(4)
	v_pk_mul_f32 v[100:101], v[144:145], v[100:101]
	v_cndmask_b32_e64 v97, v97, -v97, s[4:5]
	v_cndmask_b32_e64 v96, v96, -v96, s[4:5]
	v_cndmask_b32_e64 v99, v99, -v99, s[4:5]
	v_cndmask_b32_e64 v98, v98, -v98, s[4:5]
	v_cndmask_b32_e64 v102, v102, -v102, s[4:5]
	v_cndmask_b32_e64 v103, v103, -v103, s[4:5]
	v_cndmask_b32_e64 v100, v100, -v100, s[4:5]
	v_cndmask_b32_e64 v101, v101, -v101, s[4:5]
	s_waitcnt lgkmcnt(0)
	v_pk_fma_f32 v[62:63], v[62:63], v[146:147], v[100:101]
	v_pk_fma_f32 v[60:61], v[60:61], v[142:143], v[102:103]
	v_pk_fma_f32 v[92:93], v[92:93], v[140:141], v[98:99]
	v_pk_fma_f32 v[94:95], v[94:95], v[138:139], v[96:97]

.LBB0_1606:
	s_add_i32 s54, s54, s96
	s_cmpk_lt_u32 s54, 0x1000
	s_cselect_b64 s[2:3], -1, 0
	s_and_b64 s[2:3], s[2:3], exec
	s_cselect_b32 s6, 7, 0
	s_or_b32 s4, s48, 6
	s_cmpk_lt_u32 s54, 0x1000
	s_cselect_b64 s[2:3], -1, 0
	s_and_b64 s[2:3], s[2:3], exec
	s_cselect_b32 s8, s4, s48
	s_or_b32 s4, s48, 5
	s_cmpk_lt_u32 s54, 0x1000
	s_cselect_b64 s[2:3], -1, 0
	s_and_b64 s[2:3], s[2:3], exec
	s_cselect_b32 s9, s4, s48
	s_or_b32 s4, s48, 4
	s_cmpk_lt_u32 s54, 0x1000
	s_cselect_b64 s[2:3], -1, 0
	s_and_b64 s[2:3], s[2:3], exec
	s_cselect_b32 s10, s4, s48
	s_or_b32 s4, s48, 3
	s_cmpk_lt_u32 s54, 0x1000
	s_cselect_b64 s[2:3], -1, 0
	s_and_b64 s[2:3], s[2:3], exec
	s_cselect_b32 s11, s4, s48
	s_or_b32 s4, s48, 2
	s_cmpk_lt_u32 s54, 0x1000
	v_lshlrev_b32_e32 v64, 2, v67
	v_lshl_add_u64 v[0:1], s[56:57], 0, v[64:65]
	s_mov_b64 s[2:3], 0x1e00
	s_cselect_b64 vcc, -1, 0
	v_lshl_add_u64 v[2:3], v[0:1], 0, s[2:3]
	s_and_b64 s[2:3], vcc, exec
	s_cselect_b32 s12, s4, s48
	s_add_i32 s7, s48, -1
	s_add_i32 s2, s7, s96
	s_cmpk_lt_u32 s2, 0x1000
	s_cselect_b64 s[2:3], -1, 0
	s_and_b64 s[4:5], s[2:3], exec
	v_cndmask_b32_e64 v8, 0, 1, vcc
	s_cselect_b32 s13, s7, s48
	v_mad_i64_i32 v[4:5], s[4:5], s13, v121, v[2:3]
	v_or_b32_e32 v20, s48, v8
	s_or_b32 s14, s6, s48
	s_waitcnt lgkmcnt(0)
	s_barrier
	v_mad_i64_i32 v[6:7], s[4:5], s48, v121, v[2:3]
	v_mad_i64_i32 v[8:9], s[4:5], v20, s73, v[2:3]
	v_mad_i64_i32 v[10:11], s[4:5], s12, v121, v[2:3]
	v_mad_i64_i32 v[12:13], s[4:5], s11, v121, v[2:3]
	v_mad_i64_i32 v[14:15], s[4:5], s10, v121, v[2:3]
	v_mad_i64_i32 v[16:17], s[4:5], s9, v121, v[2:3]
	v_mad_i64_i32 v[18:19], s[4:5], s8, v121, v[2:3]
	global_load_dword v21, v[4:5], off nt
	global_load_dword v22, v[6:7], off nt
	global_load_dword v23, v[8:9], off nt
	global_load_dword v24, v[10:11], off nt
	global_load_dword v25, v[12:13], off nt
	global_load_dword v26, v[14:15], off nt
	global_load_dword v27, v[16:17], off nt
	global_load_dword v28, v[18:19], off nt
	v_mad_i64_i32 v[4:5], s[4:5], s14, v121, v[2:3]
	s_add_i32 s15, s48, 8
	s_add_i32 s4, s15, s96
	s_cmpk_lt_u32 s4, 0x1000
	s_cselect_b64 s[4:5], -1, 0
	s_and_b64 s[6:7], s[4:5], exec
	s_cselect_b32 s15, s15, s48
	v_mad_i64_i32 v[2:3], s[6:7], s15, v121, v[2:3]
	s_mov_b64 s[6:7], 0x2400
	s_nop 0
	v_lshl_add_u64 v[6:7], v[0:1], 0, s[6:7]
	v_mad_i64_i32 v[8:9], s[6:7], s13, v121, v[6:7]
	v_mad_i64_i32 v[18:19], s[6:7], s10, v121, v[6:7]
	v_mad_i64_i32 v[10:11], s[6:7], s48, v121, v[6:7]
	v_mad_i64_i32 v[12:13], s[6:7], v20, s73, v[6:7]
	v_mad_i64_i32 v[14:15], s[6:7], s12, v121, v[6:7]
	v_mad_i64_i32 v[16:17], s[6:7], s11, v121, v[6:7]
	global_load_dword v29, v[4:5], off nt
	global_load_dword v30, v[2:3], off nt
	global_load_dword v31, v[8:9], off nt
	global_load_dword v32, v[10:11], off nt
	global_load_dword v33, v[12:13], off nt
	global_load_dword v34, v[14:15], off nt
	global_load_dword v35, v[16:17], off nt
	s_nop 0
	global_load_dword v18, v[18:19], off nt
	v_mad_i64_i32 v[2:3], s[6:7], s9, v121, v[6:7]
	v_mad_i64_i32 v[4:5], s[6:7], s8, v121, v[6:7]
	v_mad_i64_i32 v[8:9], s[6:7], s14, v121, v[6:7]
	v_mad_i64_i32 v[6:7], s[6:7], s15, v121, v[6:7]
	s_mov_b64 s[6:7], 0x2a00
	s_nop 0
	v_lshl_add_u64 v[0:1], v[0:1], 0, s[6:7]
	v_mad_i64_i32 v[10:11], s[6:7], s13, v121, v[0:1]
	v_mad_i64_i32 v[12:13], s[6:7], s48, v121, v[0:1]
	v_mad_i64_i32 v[14:15], s[6:7], v20, s73, v[0:1]
	v_mad_i64_i32 v[16:17], s[6:7], s12, v121, v[0:1]
	global_load_dword v19, v[2:3], off nt
	global_load_dword v20, v[4:5], off nt
	global_load_dword v36, v[8:9], off nt
	global_load_dword v37, v[6:7], off nt
	global_load_dword v38, v[10:11], off nt
	s_nop 0
	global_load_dword v12, v[12:13], off nt
	s_nop 0
	global_load_dword v13, v[14:15], off nt
	s_nop 0
	global_load_dword v14, v[16:17], off nt
	v_mad_i64_i32 v[2:3], s[6:7], s11, v121, v[0:1]
	v_mad_i64_i32 v[4:5], s[6:7], s10, v121, v[0:1]
	v_mad_i64_i32 v[6:7], s[6:7], s9, v121, v[0:1]
	v_mad_i64_i32 v[8:9], s[6:7], s8, v121, v[0:1]
	v_mad_i64_i32 v[10:11], s[6:7], s14, v121, v[0:1]
	v_mad_i64_i32 v[0:1], s[6:7], s15, v121, v[0:1]
	global_load_dword v2, v[2:3], off nt
	s_nop 0
	global_load_dword v3, v[4:5], off nt
	s_nop 0
	global_load_dword v4, v[6:7], off nt
	global_load_dword v5, v[8:9], off nt
	s_nop 0
	global_load_dword v6, v[10:11], off nt
	s_nop 0
	global_load_dword v0, v[0:1], off nt
	s_mov_b32 s48, 0
	s_mul_i32 s18, s65, 6
	s_xor_b32 s19, s95, 63
	s_mul_i32 s20, s65, 12
	s_waitcnt vmcnt(29)
	v_cndmask_b32_e64 v68, 0, v21, s[2:3]
	s_waitcnt vmcnt(28)
	v_cndmask_b32_e32 v69, 0, v22, vcc
	s_waitcnt vmcnt(27)
	v_cndmask_b32_e32 v70, 0, v23, vcc
	s_waitcnt vmcnt(26)
	v_cndmask_b32_e32 v71, 0, v24, vcc
	s_waitcnt vmcnt(25)
	v_cndmask_b32_e32 v72, 0, v25, vcc
	s_waitcnt vmcnt(24)
	v_cndmask_b32_e32 v73, 0, v26, vcc
	s_waitcnt vmcnt(23)
	v_cndmask_b32_e32 v74, 0, v27, vcc
	s_waitcnt vmcnt(22)
	v_cndmask_b32_e32 v75, 0, v28, vcc
	s_waitcnt vmcnt(21)
	v_cndmask_b32_e32 v76, 0, v29, vcc
	s_waitcnt vmcnt(20)
	v_cndmask_b32_e64 v77, 0, v30, s[4:5]
	s_waitcnt vmcnt(19)
	v_cndmask_b32_e64 v78, 0, v31, s[2:3]
	s_waitcnt vmcnt(18)
	v_cndmask_b32_e32 v79, 0, v32, vcc
	s_waitcnt vmcnt(17)
	v_cndmask_b32_e32 v80, 0, v33, vcc
	s_waitcnt vmcnt(16)
	v_cndmask_b32_e32 v81, 0, v34, vcc
	s_waitcnt vmcnt(15)
	v_cndmask_b32_e32 v82, 0, v35, vcc
	s_waitcnt vmcnt(14)
	v_cndmask_b32_e32 v83, 0, v18, vcc
	s_waitcnt vmcnt(13)
	v_cndmask_b32_e32 v84, 0, v19, vcc
	s_waitcnt vmcnt(12)
	v_cndmask_b32_e32 v85, 0, v20, vcc
	s_waitcnt vmcnt(11)
	v_cndmask_b32_e32 v86, 0, v36, vcc
	s_waitcnt vmcnt(10)
	v_cndmask_b32_e64 v87, 0, v37, s[4:5]
	s_waitcnt vmcnt(9)
	v_cndmask_b32_e64 v88, 0, v38, s[2:3]
	s_waitcnt vmcnt(8)
	v_cndmask_b32_e32 v89, 0, v12, vcc
	s_waitcnt vmcnt(7)
	v_cndmask_b32_e32 v90, 0, v13, vcc
	s_waitcnt vmcnt(6)
	v_cndmask_b32_e32 v91, 0, v14, vcc
	s_waitcnt vmcnt(5)
	v_cndmask_b32_e32 v92, 0, v2, vcc
	s_waitcnt vmcnt(4)
	v_cndmask_b32_e32 v93, 0, v3, vcc
	s_waitcnt vmcnt(3)
	v_cndmask_b32_e32 v94, 0, v4, vcc
	s_waitcnt vmcnt(2)
	v_cndmask_b32_e32 v95, 0, v5, vcc
	s_waitcnt vmcnt(1)
	v_cndmask_b32_e32 v96, 0, v6, vcc
	s_waitcnt vmcnt(0)
	v_cndmask_b32_e64 v97, 0, v0, s[4:5]
	s_branch .LBB0_1608

.LBB0_1608:
	s_waitcnt lgkmcnt(0)
	s_barrier
	v_lshlrev_b32_e32 v24, 16, v69
	v_and_b32_e32 v38, 63, v123
	v_lshlrev_b32_e32 v39, 1, v38
	v_lshl_or_b32 v64, s48, 7, v39
	v_lshlrev_b64 v[0:1], 2, v[64:65]
	v_lshl_add_u64 v[26:27], s[44:45], 0, v[0:1]
	global_load_dwordx2 v[2:3], v[26:27], off
	v_lshl_add_u64 v[28:29], s[42:43], 0, v[0:1]
	global_load_dwordx2 v[4:5], v[28:29], off
	v_lshl_add_u64 v[0:1], s[46:47], 0, v[0:1]
	global_load_dwordx2 v[6:7], v[0:1], off
	global_load_dwordx2 v[34:35], v[26:27], off offset:3072
	global_load_dwordx2 v[32:33], v[28:29], off offset:3072
	v_add_co_u32_e32 v28, vcc, s74, v28
	v_and_b32_e32 v25, 0xffff0000, v69
	s_nop 0
	v_addc_co_u32_e32 v29, vcc, 0, v29, vcc
	v_add_co_u32_e32 v40, vcc, s74, v26
	v_lshlrev_b32_e32 v22, 16, v70
	s_nop 0
	v_addc_co_u32_e32 v41, vcc, 0, v27, vcc
	v_and_b32_e32 v23, 0xffff0000, v70
	v_lshlrev_b32_e32 v30, 16, v68
	v_and_b32_e32 v31, 0xffff0000, v68
	global_load_dwordx2 v[36:37], v[0:1], off offset:3072
	global_load_dwordx2 v[26:27], v[28:29], off offset:2048
	s_nop 0
	global_load_dwordx2 v[28:29], v[40:41], off offset:2048
	v_lshlrev_b32_e32 v20, 16, v71
	v_and_b32_e32 v21, 0xffff0000, v71
	v_readfirstlane_b32 s6, v123
	s_ashr_i32 s7, s6, 6
	s_lshl_b32 s2, s7, 11
	s_lshl_b32 s3, s7, 1
	s_add_i32 s9, s64, s2
	s_and_b32 s10, s3, 2
	v_lshlrev_b32_e32 v18, 16, v72
	v_and_b32_e32 v19, 0xffff0000, v72
	v_lshlrev_b32_e32 v16, 16, v73
	v_and_b32_e32 v17, 0xffff0000, v73
	v_lshlrev_b32_e32 v14, 16, v74
	v_and_b32_e32 v15, 0xffff0000, v74
	v_lshlrev_b32_e32 v8, 16, v75
	v_and_b32_e32 v9, 0xffff0000, v75
	s_lshl_b32 s8, s7, 3
	v_lshlrev_b32_e32 v12, 16, v76
	v_and_b32_e32 v13, 0xffff0000, v76
	v_lshlrev_b32_e32 v10, 16, v77
	v_and_b32_e32 v11, 0xffff0000, v77
	s_add_i32 s21, s48, 1
	s_waitcnt vmcnt(7)
	v_pk_mul_f32 v[40:41], v[2:3], v[24:25]
	v_pk_mul_f32 v[42:43], v[2:3], v[22:23]
	s_waitcnt vmcnt(6)
	v_pk_fma_f32 v[30:31], v[4:5], v[30:31], v[40:41]
	v_pk_fma_f32 v[24:25], v[4:5], v[24:25], v[42:43]
	s_waitcnt vmcnt(5)
	v_pk_fma_f32 v[30:31], v[6:7], v[22:23], v[30:31]
	v_pk_fma_f32 v[42:43], v[6:7], v[20:21], v[24:25]
	v_mul_f32_e32 v24, 0xbfb8aa3b, v31
	v_mul_f32_e32 v25, 0xbfb8aa3b, v30
	v_exp_f32_e32 v24, v24
	v_exp_f32_e32 v25, v25
	v_mul_f32_e32 v40, 0xbfb8aa3b, v43
	v_mul_f32_e32 v41, 0xbfb8aa3b, v42
	v_add_f32_e32 v24, 1.0, v24
	v_add_f32_e32 v25, 1.0, v25
	v_exp_f32_e32 v40, v40
	v_exp_f32_e32 v41, v41
	v_rcp_f32_e32 v45, v24
	v_rcp_f32_e32 v44, v25
	v_add_f32_e32 v40, 1.0, v40
	v_add_f32_e32 v41, 1.0, v41
	v_rcp_f32_e32 v47, v40
	v_pk_mul_f32 v[30:31], v[30:31], v[44:45]
	v_rcp_f32_e32 v46, v41
	v_pk_mul_f32 v[44:45], v[30:31], v[30:31]
	v_bfe_u32 v41, v123, 2, 4
	v_add_f32_e32 v25, v44, v45
	ds_swizzle_b32 v44, v25 offset:swizzle(SWAP,1)
	v_pk_mul_f32 v[42:43], v[42:43], v[46:47]
	v_lshlrev_b32_e32 v24, 2, v123
	v_pk_mul_f32 v[46:47], v[42:43], v[42:43]
	v_and_b32_e32 v48, 12, v24
	v_add_f32_e32 v40, v46, v47
	ds_swizzle_b32 v45, v40 offset:swizzle(SWAP,1)
	s_waitcnt lgkmcnt(1)
	v_add_f32_e32 v25, v25, v44
	ds_swizzle_b32 v44, v25 offset:swizzle(SWAP,2)
	v_bitop3_b32 v46, s3, v41, 2 bitop3:0x6c
	v_lshlrev_b32_e32 v46, 4, v46
	s_waitcnt lgkmcnt(1)
	v_add_f32_e32 v40, v40, v45
	ds_swizzle_b32 v45, v40 offset:swizzle(SWAP,2)
	s_waitcnt lgkmcnt(1)
	v_add_f32_e32 v25, v25, v44
	ds_swizzle_b32 v44, v25 offset:swizzle(SWAP,4)
	s_waitcnt lgkmcnt(1)
	v_add_f32_e32 v40, v40, v45
	ds_swizzle_b32 v45, v40 offset:swizzle(SWAP,4)
	s_waitcnt lgkmcnt(1)
	v_add_f32_e32 v25, v25, v44
	ds_swizzle_b32 v47, v25 offset:swizzle(SWAP,8)
	s_waitcnt lgkmcnt(1)
	v_add_f32_e32 v40, v40, v45
	ds_swizzle_b32 v49, v40 offset:swizzle(SWAP,8)
	v_pk_mul_f32 v[44:45], v[2:3], v[20:21]
	s_waitcnt lgkmcnt(1)
	v_add_f32_e32 v25, v25, v47
	v_pk_fma_f32 v[22:23], v[4:5], v[22:23], v[44:45]
	ds_swizzle_b32 v44, v25 offset:swizzle(SWAP,16)
	s_waitcnt lgkmcnt(1)
	v_add_f32_e32 v40, v40, v49
	ds_swizzle_b32 v45, v40 offset:swizzle(SWAP,16)
	v_pk_fma_f32 v[22:23], v[6:7], v[18:19], v[22:23]
	s_waitcnt lgkmcnt(1)
	v_add_f32_e32 v25, v25, v44
	v_mov_b32_e32 v44, v25
	s_nop 1
	v_permlane32_swap_b32_e32 v25, v44
	v_add_f32_e32 v25, v25, v44
	v_add_f32_e32 v25, 0x358637bd, v25
	s_waitcnt lgkmcnt(0)
	v_add_f32_e32 v40, v40, v45
	v_mul_f32_e32 v44, 0x4f800000, v25
	v_cmp_gt_f32_e32 vcc, s84, v25
	v_mov_b32_e32 v45, v40
	s_nop 1
	v_permlane32_swap_b32_e32 v40, v45
	v_cndmask_b32_e32 v25, v25, v44, vcc
	v_sqrt_f32_e32 v44, v25
	v_add_f32_e32 v40, v40, v45
	v_add_f32_e32 v40, 0x358637bd, v40
	v_mul_f32_e32 v45, 0x4f800000, v40
	v_cmp_gt_f32_e64 s[2:3], s84, v40
	v_add_u32_e32 v51, 1, v44
	v_fma_f32 v54, -v51, v44, v25
	v_cndmask_b32_e64 v45, v40, v45, s[2:3]
	v_add_u32_e32 v40, -1, v44
	v_fma_f32 v53, -v40, v44, v25
	v_cmp_ge_f32_e64 s[4:5], 0, v53
	v_sqrt_f32_e32 v50, v45
	v_mul_f32_e32 v47, 0xbfb8aa3b, v23
	v_cndmask_b32_e64 v40, v44, v40, s[4:5]
	v_cmp_lt_f32_e64 s[4:5], 0, v54
	v_add_u32_e32 v52, -1, v50
	v_fma_f32 v55, -v52, v50, v45
	v_cndmask_b32_e64 v40, v40, v51, s[4:5]
	v_mul_f32_e32 v44, 0x37800000, v40
	v_cndmask_b32_e32 v40, v40, v44, vcc
	v_cmp_class_f32_e32 vcc, v25, v108
	v_mul_f32_e32 v49, 0xbfb8aa3b, v22
	v_exp_f32_e32 v47, v47
	v_cndmask_b32_e32 v25, v40, v25, vcc
	v_div_scale_f32 v40, s[4:5], v25, v25, 1.0
	v_rcp_f32_e32 v44, v40
	v_cmp_ge_f32_e32 vcc, 0, v55
	v_exp_f32_e32 v49, v49
	s_or_b32 s4, s8, 4
	v_fma_f32 v53, -v40, v44, 1.0
	v_cndmask_b32_e32 v51, v50, v52, vcc
	v_div_scale_f32 v52, vcc, 1.0, v25, 1.0
	v_fmac_f32_e32 v44, v53, v44
	v_mul_f32_e32 v53, v52, v44
	v_fma_f32 v54, -v40, v53, v52
	v_fmac_f32_e32 v53, v54, v44
	v_fma_f32 v40, -v40, v53, v52
	v_div_fmas_f32 v40, v40, v44, v53
	v_div_fixup_f32 v25, v40, v25, 1.0
	v_mul_f32_e32 v40, 0x3db504f3, v25
	v_pk_mul_f32 v[30:31], v[30:31], v[40:41] op_sel_hi:[1,0]
	v_add_u32_e32 v25, 1, v50
	v_cvt_pk_bf16_f32 v40, v30, v31
	v_add_f32_e32 v30, 1.0, v47
	v_rcp_f32_e32 v31, v30
	v_add_f32_e32 v30, 1.0, v49
	v_rcp_f32_e32 v30, v30
	v_fma_f32 v44, -v25, v50, v45
	v_cmp_lt_f32_e32 vcc, 0, v44
	s_or_b32 s5, s8, 5
	v_pk_mul_f32 v[30:31], v[22:23], v[30:31]
	v_cndmask_b32_e32 v25, v51, v25, vcc
	v_pk_mul_f32 v[22:23], v[30:31], v[30:31]
	v_mul_f32_e32 v44, 0x37800000, v25
	v_add_f32_e32 v22, v22, v23
	ds_swizzle_b32 v23, v22 offset:swizzle(SWAP,1)
	v_cndmask_b32_e64 v25, v25, v44, s[2:3]
	v_cmp_class_f32_e32 vcc, v45, v108
	v_and_b32_e32 v51, 0xffff0000, v82
	s_waitcnt lgkmcnt(0)
	v_add_f32_e32 v23, v22, v23
	ds_swizzle_b32 v44, v23 offset:swizzle(SWAP,2)
	v_cndmask_b32_e32 v25, v25, v45, vcc
	v_div_scale_f32 v45, s[2:3], v25, v25, 1.0
	v_rcp_f32_e32 v47, v45
	s_waitcnt lgkmcnt(0)
	v_add_f32_e32 v23, v23, v44
	ds_swizzle_b32 v44, v23 offset:swizzle(SWAP,4)
	v_add3_u32 v22, s9, v46, v48
	v_fma_f32 v46, -v45, v47, 1.0
	v_fmac_f32_e32 v47, v46, v47
	v_div_scale_f32 v46, vcc, 1.0, v25, 1.0
	s_waitcnt lgkmcnt(0)
	v_add_f32_e32 v23, v23, v44
	ds_swizzle_b32 v44, v23 offset:swizzle(SWAP,8)
	v_mul_f32_e32 v49, v46, v47
	v_fma_f32 v50, -v45, v49, v46
	v_fmac_f32_e32 v49, v50, v47
	v_fma_f32 v45, -v45, v49, v46
	s_waitcnt lgkmcnt(0)
	v_add_f32_e32 v23, v23, v44
	ds_swizzle_b32 v46, v23 offset:swizzle(SWAP,16)
	v_div_fmas_f32 v44, v45, v47, v49
	v_div_fixup_f32 v25, v44, v25, 1.0
	v_mul_f32_e32 v44, 0x3db504f3, v25
	v_pk_mul_f32 v[42:43], v[42:43], v[44:45] op_sel_hi:[1,0]
	s_waitcnt lgkmcnt(0)
	v_add_f32_e32 v23, v23, v46
	v_mov_b32_e32 v25, v23
	s_nop 1
	v_permlane32_swap_b32_e32 v23, v25
	v_add_f32_e32 v23, v23, v25
	v_add_f32_e32 v23, 0x358637bd, v23
	v_mul_f32_e32 v25, 0x4f800000, v23
	v_cmp_gt_f32_e32 vcc, s84, v23
	s_nop 1
	v_cndmask_b32_e32 v23, v23, v25, vcc
	v_sqrt_f32_e32 v44, v23
	v_cvt_pk_bf16_f32 v25, v42, v43
	v_bitop3_b32 v42, s10, v41, 4 bitop3:0x36
	v_lshlrev_b32_e32 v45, 4, v42
	v_add_u32_e32 v42, -1, v44
	v_fma_f32 v43, -v42, v44, v23
	v_cmp_ge_f32_e64 s[2:3], 0, v43
	v_add_u32_e32 v49, 1, v44
	s_nop 0
	v_cndmask_b32_e64 v46, v44, v42, s[2:3]
	v_pk_mul_f32 v[42:43], v[2:3], v[18:19]
	v_fma_f32 v44, -v49, v44, v23
	v_pk_fma_f32 v[20:21], v[4:5], v[20:21], v[42:43]
	v_cmp_lt_f32_e64 s[2:3], 0, v44
	v_pk_fma_f32 v[20:21], v[6:7], v[16:17], v[20:21]
	s_nop 0
	v_mul_f32_e32 v42, 0xbfb8aa3b, v21
	v_exp_f32_e32 v42, v42
	v_mul_f32_e32 v43, 0xbfb8aa3b, v20
	v_exp_f32_e32 v47, v43
	v_cndmask_b32_e64 v44, v46, v49, s[2:3]
	v_add_f32_e32 v42, 1.0, v42
	v_rcp_f32_e32 v43, v42
	v_add_f32_e32 v42, 1.0, v47
	v_rcp_f32_e32 v42, v42
	v_mul_f32_e32 v46, 0x37800000, v44
	v_cndmask_b32_e32 v44, v44, v46, vcc
	v_cmp_class_f32_e32 vcc, v23, v108
	v_pk_mul_f32 v[42:43], v[20:21], v[42:43]
	s_nop 0
	v_pk_mul_f32 v[20:21], v[42:43], v[42:43]
	v_cndmask_b32_e32 v23, v44, v23, vcc
	v_add_f32_e32 v20, v20, v21
	ds_swizzle_b32 v21, v20 offset:swizzle(SWAP,1)
	v_div_scale_f32 v46, s[2:3], v23, v23, 1.0
	v_rcp_f32_e32 v47, v46
	s_waitcnt lgkmcnt(0)
	v_add_f32_e32 v21, v20, v21
	ds_swizzle_b32 v44, v21 offset:swizzle(SWAP,2)
	v_add3_u32 v20, s9, v45, v48
	v_fma_f32 v45, -v46, v47, 1.0
	v_fmac_f32_e32 v47, v45, v47
	v_div_scale_f32 v45, vcc, 1.0, v23, 1.0
	s_waitcnt lgkmcnt(0)
	v_add_f32_e32 v21, v21, v44
	ds_swizzle_b32 v44, v21 offset:swizzle(SWAP,4)
	v_mul_f32_e32 v49, v45, v47
	v_fma_f32 v50, -v46, v49, v45
	v_fmac_f32_e32 v49, v50, v47
	v_fma_f32 v45, -v46, v49, v45
	s_waitcnt lgkmcnt(0)
	v_add_f32_e32 v21, v21, v44
	ds_swizzle_b32 v44, v21 offset:swizzle(SWAP,8)
	s_waitcnt lgkmcnt(0)
	v_add_f32_e32 v21, v21, v44
	ds_swizzle_b32 v46, v21 offset:swizzle(SWAP,16)
	v_div_fmas_f32 v44, v45, v47, v49
	v_div_fixup_f32 v23, v44, v23, 1.0
	v_mul_f32_e32 v44, 0x3db504f3, v23
	v_pk_mul_f32 v[30:31], v[30:31], v[44:45] op_sel_hi:[1,0]
	s_waitcnt lgkmcnt(0)
	v_add_f32_e32 v21, v21, v46
	v_mov_b32_e32 v23, v21
	s_nop 1
	v_permlane32_swap_b32_e32 v21, v23
	v_add_f32_e32 v21, v21, v23
	v_add_f32_e32 v21, 0x358637bd, v21
	v_mul_f32_e32 v23, 0x4f800000, v21
	v_cmp_gt_f32_e32 vcc, s84, v21
	v_cvt_pk_bf16_f32 v30, v30, v31
	v_bitop3_b32 v31, s10, v41, 8 bitop3:0x36
	v_cndmask_b32_e32 v21, v21, v23, vcc
	v_sqrt_f32_e32 v23, v21
	s_nop 0
	v_add_u32_e32 v44, -1, v23
	v_fma_f32 v45, -v44, v23, v21
	v_cmp_ge_f32_e64 s[2:3], 0, v45
	v_add_u32_e32 v47, 1, v23
	s_nop 0
	v_cndmask_b32_e64 v46, v23, v44, s[2:3]
	v_pk_mul_f32 v[44:45], v[2:3], v[16:17]
	v_fma_f32 v23, -v47, v23, v21
	v_pk_fma_f32 v[18:19], v[4:5], v[18:19], v[44:45]
	v_cmp_lt_f32_e64 s[2:3], 0, v23
	v_pk_fma_f32 v[18:19], v[6:7], v[14:15], v[18:19]
	s_nop 0
	v_mul_f32_e32 v44, 0xbfb8aa3b, v19
	v_exp_f32_e32 v44, v44
	v_mul_f32_e32 v45, 0xbfb8aa3b, v18
	v_exp_f32_e32 v49, v45
	v_cndmask_b32_e64 v23, v46, v47, s[2:3]
	v_add_f32_e32 v44, 1.0, v44
	v_rcp_f32_e32 v45, v44
	v_add_f32_e32 v44, 1.0, v49
	v_rcp_f32_e32 v44, v44
	v_mul_f32_e32 v46, 0x37800000, v23
	v_cndmask_b32_e32 v23, v23, v46, vcc
	v_cmp_class_f32_e32 vcc, v21, v108
	v_pk_mul_f32 v[44:45], v[18:19], v[44:45]
	s_nop 0
	v_pk_mul_f32 v[18:19], v[44:45], v[44:45]
	v_cndmask_b32_e32 v21, v23, v21, vcc
	v_add_f32_e32 v18, v18, v19
	ds_swizzle_b32 v19, v18 offset:swizzle(SWAP,1)
	v_div_scale_f32 v23, s[2:3], v21, v21, 1.0
	v_rcp_f32_e32 v46, v23
	s_waitcnt lgkmcnt(0)
	v_add_f32_e32 v18, v18, v19
	ds_swizzle_b32 v47, v18 offset:swizzle(SWAP,2)
	v_lshlrev_b32_e32 v19, 4, v31
	v_fma_f32 v31, -v23, v46, 1.0
	v_fmac_f32_e32 v46, v31, v46
	v_add3_u32 v19, s9, v19, v48
	s_waitcnt lgkmcnt(0)
	v_add_f32_e32 v18, v18, v47
	ds_swizzle_b32 v31, v18 offset:swizzle(SWAP,4)
	v_div_scale_f32 v47, vcc, 1.0, v21, 1.0
	v_mul_f32_e32 v49, v47, v46
	v_fma_f32 v50, -v23, v49, v47
	s_waitcnt lgkmcnt(0)
	v_add_f32_e32 v18, v18, v31
	ds_swizzle_b32 v31, v18 offset:swizzle(SWAP,8)
	v_fmac_f32_e32 v49, v50, v46
	v_fma_f32 v23, -v23, v49, v47
	v_div_fmas_f32 v23, v23, v46, v49
	s_waitcnt lgkmcnt(0)
	v_add_f32_e32 v31, v18, v31
	ds_swizzle_b32 v46, v31 offset:swizzle(SWAP,16)
	v_div_fixup_f32 v18, v23, v21, 1.0
	v_mul_f32_e32 v18, 0x3db504f3, v18
	v_pk_mul_f32 v[42:43], v[42:43], v[18:19] op_sel_hi:[1,0]
	s_waitcnt lgkmcnt(0)
	v_add_f32_e32 v18, v31, v46
	v_mov_b32_e32 v21, v18
	s_nop 1
	v_permlane32_swap_b32_e32 v18, v21
	v_add_f32_e32 v18, v18, v21
	v_add_f32_e32 v18, 0x358637bd, v18
	v_mul_f32_e32 v21, 0x4f800000, v18
	v_cmp_gt_f32_e32 vcc, s84, v18
	v_cvt_pk_bf16_f32 v23, v42, v43
	s_nop 0
	v_cndmask_b32_e32 v21, v18, v21, vcc
	v_sqrt_f32_e32 v31, v21
	v_bitop3_b32 v18, s10, v41, 12 bitop3:0x36
	v_lshlrev_b32_e32 v18, 4, v18
	v_add3_u32 v18, s9, v18, v48
	v_add_u32_e32 v42, -1, v31
	v_fma_f32 v43, -v42, v31, v21
	v_cmp_ge_f32_e64 s[2:3], 0, v43
	v_add_u32_e32 v43, 1, v31
	s_nop 0
	v_cndmask_b32_e64 v42, v31, v42, s[2:3]
	v_fma_f32 v31, -v43, v31, v21
	v_cmp_lt_f32_e64 s[2:3], 0, v31
	s_nop 1
	v_cndmask_b32_e64 v31, v42, v43, s[2:3]
	v_pk_mul_f32 v[42:43], v[2:3], v[14:15]
	v_mul_f32_e32 v47, 0x37800000, v31
	v_pk_fma_f32 v[16:17], v[4:5], v[16:17], v[42:43]
	v_cndmask_b32_e32 v31, v31, v47, vcc
	v_pk_fma_f32 v[16:17], v[6:7], v[8:9], v[16:17]
	v_cmp_class_f32_e32 vcc, v21, v108
	v_mul_f32_e32 v42, 0xbfb8aa3b, v17
	v_exp_f32_e32 v42, v42
	v_mul_f32_e32 v43, 0xbfb8aa3b, v16
	v_exp_f32_e32 v46, v43
	v_cndmask_b32_e32 v21, v31, v21, vcc
	v_add_f32_e32 v42, 1.0, v42
	v_rcp_f32_e32 v43, v42
	v_add_f32_e32 v42, 1.0, v46
	v_rcp_f32_e32 v42, v42
	v_div_scale_f32 v31, s[2:3], v21, v21, 1.0
	v_rcp_f32_e32 v46, v31
	v_pk_mul_f32 v[42:43], v[16:17], v[42:43]
	s_lshr_b32 s3, s4, 2
	v_pk_mul_f32 v[16:17], v[42:43], v[42:43]
	v_fma_f32 v47, -v31, v46, 1.0
	v_add_f32_e32 v16, v16, v17
	ds_swizzle_b32 v17, v16 offset:swizzle(SWAP,1)
	v_fmac_f32_e32 v46, v47, v46
	v_div_scale_f32 v47, vcc, 1.0, v21, 1.0
	v_mul_f32_e32 v49, v47, v46
	s_waitcnt lgkmcnt(0)
	v_add_f32_e32 v16, v16, v17
	ds_swizzle_b32 v17, v16 offset:swizzle(SWAP,2)
	v_fma_f32 v50, -v31, v49, v47
	v_fmac_f32_e32 v49, v50, v46
	v_fma_f32 v31, -v31, v49, v47
	s_lshl_b32 s2, s4, 8
	s_waitcnt lgkmcnt(0)
	v_add_f32_e32 v16, v16, v17
	ds_swizzle_b32 v17, v16 offset:swizzle(SWAP,4)
	s_add_i32 s2, s64, s2
	s_waitcnt lgkmcnt(0)
	v_add_f32_e32 v47, v16, v17
	ds_swizzle_b32 v50, v47 offset:swizzle(SWAP,8)
	v_div_fmas_f32 v16, v31, v46, v49
	v_div_fixup_f32 v16, v16, v21, 1.0
	v_mul_f32_e32 v16, 0x3db504f3, v16
	v_pk_mul_f32 v[16:17], v[44:45], v[16:17] op_sel_hi:[1,0]
	s_waitcnt lgkmcnt(0)
	v_add_f32_e32 v21, v47, v50
	ds_swizzle_b32 v44, v21 offset:swizzle(SWAP,16)
	v_cvt_pk_bf16_f32 v31, v16, v17
	s_waitcnt lgkmcnt(0)
	v_add_f32_e32 v16, v21, v44
	v_mov_b32_e32 v17, v16
	s_nop 1
	v_permlane32_swap_b32_e32 v16, v17
	v_add_f32_e32 v16, v16, v17
	v_add_f32_e32 v16, 0x358637bd, v16
	v_mul_f32_e32 v17, 0x4f800000, v16
	v_cmp_gt_f32_e32 vcc, s84, v16
	s_nop 1
	v_cndmask_b32_e32 v17, v16, v17, vcc
	v_sqrt_f32_e32 v21, v17
	v_bitop3_b32 v16, s3, v41, 3 bitop3:0x6c
	v_lshlrev_b32_e32 v16, 4, v16
	v_add3_u32 v16, s2, v16, v48
	v_add_u32_e32 v44, -1, v21
	v_fma_f32 v45, -v44, v21, v17
	v_cmp_ge_f32_e64 s[2:3], 0, v45
	v_add_u32_e32 v45, 1, v21
	s_nop 0
	v_cndmask_b32_e64 v44, v21, v44, s[2:3]
	v_fma_f32 v21, -v45, v21, v17
	v_cmp_lt_f32_e64 s[2:3], 0, v21
	s_nop 1
	v_cndmask_b32_e64 v21, v44, v45, s[2:3]
	v_pk_mul_f32 v[44:45], v[2:3], v[8:9]
	v_mul_f32_e32 v47, 0x37800000, v21
	v_pk_fma_f32 v[14:15], v[4:5], v[14:15], v[44:45]
	v_cndmask_b32_e32 v21, v21, v47, vcc
	v_pk_fma_f32 v[14:15], v[6:7], v[12:13], v[14:15]
	v_cmp_class_f32_e32 vcc, v17, v108
	v_mul_f32_e32 v44, 0xbfb8aa3b, v15
	v_exp_f32_e32 v44, v44
	v_mul_f32_e32 v45, 0xbfb8aa3b, v14
	v_exp_f32_e32 v46, v45
	v_cndmask_b32_e32 v17, v21, v17, vcc
	v_add_f32_e32 v44, 1.0, v44
	v_rcp_f32_e32 v45, v44
	v_add_f32_e32 v44, 1.0, v46
	v_rcp_f32_e32 v44, v44
	v_div_scale_f32 v21, s[2:3], v17, v17, 1.0
	v_rcp_f32_e32 v46, v21
	v_pk_mul_f32 v[44:45], v[14:15], v[44:45]
	v_pk_mul_f32 v[2:3], v[2:3], v[12:13]
	v_pk_mul_f32 v[14:15], v[44:45], v[44:45]
	v_fma_f32 v47, -v21, v46, 1.0
	v_add_f32_e32 v14, v14, v15
	ds_swizzle_b32 v15, v14 offset:swizzle(SWAP,1)
	v_fmac_f32_e32 v46, v47, v46
	v_div_scale_f32 v47, vcc, 1.0, v17, 1.0
	v_mul_f32_e32 v49, v47, v46
	s_waitcnt lgkmcnt(0)
	v_add_f32_e32 v14, v14, v15
	ds_swizzle_b32 v15, v14 offset:swizzle(SWAP,2)
	v_fma_f32 v50, -v21, v49, v47
	v_fmac_f32_e32 v49, v50, v46
	v_fma_f32 v21, -v21, v49, v47
	v_pk_fma_f32 v[2:3], v[4:5], v[8:9], v[2:3]
	s_waitcnt lgkmcnt(0)
	v_add_f32_e32 v14, v14, v15
	ds_swizzle_b32 v15, v14 offset:swizzle(SWAP,4)
	v_pk_fma_f32 v[2:3], v[6:7], v[10:11], v[2:3]
	s_lshl_b32 s2, s5, 8
	v_mul_f32_e32 v4, 0xbfb8aa3b, v3
	v_exp_f32_e32 v4, v4
	s_waitcnt lgkmcnt(0)
	v_add_f32_e32 v15, v14, v15
	ds_swizzle_b32 v47, v15 offset:swizzle(SWAP,8)
	v_div_fmas_f32 v14, v21, v46, v49
	v_div_fixup_f32 v14, v14, v17, 1.0
	v_mul_f32_e32 v5, 0xbfb8aa3b, v2
	v_exp_f32_e32 v6, v5
	s_waitcnt lgkmcnt(0)
	v_add_f32_e32 v17, v15, v47
	ds_swizzle_b32 v21, v17 offset:swizzle(SWAP,16)
	v_mul_f32_e32 v14, 0x3db504f3, v14
	v_pk_mul_f32 v[14:15], v[42:43], v[14:15] op_sel_hi:[1,0]
	v_add_f32_e32 v4, 1.0, v4
	v_cvt_pk_bf16_f32 v15, v14, v15
	s_waitcnt lgkmcnt(0)
	v_add_f32_e32 v14, v17, v21
	v_mov_b32_e32 v17, v14
	v_rcp_f32_e32 v5, v4
	v_add_f32_e32 v4, 1.0, v6
	v_permlane32_swap_b32_e32 v14, v17
	v_rcp_f32_e32 v4, v4
	v_add_f32_e32 v14, v14, v17
	v_add_f32_e32 v14, 0x358637bd, v14
	v_mul_f32_e32 v17, 0x4f800000, v14
	v_cmp_gt_f32_e32 vcc, s84, v14
	v_pk_mul_f32 v[2:3], v[2:3], v[4:5]
	s_add_i32 s9, s64, s2
	v_cndmask_b32_e32 v14, v14, v17, vcc
	v_sqrt_f32_e32 v17, v14
	v_pk_mul_f32 v[4:5], v[2:3], v[2:3]
	s_bfe_u32 s2, s5, 0x20002
	v_add_f32_e32 v4, v4, v5
	ds_swizzle_b32 v5, v4 offset:swizzle(SWAP,1)
	v_add_u32_e32 v42, -1, v17
	v_fma_f32 v43, -v42, v17, v14
	v_bitop3_b32 v21, s2, v41, 4 bitop3:0x36
	v_cmp_ge_f32_e64 s[2:3], 0, v43
	v_add_u32_e32 v43, 1, v17
	v_fma_f32 v7, -v43, v17, v14
	s_waitcnt lgkmcnt(0)
	v_add_f32_e32 v4, v4, v5
	v_cndmask_b32_e64 v42, v17, v42, s[2:3]
	v_cmp_lt_f32_e64 s[2:3], 0, v7
	ds_swizzle_b32 v5, v4 offset:swizzle(SWAP,2)
	v_lshlrev_b32_e32 v21, 4, v21
	v_cndmask_b32_e64 v6, v42, v43, s[2:3]
	v_mul_f32_e32 v7, 0x37800000, v6
	v_cndmask_b32_e32 v6, v6, v7, vcc
	v_cmp_class_f32_e32 vcc, v14, v108
	s_waitcnt lgkmcnt(0)
	v_add_f32_e32 v4, v4, v5
	ds_swizzle_b32 v5, v4 offset:swizzle(SWAP,4)
	v_cndmask_b32_e32 v6, v6, v14, vcc
	v_div_scale_f32 v7, s[2:3], v6, v6, 1.0
	v_rcp_f32_e32 v8, v7
	s_waitcnt lgkmcnt(0)
	v_add_f32_e32 v4, v4, v5
	ds_swizzle_b32 v5, v4 offset:swizzle(SWAP,8)
	v_add3_u32 v13, s9, v21, v48
	v_fma_f32 v9, -v7, v8, 1.0
	v_fmac_f32_e32 v8, v9, v8
	v_div_scale_f32 v9, vcc, 1.0, v6, 1.0
	v_mul_f32_e32 v10, v9, v8
	v_fma_f32 v11, -v7, v10, v9
	v_fmac_f32_e32 v10, v11, v8
	v_fma_f32 v7, -v7, v10, v9
	v_div_fmas_f32 v7, v7, v8, v10
	v_div_fixup_f32 v6, v7, v6, 1.0
	s_waitcnt lgkmcnt(0)
	v_add_f32_e32 v7, v4, v5
	ds_swizzle_b32 v8, v7 offset:swizzle(SWAP,16)
	v_mul_f32_e32 v4, 0x3db504f3, v6
	v_pk_mul_f32 v[4:5], v[44:45], v[4:5] op_sel_hi:[1,0]
	s_or_b32 s9, s8, 6
	v_cvt_pk_bf16_f32 v17, v4, v5
	s_waitcnt lgkmcnt(0)
	v_add_f32_e32 v4, v7, v8
	v_mov_b32_e32 v5, v4
	s_nop 1
	v_permlane32_swap_b32_e32 v4, v5
	v_add_f32_e32 v4, v4, v5
	v_add_f32_e32 v4, 0x358637bd, v4
	v_mul_f32_e32 v5, 0x4f800000, v4
	v_cmp_gt_f32_e32 vcc, s84, v4
	s_lshl_b32 s2, s9, 8
	s_add_i32 s10, s64, s2
	v_cndmask_b32_e32 v4, v4, v5, vcc
	v_sqrt_f32_e32 v5, v4
	s_bfe_u32 s2, s9, 0x20002
	v_bitop3_b32 v6, s2, v41, 8 bitop3:0x36
	v_lshlrev_b32_e32 v42, 16, v79
	v_add_u32_e32 v7, -1, v5
	v_fma_f32 v8, -v7, v5, v4
	v_cmp_ge_f32_e64 s[2:3], 0, v8
	v_add_u32_e32 v8, 1, v5
	v_and_b32_e32 v43, 0xffff0000, v79
	v_cndmask_b32_e64 v7, v5, v7, s[2:3]
	v_fma_f32 v5, -v8, v5, v4
	v_cmp_lt_f32_e64 s[2:3], 0, v5
	v_lshlrev_b32_e32 v44, 16, v80
	v_and_b32_e32 v45, 0xffff0000, v80
	v_cndmask_b32_e64 v5, v7, v8, s[2:3]
	v_mul_f32_e32 v7, 0x37800000, v5
	v_cndmask_b32_e32 v5, v5, v7, vcc
	v_cmp_class_f32_e32 vcc, v4, v108
	s_waitcnt vmcnt(4)
	v_pk_mul_f32 v[52:53], v[34:35], v[44:45]
	v_and_b32_e32 v49, 0xffff0000, v81
	v_cndmask_b32_e32 v8, v5, v4, vcc
	v_div_scale_f32 v4, s[2:3], v8, v8, 1.0
	v_rcp_f32_e32 v9, v4
	v_lshlrev_b32_e32 v5, 4, v6
	v_add3_u32 v12, s10, v5, v48
	s_or_b32 s10, s8, 7
	v_fma_f32 v5, -v4, v9, 1.0
	v_fmac_f32_e32 v9, v5, v9
	v_div_scale_f32 v5, vcc, 1.0, v8, 1.0
	v_mul_f32_e32 v10, v5, v9
	v_fma_f32 v6, -v4, v10, v5
	v_fmac_f32_e32 v10, v6, v9
	v_fma_f32 v11, -v4, v10, v5
	v_lshlrev_b32_e32 v4, 16, v78
	v_and_b32_e32 v5, 0xffff0000, v78
	v_pk_mul_f32 v[6:7], v[34:35], v[42:43]
	v_div_fmas_f32 v9, v11, v9, v10
	s_waitcnt vmcnt(3)
	v_pk_fma_f32 v[4:5], v[32:33], v[4:5], v[6:7]
	v_div_fixup_f32 v8, v9, v8, 1.0
	s_waitcnt vmcnt(2)
	v_pk_fma_f32 v[4:5], v[36:37], v[44:45], v[4:5]
	v_mul_f32_e32 v8, 0x3db504f3, v8
	v_mul_f32_e32 v6, 0xbfb8aa3b, v5
	v_exp_f32_e32 v6, v6
	v_mul_f32_e32 v7, 0xbfb8aa3b, v4
	v_exp_f32_e32 v14, v7
	v_pk_mul_f32 v[2:3], v[2:3], v[8:9] op_sel_hi:[1,0]
	v_add_f32_e32 v6, 1.0, v6
	v_rcp_f32_e32 v7, v6
	v_add_f32_e32 v6, 1.0, v14
	v_rcp_f32_e32 v6, v6
	v_cvt_pk_bf16_f32 v21, v2, v3
	s_bfe_u32 s3, s10, 0x20002
	s_lshl_b32 s2, s10, 8
	v_pk_mul_f32 v[46:47], v[4:5], v[6:7]
	s_add_i32 s2, s64, s2
	v_pk_mul_f32 v[4:5], v[46:47], v[46:47]
	v_pk_fma_f32 v[42:43], v[32:33], v[42:43], v[52:53]
	v_add_f32_e32 v4, v4, v5
	ds_swizzle_b32 v5, v4 offset:swizzle(SWAP,1)
	v_lshlrev_b32_e32 v50, 16, v82
	v_lshlrev_b32_e32 v10, 16, v83
	v_and_b32_e32 v11, 0xffff0000, v83
	v_lshlrev_b32_e32 v8, 16, v86
	s_waitcnt lgkmcnt(0)
	v_add_f32_e32 v2, v4, v5
	ds_swizzle_b32 v3, v2 offset:swizzle(SWAP,2)
	v_bitop3_b32 v4, s3, v41, 12 bitop3:0x36
	v_lshlrev_b32_e32 v4, 4, v4
	v_add3_u32 v14, s2, v4, v48
	v_lshlrev_b32_e32 v48, 16, v81
	s_waitcnt lgkmcnt(0)
	v_add_f32_e32 v2, v2, v3
	v_pk_fma_f32 v[42:43], v[36:37], v[48:49], v[42:43]
	ds_swizzle_b32 v3, v2 offset:swizzle(SWAP,4)
	v_mul_f32_e32 v52, 0xbfb8aa3b, v43
	v_exp_f32_e32 v52, v52
	v_mul_f32_e32 v53, 0xbfb8aa3b, v42
	v_exp_f32_e32 v54, v53
	s_waitcnt lgkmcnt(0)
	v_add_f32_e32 v5, v2, v3
	v_add_f32_e32 v52, 1.0, v52
	ds_swizzle_b32 v6, v5 offset:swizzle(SWAP,8)
	v_rcp_f32_e32 v53, v52
	v_add_f32_e32 v52, 1.0, v54
	v_rcp_f32_e32 v52, v52
	v_lshlrev_b32_e32 v2, 16, v84
	s_waitcnt lgkmcnt(0)
	v_add_f32_e32 v7, v5, v6
	ds_swizzle_b32 v41, v7 offset:swizzle(SWAP,16)
	v_pk_mul_f32 v[42:43], v[42:43], v[52:53]
	v_and_b32_e32 v3, 0xffff0000, v84
	v_pk_mul_f32 v[52:53], v[42:43], v[42:43]
	v_lshlrev_b32_e32 v4, 16, v85
	v_add_f32_e32 v52, v52, v53
	ds_swizzle_b32 v53, v52 offset:swizzle(SWAP,1)
	s_waitcnt lgkmcnt(1)
	v_add_f32_e32 v7, v7, v41
	v_mov_b32_e32 v41, v7
	s_nop 1
	v_permlane32_swap_b32_e32 v7, v41
	s_waitcnt lgkmcnt(0)
	v_add_f32_e32 v52, v52, v53
	v_add_f32_e32 v7, v7, v41
	ds_swizzle_b32 v53, v52 offset:swizzle(SWAP,2)
	v_add_f32_e32 v7, 0x358637bd, v7
	v_mul_f32_e32 v41, 0x4f800000, v7
	v_cmp_gt_f32_e32 vcc, s84, v7
	v_and_b32_e32 v5, 0xffff0000, v85
	s_waitcnt lgkmcnt(0)
	v_add_f32_e32 v52, v52, v53
	v_cndmask_b32_e32 v7, v7, v41, vcc
	v_sqrt_f32_e32 v41, v7
	ds_swizzle_b32 v53, v52 offset:swizzle(SWAP,4)
	v_and_b32_e32 v9, 0xffff0000, v86
	v_lshlrev_b32_e32 v6, 16, v87
	v_add_u32_e32 v55, -1, v41
	v_fma_f32 v54, -v55, v41, v7
	v_cmp_ge_f32_e64 s[2:3], 0, v54
	s_waitcnt lgkmcnt(0)
	v_add_f32_e32 v52, v52, v53
	ds_swizzle_b32 v53, v52 offset:swizzle(SWAP,8)
	v_cndmask_b32_e64 v54, v41, v55, s[2:3]
	v_add_u32_e32 v55, 1, v41
	v_fma_f32 v41, -v55, v41, v7
	v_cmp_lt_f32_e64 s[2:3], 0, v41
	s_waitcnt lgkmcnt(0)
	v_add_f32_e32 v52, v52, v53
	ds_swizzle_b32 v53, v52 offset:swizzle(SWAP,16)
	v_cndmask_b32_e64 v41, v54, v55, s[2:3]
	v_mul_f32_e32 v54, 0x37800000, v41
	v_cndmask_b32_e32 v41, v41, v54, vcc
	v_cmp_class_f32_e32 vcc, v7, v108
	s_waitcnt lgkmcnt(0)
	v_add_f32_e32 v52, v52, v53
	v_mov_b32_e32 v53, v52
	v_cndmask_b32_e32 v41, v41, v7, vcc
	v_div_scale_f32 v54, s[2:3], v41, v41, 1.0
	v_rcp_f32_e32 v55, v54
	v_permlane32_swap_b32_e32 v52, v53
	v_add_f32_e32 v52, v52, v53
	v_fma_f32 v56, -v54, v55, 1.0
	v_fmac_f32_e32 v55, v56, v55
	v_div_scale_f32 v56, vcc, 1.0, v41, 1.0
	v_mul_f32_e32 v57, v56, v55
	v_fma_f32 v58, -v54, v57, v56
	v_fmac_f32_e32 v57, v58, v55
	v_add_f32_e32 v52, 0x358637bd, v52
	v_fma_f32 v54, -v54, v57, v56
	v_mul_f32_e32 v53, 0x4f800000, v52
	v_cmp_gt_f32_e64 s[2:3], s84, v52
	v_and_b32_e32 v7, 0xffff0000, v87
	s_cmp_eq_u32 s48, 5
	v_cndmask_b32_e64 v56, v52, v53, s[2:3]
	v_div_fmas_f32 v52, v54, v55, v57
	v_div_fixup_f32 v52, v52, v41, 1.0
	v_pk_mul_f32 v[46:47], v[46:47], v[52:53] op_sel_hi:[1,0]
	v_pk_mul_f32 v[52:53], v[34:35], v[48:49]
	v_sqrt_f32_e32 v58, v56
	v_pk_fma_f32 v[44:45], v[32:33], v[44:45], v[52:53]
	v_cvt_pk_bf16_f32 v46, v46, v47
	v_pk_fma_f32 v[44:45], v[36:37], v[50:51], v[44:45]
	v_add_u32_e32 v41, -1, v58
	v_mul_f32_e32 v52, 0xbfb8aa3b, v45
	v_exp_f32_e32 v52, v52
	v_mul_f32_e32 v53, 0xbfb8aa3b, v44
	v_exp_f32_e32 v54, v53
	v_fma_f32 v55, -v41, v58, v56
	v_add_f32_e32 v52, 1.0, v52
	v_rcp_f32_e32 v53, v52
	v_add_f32_e32 v52, 1.0, v54
	v_rcp_f32_e32 v52, v52
	v_add_u32_e32 v54, 1, v58
	v_cmp_ge_f32_e32 vcc, 0, v55
	v_fma_f32 v55, -v54, v58, v56
	v_pk_mul_f32 v[44:45], v[44:45], v[52:53]
	v_cndmask_b32_e32 v41, v58, v41, vcc
	v_pk_mul_f32 v[52:53], v[44:45], v[44:45]
	v_cmp_lt_f32_e32 vcc, 0, v55
	v_add_f32_e32 v52, v52, v53
	ds_swizzle_b32 v53, v52 offset:swizzle(SWAP,1)
	v_cndmask_b32_e32 v41, v41, v54, vcc
	v_mul_f32_e32 v54, 0x37800000, v41
	v_cndmask_b32_e64 v41, v41, v54, s[2:3]
	v_cmp_class_f32_e32 vcc, v56, v108
	s_waitcnt lgkmcnt(0)
	v_add_f32_e32 v52, v52, v53
	ds_swizzle_b32 v53, v52 offset:swizzle(SWAP,2)
	v_cndmask_b32_e32 v41, v41, v56, vcc
	v_div_scale_f32 v54, s[2:3], v41, v41, 1.0
	v_rcp_f32_e32 v55, v54
	s_waitcnt lgkmcnt(0)
	v_add_f32_e32 v52, v52, v53
	ds_swizzle_b32 v53, v52 offset:swizzle(SWAP,4)
	ds_write2st64_b32 v22, v46, v40 offset1:64
	v_fma_f32 v40, -v54, v55, 1.0
	v_fmac_f32_e32 v55, v40, v55
	v_div_scale_f32 v47, vcc, 1.0, v41, 1.0
	s_waitcnt lgkmcnt(1)
	v_add_f32_e32 v40, v52, v53
	ds_swizzle_b32 v46, v40 offset:swizzle(SWAP,8)
	v_mul_f32_e32 v52, v47, v55
	v_fma_f32 v53, -v54, v52, v47
	v_fmac_f32_e32 v52, v53, v55
	v_fma_f32 v47, -v54, v52, v47
	s_waitcnt lgkmcnt(0)
	v_add_f32_e32 v40, v40, v46
	ds_swizzle_b32 v46, v40 offset:swizzle(SWAP,16)
	v_div_fmas_f32 v47, v47, v55, v52
	s_waitcnt lgkmcnt(0)
	v_add_f32_e32 v40, v40, v46
	v_mov_b32_e32 v46, v40
	s_nop 1
	v_permlane32_swap_b32_e32 v40, v46
	v_add_f32_e32 v40, v40, v46
	v_add_f32_e32 v40, 0x358637bd, v40
	v_mul_f32_e32 v46, 0x4f800000, v40
	v_cmp_gt_f32_e32 vcc, s84, v40
	s_nop 1
	v_cndmask_b32_e32 v46, v40, v46, vcc
	v_sqrt_f32_e32 v52, v46
	v_div_fixup_f32 v40, v47, v41, 1.0
	v_pk_mul_f32 v[40:41], v[42:43], v[40:41] op_sel_hi:[1,0]
	s_nop 0
	v_cvt_pk_bf16_f32 v47, v40, v41
	v_add_u32_e32 v40, -1, v52
	v_fma_f32 v41, -v40, v52, v46
	v_cmp_ge_f32_e64 s[2:3], 0, v41
	ds_write2st64_b32 v20, v47, v25 offset0:1 offset1:65
	s_nop 0
	v_cndmask_b32_e64 v53, v52, v40, s[2:3]
	v_pk_mul_f32 v[40:41], v[34:35], v[50:51]
	s_nop 0
	v_pk_fma_f32 v[40:41], v[32:33], v[48:49], v[40:41]
	v_add_u32_e32 v49, 1, v52
	v_pk_fma_f32 v[40:41], v[36:37], v[10:11], v[40:41]
	s_nop 0
	v_mul_f32_e32 v42, 0xbfb8aa3b, v41
	v_exp_f32_e32 v42, v42
	v_mul_f32_e32 v43, 0xbfb8aa3b, v40
	v_exp_f32_e32 v48, v43
	v_add_f32_e32 v42, 1.0, v42
	v_rcp_f32_e32 v43, v42
	v_add_f32_e32 v42, 1.0, v48
	v_rcp_f32_e32 v42, v42
	v_fma_f32 v48, -v49, v52, v46
	v_cmp_lt_f32_e64 s[2:3], 0, v48
	v_pk_mul_f32 v[40:41], v[40:41], v[42:43]
	s_nop 0
	v_pk_mul_f32 v[42:43], v[40:41], v[40:41]
	v_cndmask_b32_e64 v48, v53, v49, s[2:3]
	v_add_f32_e32 v42, v42, v43
	ds_swizzle_b32 v43, v42 offset:swizzle(SWAP,1)
	v_mul_f32_e32 v49, 0x37800000, v48
	v_cndmask_b32_e32 v48, v48, v49, vcc
	v_cmp_class_f32_e32 vcc, v46, v108
	s_waitcnt lgkmcnt(0)
	v_add_f32_e32 v42, v42, v43
	ds_swizzle_b32 v43, v42 offset:swizzle(SWAP,2)
	v_cndmask_b32_e32 v46, v48, v46, vcc
	v_div_scale_f32 v48, s[2:3], v46, v46, 1.0
	v_rcp_f32_e32 v49, v48
	s_waitcnt lgkmcnt(0)
	v_add_f32_e32 v25, v42, v43
	ds_swizzle_b32 v42, v25 offset:swizzle(SWAP,4)
	v_fma_f32 v43, -v48, v49, 1.0
	v_fmac_f32_e32 v49, v43, v49
	v_div_scale_f32 v43, vcc, 1.0, v46, 1.0
	s_waitcnt lgkmcnt(0)
	v_add_f32_e32 v25, v25, v42
	ds_swizzle_b32 v42, v25 offset:swizzle(SWAP,8)
	v_mul_f32_e32 v47, v43, v49
	v_fma_f32 v52, -v48, v47, v43
	v_fmac_f32_e32 v47, v52, v49
	v_fma_f32 v43, -v48, v47, v43
	s_waitcnt lgkmcnt(0)
	v_add_f32_e32 v25, v25, v42
	ds_swizzle_b32 v48, v25 offset:swizzle(SWAP,16)
	v_div_fmas_f32 v42, v43, v49, v47
	v_div_fixup_f32 v42, v42, v46, 1.0
	v_pk_mul_f32 v[42:43], v[44:45], v[42:43] op_sel_hi:[1,0]
	s_waitcnt lgkmcnt(0)
	v_add_f32_e32 v25, v25, v48
	v_cvt_pk_bf16_f32 v46, v42, v43
	v_mov_b32_e32 v42, v25
	s_nop 1
	v_permlane32_swap_b32_e32 v25, v42
	v_add_f32_e32 v25, v25, v42
	v_add_f32_e32 v25, 0x358637bd, v25
	v_mul_f32_e32 v42, 0x4f800000, v25
	v_cmp_gt_f32_e32 vcc, s84, v25
	ds_write2st64_b32 v19, v46, v30 offset0:2 offset1:66
	s_nop 0
	v_cndmask_b32_e32 v25, v25, v42, vcc
	v_pk_mul_f32 v[42:43], v[34:35], v[10:11]
	v_sqrt_f32_e32 v47, v25
	v_pk_fma_f32 v[42:43], v[32:33], v[50:51], v[42:43]
	v_add_u32_e32 v49, -1, v47
	v_pk_fma_f32 v[42:43], v[36:37], v[2:3], v[42:43]
	s_nop 0
	v_mul_f32_e32 v44, 0xbfb8aa3b, v43
	v_exp_f32_e32 v44, v44
	v_mul_f32_e32 v45, 0xbfb8aa3b, v42
	v_exp_f32_e32 v48, v45
	v_add_f32_e32 v44, 1.0, v44
	v_rcp_f32_e32 v45, v44
	v_add_f32_e32 v44, 1.0, v48
	v_rcp_f32_e32 v44, v44
	v_fma_f32 v48, -v49, v47, v25
	v_cmp_ge_f32_e64 s[2:3], 0, v48
	v_pk_mul_f32 v[42:43], v[42:43], v[44:45]
	s_nop 0
	v_pk_mul_f32 v[44:45], v[42:43], v[42:43]
	v_cndmask_b32_e64 v48, v47, v49, s[2:3]
	v_add_f32_e32 v44, v44, v45
	ds_swizzle_b32 v45, v44 offset:swizzle(SWAP,1)
	v_add_u32_e32 v49, 1, v47
	v_fma_f32 v47, -v49, v47, v25
	v_cmp_lt_f32_e64 s[2:3], 0, v47
	s_waitcnt lgkmcnt(0)
	v_add_f32_e32 v44, v44, v45
	ds_swizzle_b32 v45, v44 offset:swizzle(SWAP,2)
	v_cndmask_b32_e64 v47, v48, v49, s[2:3]
	v_mul_f32_e32 v48, 0x37800000, v47
	v_cndmask_b32_e32 v47, v47, v48, vcc
	v_cmp_class_f32_e32 vcc, v25, v108
	s_waitcnt lgkmcnt(0)
	v_add_f32_e32 v44, v44, v45
	ds_swizzle_b32 v45, v44 offset:swizzle(SWAP,4)
	v_cndmask_b32_e32 v25, v47, v25, vcc
	v_div_scale_f32 v47, s[2:3], v25, v25, 1.0
	v_rcp_f32_e32 v48, v47
	s_waitcnt lgkmcnt(0)
	v_add_f32_e32 v30, v44, v45
	ds_swizzle_b32 v44, v30 offset:swizzle(SWAP,8)
	v_fma_f32 v45, -v47, v48, 1.0
	v_fmac_f32_e32 v48, v45, v48
	v_div_scale_f32 v45, vcc, 1.0, v25, 1.0
	s_waitcnt lgkmcnt(0)
	v_add_f32_e32 v30, v30, v44
	ds_swizzle_b32 v44, v30 offset:swizzle(SWAP,16)
	v_mul_f32_e32 v46, v45, v48
	v_fma_f32 v49, -v47, v46, v45
	v_fmac_f32_e32 v46, v49, v48
	v_fma_f32 v45, -v47, v46, v45
	s_waitcnt lgkmcnt(0)
	v_add_f32_e32 v30, v30, v44
	v_mov_b32_e32 v44, v30
	s_nop 1
	v_permlane32_swap_b32_e32 v30, v44
	v_add_f32_e32 v30, v30, v44
	v_add_f32_e32 v30, 0x358637bd, v30
	v_mul_f32_e32 v44, 0x4f800000, v30
	v_cmp_gt_f32_e64 s[2:3], s84, v30
	s_nop 1
	v_cndmask_b32_e64 v47, v30, v44, s[2:3]
	v_div_fmas_f32 v30, v45, v48, v46
	v_pk_mul_f32 v[44:45], v[34:35], v[2:3]
	v_div_fixup_f32 v30, v30, v25, 1.0
	v_pk_fma_f32 v[10:11], v[32:33], v[10:11], v[44:45]
	v_pk_mul_f32 v[40:41], v[40:41], v[30:31] op_sel_hi:[1,0]
	v_pk_fma_f32 v[10:11], v[36:37], v[4:5], v[10:11]
	v_sqrt_f32_e32 v49, v47
	v_mul_f32_e32 v30, 0xbfb8aa3b, v11
	v_exp_f32_e32 v30, v30
	v_mul_f32_e32 v44, 0xbfb8aa3b, v10
	v_exp_f32_e32 v44, v44
	v_add_u32_e32 v25, -1, v49
	v_add_f32_e32 v30, 1.0, v30
	v_rcp_f32_e32 v45, v30
	v_add_f32_e32 v30, 1.0, v44
	v_rcp_f32_e32 v44, v30
	v_fma_f32 v46, -v25, v49, v47
	v_add_u32_e32 v30, 1, v49
	v_cmp_ge_f32_e32 vcc, 0, v46
	v_pk_mul_f32 v[10:11], v[10:11], v[44:45]
	v_fma_f32 v46, -v30, v49, v47
	v_pk_mul_f32 v[44:45], v[10:11], v[10:11]
	v_cndmask_b32_e32 v25, v49, v25, vcc
	v_add_f32_e32 v44, v44, v45
	ds_swizzle_b32 v45, v44 offset:swizzle(SWAP,1)
	v_cmp_lt_f32_e32 vcc, 0, v46
	v_cvt_pk_bf16_f32 v40, v40, v41
	ds_write2st64_b32 v18, v40, v23 offset0:3 offset1:67
	v_cndmask_b32_e32 v25, v25, v30, vcc
	v_mul_f32_e32 v30, 0x37800000, v25
	v_cndmask_b32_e64 v25, v25, v30, s[2:3]
	s_waitcnt lgkmcnt(1)
	v_add_f32_e32 v30, v44, v45
	ds_swizzle_b32 v44, v30 offset:swizzle(SWAP,2)
	v_cmp_class_f32_e32 vcc, v47, v108
	s_waitcnt lgkmcnt(0)
	v_add_f32_e32 v30, v30, v44
	v_cndmask_b32_e32 v25, v25, v47, vcc
	v_div_scale_f32 v45, s[2:3], v25, v25, 1.0
	v_rcp_f32_e32 v46, v45
	ds_swizzle_b32 v44, v30 offset:swizzle(SWAP,4)
	v_div_scale_f32 v40, vcc, 1.0, v25, 1.0
	v_fma_f32 v23, -v45, v46, 1.0
	v_fmac_f32_e32 v46, v23, v46
	s_waitcnt lgkmcnt(0)
	v_add_f32_e32 v23, v30, v44
	ds_swizzle_b32 v30, v23 offset:swizzle(SWAP,8)
	v_mul_f32_e32 v41, v40, v46
	v_fma_f32 v44, -v45, v41, v40
	v_fmac_f32_e32 v41, v44, v46
	v_fma_f32 v40, -v45, v41, v40
	s_waitcnt lgkmcnt(0)
	v_add_f32_e32 v23, v23, v30
	ds_swizzle_b32 v30, v23 offset:swizzle(SWAP,16)
	v_div_fmas_f32 v40, v40, v46, v41
	s_waitcnt lgkmcnt(0)
	v_add_f32_e32 v23, v23, v30
	v_mov_b32_e32 v30, v23
	s_nop 1
	v_permlane32_swap_b32_e32 v23, v30
	v_add_f32_e32 v23, v23, v30
	v_add_f32_e32 v23, 0x358637bd, v23
	v_mul_f32_e32 v30, 0x4f800000, v23
	v_cmp_gt_f32_e32 vcc, s84, v23
	s_nop 1
	v_cndmask_b32_e32 v23, v23, v30, vcc
	v_sqrt_f32_e32 v44, v23
	v_div_fixup_f32 v30, v40, v25, 1.0
	v_pk_mul_f32 v[40:41], v[42:43], v[30:31] op_sel_hi:[1,0]
	v_add_u32_e32 v30, -1, v44
	v_cvt_pk_bf16_f32 v25, v40, v41
	v_fma_f32 v40, -v30, v44, v23
	v_cmp_ge_f32_e64 s[2:3], 0, v40
	v_pk_mul_f32 v[40:41], v[34:35], v[4:5]
	v_add_u32_e32 v43, 1, v44
	v_pk_fma_f32 v[2:3], v[32:33], v[2:3], v[40:41]
	v_cndmask_b32_e64 v30, v44, v30, s[2:3]
	v_pk_fma_f32 v[2:3], v[36:37], v[8:9], v[2:3]
	ds_write2st64_b32 v16, v25, v31 offset1:64
	v_mul_f32_e32 v40, 0xbfb8aa3b, v3
	v_exp_f32_e32 v40, v40
	v_mul_f32_e32 v41, 0xbfb8aa3b, v2
	v_exp_f32_e32 v42, v41
	v_pk_mul_f32 v[8:9], v[34:35], v[8:9]
	v_add_f32_e32 v40, 1.0, v40
	v_rcp_f32_e32 v41, v40
	v_add_f32_e32 v40, 1.0, v42
	v_rcp_f32_e32 v40, v40
	v_fma_f32 v42, -v43, v44, v23
	v_cmp_lt_f32_e64 s[2:3], 0, v42
	v_pk_fma_f32 v[4:5], v[32:33], v[4:5], v[8:9]
	v_pk_mul_f32 v[2:3], v[2:3], v[40:41]
	v_cndmask_b32_e64 v30, v30, v43, s[2:3]
	v_pk_mul_f32 v[40:41], v[2:3], v[2:3]
	v_mul_f32_e32 v42, 0x37800000, v30
	v_add_f32_e32 v40, v40, v41
	ds_swizzle_b32 v41, v40 offset:swizzle(SWAP,1)
	v_cndmask_b32_e32 v30, v30, v42, vcc
	v_cmp_class_f32_e32 vcc, v23, v108
	v_pk_fma_f32 v[4:5], v[36:37], v[6:7], v[4:5]
	v_lshlrev_b32_e32 v36, 16, v89
	v_cndmask_b32_e32 v23, v30, v23, vcc
	s_waitcnt lgkmcnt(0)
	v_add_f32_e32 v30, v40, v41
	ds_swizzle_b32 v40, v30 offset:swizzle(SWAP,2)
	v_div_scale_f32 v41, s[2:3], v23, v23, 1.0
	v_rcp_f32_e32 v42, v41
	v_mul_f32_e32 v6, 0xbfb8aa3b, v5
	s_waitcnt lgkmcnt(0)
	v_add_f32_e32 v25, v30, v40
	ds_swizzle_b32 v30, v25 offset:swizzle(SWAP,4)
	v_fma_f32 v31, -v41, v42, 1.0
	v_fmac_f32_e32 v42, v31, v42
	v_div_scale_f32 v31, vcc, 1.0, v23, 1.0
	s_waitcnt lgkmcnt(0)
	v_add_f32_e32 v25, v25, v30
	ds_swizzle_b32 v30, v25 offset:swizzle(SWAP,8)
	v_mul_f32_e32 v40, v31, v42
	v_fma_f32 v43, -v41, v40, v31
	v_fmac_f32_e32 v40, v43, v42
	v_fma_f32 v31, -v41, v40, v31
	s_waitcnt lgkmcnt(0)
	v_add_f32_e32 v25, v25, v30
	ds_swizzle_b32 v41, v25 offset:swizzle(SWAP,16)
	v_div_fmas_f32 v30, v31, v42, v40
	v_div_fixup_f32 v30, v30, v23, 1.0
	v_pk_mul_f32 v[10:11], v[10:11], v[30:31] op_sel_hi:[1,0]
	v_exp_f32_e32 v6, v6
	v_cvt_pk_bf16_f32 v10, v10, v11
	s_waitcnt lgkmcnt(0)
	v_add_f32_e32 v11, v25, v41
	v_mul_f32_e32 v7, 0xbfb8aa3b, v4
	v_mov_b32_e32 v23, v11
	v_exp_f32_e32 v8, v7
	s_nop 0
	v_permlane32_swap_b32_e32 v11, v23
	v_add_f32_e32 v11, v11, v23
	v_add_f32_e32 v11, 0x358637bd, v11
	v_add_f32_e32 v6, 1.0, v6
	v_mul_f32_e32 v23, 0x4f800000, v11
	v_cmp_gt_f32_e32 vcc, s84, v11
	v_rcp_f32_e32 v7, v6
	v_add_f32_e32 v6, 1.0, v8
	v_cndmask_b32_e32 v11, v11, v23, vcc
	v_rcp_f32_e32 v6, v6
	v_sqrt_f32_e32 v23, v11
	ds_write2st64_b32 v13, v10, v15 offset1:64
	v_and_b32_e32 v37, 0xffff0000, v89
	v_pk_mul_f32 v[4:5], v[4:5], v[6:7]
	v_add_u32_e32 v9, -1, v23
	v_pk_mul_f32 v[6:7], v[4:5], v[4:5]
	v_fma_f32 v8, -v9, v23, v11
	v_add_f32_e32 v6, v6, v7
	v_cmp_ge_f32_e64 s[2:3], 0, v8
	ds_swizzle_b32 v7, v6 offset:swizzle(SWAP,1)
	v_lshlrev_b32_e32 v34, 16, v88
	v_cndmask_b32_e64 v8, v23, v9, s[2:3]
	v_add_u32_e32 v9, 1, v23
	v_fma_f32 v23, -v9, v23, v11
	v_cmp_lt_f32_e64 s[2:3], 0, v23
	s_waitcnt lgkmcnt(0)
	v_add_f32_e32 v7, v6, v7
	v_and_b32_e32 v35, 0xffff0000, v88
	v_cndmask_b32_e64 v8, v8, v9, s[2:3]
	v_mul_f32_e32 v6, 0x37800000, v8
	v_cndmask_b32_e32 v6, v8, v6, vcc
	v_cmp_class_f32_e32 vcc, v11, v108
	ds_swizzle_b32 v9, v7 offset:swizzle(SWAP,2)
	s_waitcnt vmcnt(0)
	v_pk_mul_f32 v[40:41], v[28:29], v[36:37]
	v_cndmask_b32_e32 v6, v6, v11, vcc
	v_add_co_u32_e32 v0, vcc, s74, v0
	s_waitcnt lgkmcnt(0)
	v_add_f32_e32 v7, v7, v9
	v_addc_co_u32_e32 v1, vcc, 0, v1, vcc
	global_load_dwordx2 v[0:1], v[0:1], off offset:2048
	ds_swizzle_b32 v8, v7 offset:swizzle(SWAP,4)
	v_div_scale_f32 v9, s[2:3], v6, v6, 1.0
	v_rcp_f32_e32 v11, v9
	v_lshlrev_b32_e32 v30, 16, v90
	s_waitcnt lgkmcnt(0)
	v_add_f32_e32 v7, v7, v8
	ds_swizzle_b32 v8, v7 offset:swizzle(SWAP,8)
	v_fma_f32 v10, -v9, v11, 1.0
	v_fmac_f32_e32 v11, v10, v11
	v_div_scale_f32 v10, vcc, 1.0, v6, 1.0
	s_waitcnt lgkmcnt(0)
	v_add_f32_e32 v7, v7, v8
	ds_swizzle_b32 v8, v7 offset:swizzle(SWAP,16)
	v_mul_f32_e32 v15, v10, v11
	v_fma_f32 v23, -v9, v15, v10
	v_fmac_f32_e32 v15, v23, v11
	v_fma_f32 v9, -v9, v15, v10
	s_waitcnt lgkmcnt(0)
	v_add_f32_e32 v7, v7, v8
	v_mov_b32_e32 v8, v7
	s_nop 1
	v_permlane32_swap_b32_e32 v7, v8
	v_add_f32_e32 v7, v7, v8
	v_add_f32_e32 v7, 0x358637bd, v7
	v_mul_f32_e32 v8, 0x4f800000, v7
	v_cmp_gt_f32_e64 s[2:3], s84, v7
	v_div_fmas_f32 v9, v9, v11, v15
	v_div_fixup_f32 v6, v9, v6, 1.0
	v_cndmask_b32_e64 v7, v7, v8, s[2:3]
	v_sqrt_f32_e32 v8, v7
	v_and_b32_e32 v31, 0xffff0000, v90
	v_pk_fma_f32 v[34:35], v[26:27], v[34:35], v[40:41]
	v_pk_mul_f32 v[44:45], v[28:29], v[30:31]
	v_add_u32_e32 v9, -1, v8
	v_fma_f32 v10, -v9, v8, v7
	v_cmp_ge_f32_e32 vcc, 0, v10
	v_add_u32_e32 v10, 1, v8
	v_lshlrev_b32_e32 v42, 16, v91
	v_cndmask_b32_e32 v9, v8, v9, vcc
	v_fma_f32 v8, -v10, v8, v7
	v_cmp_lt_f32_e32 vcc, 0, v8
	v_and_b32_e32 v43, 0xffff0000, v91
	v_pk_fma_f32 v[36:37], v[26:27], v[36:37], v[44:45]
	v_cndmask_b32_e32 v8, v9, v10, vcc
	v_mul_f32_e32 v9, 0x37800000, v8
	v_cndmask_b32_e64 v8, v8, v9, s[2:3]
	v_cmp_class_f32_e32 vcc, v7, v108
	v_lshlrev_b32_e32 v32, 16, v92
	v_and_b32_e32 v33, 0xffff0000, v92
	v_cndmask_b32_e32 v7, v8, v7, vcc
	v_div_scale_f32 v8, s[2:3], v7, v7, 1.0
	v_rcp_f32_e32 v9, v8
	v_pk_mul_f32 v[2:3], v[2:3], v[6:7] op_sel_hi:[1,0]
	v_lshlrev_b32_e32 v10, 16, v93
	v_cvt_pk_bf16_f32 v2, v2, v3
	ds_write2st64_b32 v12, v2, v17 offset1:64
	v_fma_f32 v2, -v8, v9, 1.0
	v_fmac_f32_e32 v9, v2, v9
	v_div_scale_f32 v2, vcc, 1.0, v7, 1.0
	v_mul_f32_e32 v3, v2, v9
	v_fma_f32 v6, -v8, v3, v2
	v_fmac_f32_e32 v3, v6, v9
	v_fma_f32 v2, -v8, v3, v2
	v_div_fmas_f32 v2, v2, v9, v3
	v_div_fixup_f32 v2, v2, v7, 1.0
	v_pk_mul_f32 v[2:3], v[4:5], v[2:3] op_sel_hi:[1,0]
	v_and_b32_e32 v11, 0xffff0000, v93
	v_cvt_pk_bf16_f32 v2, v2, v3
	ds_write2st64_b32 v14, v2, v21 offset1:64
	v_lshlrev_b32_e32 v8, 16, v94
	v_and_b32_e32 v9, 0xffff0000, v94
	v_lshlrev_b32_e32 v2, 16, v95
	v_and_b32_e32 v3, 0xffff0000, v95
	v_lshlrev_b32_e32 v6, 16, v96
	v_and_b32_e32 v7, 0xffff0000, v96
	v_lshlrev_b32_e32 v4, 16, v97
	s_waitcnt vmcnt(0)
	v_pk_fma_f32 v[34:35], v[0:1], v[30:31], v[34:35]
	s_nop 0
	v_mul_f32_e32 v5, 0xbfb8aa3b, v34
	v_exp_f32_e32 v15, v5
	v_mul_f32_e32 v5, 0xbfb8aa3b, v35
	v_exp_f32_e32 v17, v5
	v_pk_fma_f32 v[36:37], v[0:1], v[42:43], v[36:37]
	v_add_f32_e32 v15, 1.0, v15
	v_rcp_f32_e32 v40, v15
	v_add_f32_e32 v15, 1.0, v17
	v_mul_f32_e32 v17, 0xbfb8aa3b, v36
	v_exp_f32_e32 v17, v17
	v_mul_f32_e32 v21, 0xbfb8aa3b, v37
	v_exp_f32_e32 v21, v21
	v_rcp_f32_e32 v41, v15
	v_add_f32_e32 v15, 1.0, v17
	v_rcp_f32_e32 v44, v15
	v_add_f32_e32 v15, 1.0, v21
	v_rcp_f32_e32 v45, v15
	v_pk_mul_f32 v[34:35], v[34:35], v[40:41]
	v_and_b32_e32 v5, 0xffff0000, v97
	v_cvt_pk_bf16_f32 v15, v34, v35
	ds_write_b32 v22, v15 offset:32768
	v_pk_mul_f32 v[22:23], v[36:37], v[44:45]
	s_nop 0
	v_cvt_pk_bf16_f32 v15, v22, v23
	v_pk_mul_f32 v[22:23], v[28:29], v[42:43]
	ds_write_b32 v20, v15 offset:33024
	v_pk_fma_f32 v[22:23], v[26:27], v[30:31], v[22:23]
	v_pk_mul_f32 v[30:31], v[28:29], v[32:33]
	v_pk_fma_f32 v[22:23], v[0:1], v[32:33], v[22:23]
	v_pk_fma_f32 v[30:31], v[26:27], v[42:43], v[30:31]
	v_mul_f32_e32 v17, 0xbfb8aa3b, v22
	v_exp_f32_e32 v17, v17
	v_mul_f32_e32 v21, 0xbfb8aa3b, v23
	v_exp_f32_e32 v21, v21
	v_pk_fma_f32 v[30:31], v[0:1], v[10:11], v[30:31]
	v_add_f32_e32 v15, 1.0, v17
	v_mul_f32_e32 v17, 0xbfb8aa3b, v30
	v_rcp_f32_e32 v20, v15
	v_add_f32_e32 v15, 1.0, v21
	v_exp_f32_e32 v17, v17
	v_mul_f32_e32 v21, 0xbfb8aa3b, v31
	v_exp_f32_e32 v25, v21
	v_rcp_f32_e32 v21, v15
	v_add_f32_e32 v15, 1.0, v17
	v_rcp_f32_e32 v34, v15
	v_add_f32_e32 v15, 1.0, v25
	v_rcp_f32_e32 v35, v15
	v_pk_mul_f32 v[20:21], v[22:23], v[20:21]
	v_pk_mul_f32 v[22:23], v[28:29], v[8:9]
	v_cvt_pk_bf16_f32 v15, v20, v21
	v_pk_mul_f32 v[20:21], v[30:31], v[34:35]
	ds_write_b32 v19, v15 offset:33280
	v_cvt_pk_bf16_f32 v15, v20, v21
	v_pk_mul_f32 v[20:21], v[28:29], v[10:11]
	v_pk_fma_f32 v[10:11], v[26:27], v[10:11], v[22:23]
	v_pk_fma_f32 v[20:21], v[26:27], v[32:33], v[20:21]
	v_pk_fma_f32 v[10:11], v[0:1], v[2:3], v[10:11]
	v_pk_fma_f32 v[20:21], v[0:1], v[8:9], v[20:21]
	ds_write_b32 v18, v15 offset:33536
	v_mul_f32_e32 v17, 0xbfb8aa3b, v20
	v_exp_f32_e32 v17, v17
	v_mul_f32_e32 v19, 0xbfb8aa3b, v21
	v_exp_f32_e32 v19, v19
	v_add_f32_e32 v15, 1.0, v17
	v_mul_f32_e32 v17, 0xbfb8aa3b, v10
	v_rcp_f32_e32 v18, v15
	v_add_f32_e32 v15, 1.0, v19
	v_exp_f32_e32 v17, v17
	v_mul_f32_e32 v19, 0xbfb8aa3b, v11
	v_exp_f32_e32 v23, v19
	v_rcp_f32_e32 v19, v15
	v_add_f32_e32 v15, 1.0, v17
	v_rcp_f32_e32 v22, v15
	v_add_f32_e32 v15, 1.0, v23
	v_rcp_f32_e32 v23, v15
	v_pk_mul_f32 v[18:19], v[20:21], v[18:19]
	v_pk_mul_f32 v[10:11], v[10:11], v[22:23]
	v_cvt_pk_bf16_f32 v15, v18, v19
	ds_write_b32 v16, v15 offset:32768
	v_cvt_pk_bf16_f32 v15, v10, v11
	v_pk_mul_f32 v[10:11], v[28:29], v[2:3]
	ds_write_b32 v13, v15 offset:32768
	v_pk_fma_f32 v[8:9], v[26:27], v[8:9], v[10:11]
	s_nop 0
	v_pk_fma_f32 v[8:9], v[0:1], v[6:7], v[8:9]
	v_pk_mul_f32 v[6:7], v[28:29], v[6:7]
	v_mul_f32_e32 v10, 0xbfb8aa3b, v8
	v_pk_fma_f32 v[2:3], v[26:27], v[2:3], v[6:7]
	v_mul_f32_e32 v11, 0xbfb8aa3b, v9
	v_pk_fma_f32 v[0:1], v[0:1], v[4:5], v[2:3]
	v_exp_f32_e32 v10, v10
	v_mul_f32_e32 v2, 0xbfb8aa3b, v0
	v_mul_f32_e32 v3, 0xbfb8aa3b, v1
	v_exp_f32_e32 v11, v11
	v_exp_f32_e32 v2, v2
	v_exp_f32_e32 v3, v3
	v_add_f32_e32 v10, 1.0, v10
	v_add_f32_e32 v11, 1.0, v11
	v_add_f32_e32 v2, 1.0, v2
	v_add_f32_e32 v3, 1.0, v3
	v_rcp_f32_e32 v10, v10
	v_rcp_f32_e32 v11, v11
	v_rcp_f32_e32 v2, v2
	v_rcp_f32_e32 v3, v3
	v_pk_mul_f32 v[4:5], v[8:9], v[10:11]
	s_nop 0
	v_cvt_pk_bf16_f32 v4, v4, v5
	v_pk_mul_f32 v[0:1], v[0:1], v[2:3]
	ds_write_b32 v12, v4 offset:32768
	v_cvt_pk_bf16_f32 v0, v0, v1
	ds_write_b32 v14, v0 offset:32768
	s_cbranch_scc1 .LBB0_1610
	s_add_i32 s14, s8, s96
	s_cmpk_lt_u32 s14, 0x1000
	s_cselect_b64 s[2:3], -1, 0
	s_and_b64 s[2:3], s[2:3], exec
	s_cselect_b32 s13, s4, s8
	s_cselect_b32 s12, s5, s8
	s_cselect_b32 s11, s9, s8
	s_cselect_b32 s9, s10, s8
	s_or_b32 s4, s8, 3
	s_cmpk_lt_u32 s14, 0x1000
	s_cselect_b64 s[2:3], -1, 0
	s_and_b64 s[2:3], s[2:3], exec
	s_cselect_b32 s10, s4, s8
	s_or_b32 s4, s8, 2
	s_cmpk_lt_u32 s14, 0x1000
	s_cselect_b64 vcc, -1, 0
	s_and_b64 s[2:3], vcc, exec
	s_cselect_b32 s14, s4, s8
	s_lshl_b32 s15, s21, 7
	s_add_i32 s2, s15, 0xf00
	s_add_i32 s16, s8, -1
	v_or_b32_e32 v0, s2, v39
	s_add_i32 s2, s16, s96
	s_cmpk_lt_u32 s2, 0x1000
	s_cselect_b64 s[2:3], -1, 0
	v_lshlrev_b32_e32 v64, 1, v0
	s_and_b64 s[4:5], s[2:3], exec
	v_lshl_add_u64 v[0:1], s[56:57], 0, v[64:65]
	s_cselect_b32 s16, s16, s8
	v_cndmask_b32_e64 v6, 0, 1, vcc
	v_mad_i64_i32 v[2:3], s[4:5], s16, v121, v[0:1]
	v_or_b32_e32 v18, s8, v6
	v_mad_i64_i32 v[4:5], s[4:5], s8, v121, v[0:1]
	v_mad_i64_i32 v[6:7], s[4:5], v18, s73, v[0:1]
	v_mad_i64_i32 v[8:9], s[4:5], s14, v121, v[0:1]
	v_mad_i64_i32 v[10:11], s[4:5], s10, v121, v[0:1]
	v_mad_i64_i32 v[12:13], s[4:5], s13, v121, v[0:1]
	v_mad_i64_i32 v[14:15], s[4:5], s12, v121, v[0:1]
	v_mad_i64_i32 v[16:17], s[4:5], s11, v121, v[0:1]
	global_load_dword v19, v[2:3], off nt
	global_load_dword v20, v[4:5], off nt
	global_load_dword v21, v[6:7], off nt
	global_load_dword v22, v[8:9], off nt
	global_load_dword v23, v[10:11], off nt
	global_load_dword v25, v[12:13], off nt
	global_load_dword v26, v[14:15], off nt
	global_load_dword v27, v[16:17], off nt
	v_mad_i64_i32 v[2:3], s[4:5], s9, v121, v[0:1]
	s_add_i32 s17, s8, 8
	s_add_i32 s4, s17, s96
	s_cmpk_lt_u32 s4, 0x1000
	s_cselect_b64 s[4:5], -1, 0
	s_and_b64 s[22:23], s[4:5], exec
	s_cselect_b32 s17, s17, s8
	v_mad_i64_i32 v[0:1], s[22:23], s17, v121, v[0:1]
	s_add_i32 s22, s15, 0x1200
	s_nop 0
	v_or_b32_e32 v4, s22, v39
	v_lshlrev_b32_e32 v64, 1, v4
	v_lshl_add_u64 v[4:5], s[56:57], 0, v[64:65]
	v_mad_i64_i32 v[8:9], s[22:23], s8, v121, v[4:5]
	s_addk_i32 s15, 0x1500
	v_mad_i64_i32 v[6:7], s[22:23], s16, v121, v[4:5]
	v_mad_i64_i32 v[10:11], s[22:23], v18, s73, v[4:5]
	v_mad_i64_i32 v[12:13], s[22:23], s14, v121, v[4:5]
	v_mad_i64_i32 v[14:15], s[22:23], s10, v121, v[4:5]
	v_mad_i64_i32 v[16:17], s[22:23], s13, v121, v[4:5]
	global_load_dword v28, v[2:3], off nt
	global_load_dword v29, v[0:1], off nt
	global_load_dword v30, v[6:7], off nt
	global_load_dword v31, v[8:9], off nt
	global_load_dword v32, v[10:11], off nt
	global_load_dword v33, v[12:13], off nt
	global_load_dword v34, v[14:15], off nt
	global_load_dword v35, v[16:17], off nt
	v_or_b32_e32 v8, s15, v39
	v_lshlrev_b32_e32 v64, 1, v8
	v_lshl_add_u64 v[8:9], s[56:57], 0, v[64:65]
	v_mad_i64_i32 v[0:1], s[22:23], s12, v121, v[4:5]
	v_mad_i64_i32 v[2:3], s[22:23], s11, v121, v[4:5]
	v_mad_i64_i32 v[6:7], s[22:23], s9, v121, v[4:5]
	v_mad_i64_i32 v[4:5], s[22:23], s17, v121, v[4:5]
	v_mad_i64_i32 v[12:13], s[22:23], s8, v121, v[8:9]
	v_mad_i64_i32 v[14:15], s[22:23], v18, s73, v[8:9]
	v_mad_i64_i32 v[10:11], s[22:23], s16, v121, v[8:9]
	v_mad_i64_i32 v[16:17], s[14:15], s14, v121, v[8:9]
	global_load_dword v18, v[0:1], off nt
	global_load_dword v36, v[2:3], off nt
	global_load_dword v37, v[6:7], off nt
	global_load_dword v39, v[4:5], off nt
	global_load_dword v40, v[10:11], off nt
	s_nop 0
	global_load_dword v12, v[12:13], off nt
	s_nop 0
	global_load_dword v13, v[14:15], off nt
	s_nop 0
	global_load_dword v14, v[16:17], off nt
	v_mad_i64_i32 v[0:1], s[14:15], s10, v121, v[8:9]
	v_mad_i64_i32 v[2:3], s[14:15], s13, v121, v[8:9]
	v_mad_i64_i32 v[4:5], s[12:13], s12, v121, v[8:9]
	v_mad_i64_i32 v[6:7], s[10:11], s11, v121, v[8:9]
	v_mad_i64_i32 v[10:11], s[8:9], s9, v121, v[8:9]
	v_mad_i64_i32 v[8:9], s[8:9], s17, v121, v[8:9]
	global_load_dword v0, v[0:1], off nt
	s_nop 0
	global_load_dword v1, v[2:3], off nt
	s_nop 0
	global_load_dword v2, v[4:5], off nt
	global_load_dword v3, v[6:7], off nt
	s_nop 0
	global_load_dword v4, v[10:11], off nt
	global_load_dword v5, v[8:9], off nt
	s_waitcnt vmcnt(29)
	v_cndmask_b32_e64 v68, 0, v19, s[2:3]
	s_waitcnt vmcnt(28)
	v_cndmask_b32_e32 v69, 0, v20, vcc
	s_waitcnt vmcnt(27)
	v_cndmask_b32_e32 v70, 0, v21, vcc
	s_waitcnt vmcnt(26)
	v_cndmask_b32_e32 v71, 0, v22, vcc
	s_waitcnt vmcnt(25)
	v_cndmask_b32_e32 v72, 0, v23, vcc
	s_waitcnt vmcnt(24)
	v_cndmask_b32_e32 v73, 0, v25, vcc
	s_waitcnt vmcnt(23)
	v_cndmask_b32_e32 v74, 0, v26, vcc
	s_waitcnt vmcnt(22)
	v_cndmask_b32_e32 v75, 0, v27, vcc
	s_waitcnt vmcnt(21)
	v_cndmask_b32_e32 v76, 0, v28, vcc
	s_waitcnt vmcnt(20)
	v_cndmask_b32_e64 v77, 0, v29, s[4:5]
	s_waitcnt vmcnt(19)
	v_cndmask_b32_e64 v78, 0, v30, s[2:3]
	s_waitcnt vmcnt(18)
	v_cndmask_b32_e32 v79, 0, v31, vcc
	s_waitcnt vmcnt(17)
	v_cndmask_b32_e32 v80, 0, v32, vcc
	s_waitcnt vmcnt(16)
	v_cndmask_b32_e32 v81, 0, v33, vcc
	s_waitcnt vmcnt(15)
	v_cndmask_b32_e32 v82, 0, v34, vcc
	s_waitcnt vmcnt(14)
	v_cndmask_b32_e32 v83, 0, v35, vcc
	s_waitcnt vmcnt(13)
	v_cndmask_b32_e32 v84, 0, v18, vcc
	s_waitcnt vmcnt(12)
	v_cndmask_b32_e32 v85, 0, v36, vcc
	s_waitcnt vmcnt(11)
	v_cndmask_b32_e32 v86, 0, v37, vcc
	s_waitcnt vmcnt(10)
	v_cndmask_b32_e64 v87, 0, v39, s[4:5]
	s_waitcnt vmcnt(9)
	v_cndmask_b32_e64 v88, 0, v40, s[2:3]
	s_waitcnt vmcnt(8)
	v_cndmask_b32_e32 v89, 0, v12, vcc
	s_waitcnt vmcnt(7)
	v_cndmask_b32_e32 v90, 0, v13, vcc
	s_waitcnt vmcnt(6)
	v_cndmask_b32_e32 v91, 0, v14, vcc
	s_waitcnt vmcnt(5)
	v_cndmask_b32_e32 v92, 0, v0, vcc
	s_waitcnt vmcnt(4)
	v_cndmask_b32_e32 v93, 0, v1, vcc
	s_waitcnt vmcnt(3)
	v_cndmask_b32_e32 v94, 0, v2, vcc
	s_waitcnt vmcnt(2)
	v_cndmask_b32_e32 v95, 0, v3, vcc
	s_waitcnt vmcnt(1)
	v_cndmask_b32_e32 v96, 0, v4, vcc
	s_waitcnt vmcnt(0)
	v_cndmask_b32_e64 v97, 0, v5, s[4:5]
.LBB0_1610:
	s_cmp_gt_i32 s7, 1
	s_cbranch_scc1 .LBB0_1614
	s_mul_i32 s2, s7, 6
	s_add_i32 s2, s2, s48
	s_add_i32 s4, s2, 12
	s_ashr_i32 s3, s2, 31
	s_ashr_i32 s5, s4, 31
	s_cmp_lt_u32 s6, 64
	s_cselect_b64 vcc, -1, 0
	s_and_b64 s[8:9], vcc, exec
	s_cselect_b32 s6, s85, 0x70
	s_cselect_b32 s12, s87, 0x80
	s_add_u32 s8, s34, s6
	s_addc_u32 s9, s35, 0
	s_load_dwordx2 s[8:9], s[8:9], 0x0
	s_lshl_b64 s[10:11], s[48:49], 2
	v_xor_b32_e32 v0, 63, v38
	v_cndmask_b32_e32 v0, v0, v38, vcc
	v_or_b32_e32 v0, s97, v0
	s_waitcnt lgkmcnt(0)
	s_add_u32 s8, s8, s10
	s_addc_u32 s9, s9, s11
	s_add_u32 s12, s34, s12
	s_addc_u32 s13, s35, 0
	s_load_dwordx2 s[12:13], s[12:13], 0x0
	v_ashrrev_i32_e32 v1, 31, v0
	v_lshlrev_b64 v[0:1], 7, v[0:1]
	v_lshl_add_u64 v[0:1], s[40:41], 0, v[0:1]
	v_lshl_add_u64 v[2:3], s[2:3], 2, v[0:1]
	s_waitcnt lgkmcnt(0)
	s_add_u32 s2, s12, s10
	v_lshl_add_u64 v[0:1], s[4:5], 2, v[0:1]
	s_addc_u32 s3, s13, s11
	global_load_dword v4, v65, s[2:3] offset:24
	global_load_dword v5, v[0:1], off nt
	s_nop 0
	global_load_dword v0, v[2:3], off nt
	global_load_dword v1, v65, s[8:9] offset:24
	s_waitcnt vmcnt(2)
	v_add_f32_e32 v2, v5, v4
	v_cmp_nlt_f32_e32 vcc, s88, v2
	s_and_saveexec_b64 s[2:3], vcc
	s_cbranch_execz .LBB0_1613
	v_mul_f32_e32 v3, 0x3fb8aa3b, v2
	v_rndne_f32_e32 v4, v3
	v_sub_f32_e32 v5, v3, v4
	v_fma_f32 v3, v2, s80, -v3
	v_fmac_f32_e32 v3, 0x32a5705f, v2
	v_add_f32_e32 v3, v5, v3
	v_cvt_i32_f32_e32 v4, v4
	v_exp_f32_e32 v3, v3
	v_cmp_ngt_f32_e32 vcc, s81, v2
	v_ldexp_f32 v3, v3, v4
	s_nop 0
	v_cndmask_b32_e32 v3, 0, v3, vcc
	v_cmp_nlt_f32_e32 vcc, s79, v2
	s_nop 1
	v_cndmask_b32_e32 v16, v112, v3, vcc
	v_add_f32_e32 v4, 1.0, v16
	v_add_f32_e32 v2, -1.0, v4
	v_sub_f32_e32 v3, v2, v4
	v_add_f32_e32 v3, 1.0, v3
	v_sub_f32_e32 v2, v16, v2
	v_add_f32_e32 v5, v2, v3
	v_frexp_mant_f32_e32 v6, v4
	v_cvt_f64_f32_e32 v[2:3], v4
	v_frexp_exp_i32_f64_e32 v2, v[2:3]
	v_cmp_gt_f32_e32 vcc, s75, v6
	s_nop 1
	v_subbrev_co_u32_e32 v10, vcc, 0, v2, vcc
	v_sub_u32_e32 v2, 0, v10
	v_ldexp_f32 v3, v4, v2
	v_add_f32_e32 v4, -1.0, v3
	v_add_f32_e32 v6, 1.0, v3
	v_ldexp_f32 v2, v5, v2
	v_add_f32_e32 v5, 1.0, v4
	v_add_f32_e32 v7, -1.0, v6
	v_sub_f32_e32 v5, v3, v5
	v_sub_f32_e32 v3, v3, v7
	v_add_f32_e32 v5, v2, v5
	v_add_f32_e32 v2, v2, v3
	v_add_f32_e32 v11, v6, v2
	v_rcp_f32_e32 v13, v11
	v_sub_f32_e32 v3, v6, v11
	v_add_f32_e32 v12, v2, v3
	v_add_f32_e32 v3, v4, v5
	v_mul_f32_e32 v15, v3, v13
	v_sub_f32_e32 v2, v4, v3
	v_mul_f32_e32 v4, v11, v15
	v_fma_f32 v6, v15, v11, -v4
	v_fmac_f32_e32 v6, v15, v12
	v_add_f32_e32 v14, v5, v2
	v_add_f32_e32 v2, v4, v6
	v_sub_f32_e32 v5, v3, v2
	v_pk_add_f32 v[8:9], v[2:3], v[4:5] neg_lo:[0,1] neg_hi:[0,1]
	v_mov_b32_e32 v7, v2
	v_pk_add_f32 v[2:3], v[8:9], v[6:7] neg_lo:[0,1] neg_hi:[0,1]
	v_cmp_neq_f32_e32 vcc, s78, v16
	v_add_f32_e32 v3, v14, v3
	v_add_f32_e32 v2, v2, v3
	v_add_f32_e32 v3, v5, v2
	v_mul_f32_e32 v14, v13, v3
	v_mul_f32_e32 v4, v11, v14
	v_fma_f32 v6, v14, v11, -v4
	v_fmac_f32_e32 v6, v14, v12
	v_sub_f32_e32 v5, v5, v3
	v_add_f32_e32 v11, v2, v5
	v_add_f32_e32 v2, v4, v6
	v_sub_f32_e32 v5, v3, v2
	v_pk_add_f32 v[8:9], v[2:3], v[4:5] neg_lo:[0,1] neg_hi:[0,1]
	v_mov_b32_e32 v7, v2
	v_pk_add_f32 v[2:3], v[8:9], v[6:7] neg_lo:[0,1] neg_hi:[0,1]
	s_nop 0
	v_add_f32_e32 v3, v11, v3
	v_add_f32_e32 v2, v2, v3
	v_add_f32_e32 v3, v15, v14
	v_add_f32_e32 v2, v5, v2
	v_sub_f32_e32 v4, v3, v15
	v_mul_f32_e32 v2, v13, v2
	v_sub_f32_e32 v4, v14, v4
	v_add_f32_e32 v4, v4, v2
	v_add_f32_e32 v6, v3, v4
	v_mul_f32_e32 v7, v6, v6
	v_fmamk_f32 v2, v7, 0x3e9b6dac, v109
	v_fmaak_f32 v67, v7, v2, 0x3f2aaada
	v_cvt_f32_i32_e32 v2, v10
	v_sub_f32_e32 v3, v6, v3
	v_sub_f32_e32 v3, v4, v3
	v_ldexp_f32 v8, v3, 1
	v_mul_f32_e32 v3, v6, v7
	v_ldexp_f32 v5, v6, 1
	v_pk_mul_f32 v[6:7], v[2:3], v[66:67]
	s_nop 0
	v_fma_f32 v4, v2, s76, -v6
	v_fmac_f32_e32 v4, 0xb102e308, v2
	v_pk_add_f32 v[2:3], v[6:7], v[4:5]
	s_nop 0
	v_sub_f32_e32 v5, v3, v5
	v_sub_f32_e32 v5, v7, v5
	v_add_f32_e32 v9, v8, v5
	v_mov_b32_e32 v8, v6
	v_pk_add_f32 v[6:7], v[2:3], v[6:7] neg_lo:[0,1] neg_hi:[0,1]
	v_pk_add_f32 v[10:11], v[2:3], v[8:9]
	v_mov_b32_e32 v5, v2
	v_mov_b32_e32 v7, v11
	v_pk_add_f32 v[12:13], v[4:5], v[6:7] neg_lo:[0,1] neg_hi:[0,1]
	v_pk_add_f32 v[4:5], v[4:5], v[6:7]
	v_mov_b32_e32 v8, v9
	v_pk_add_f32 v[6:7], v[4:5], v[2:3] op_sel:[1,0] op_sel_hi:[0,1] neg_lo:[0,1] neg_hi:[0,1]
	v_pk_add_f32 v[14:15], v[10:11], v[6:7] op_sel_hi:[1,0] neg_lo:[0,1] neg_hi:[0,1]
	v_mov_b32_e32 v10, v11
	v_mov_b32_e32 v11, v5
	v_pk_mov_b32 v[6:7], v[2:3], v[6:7] op_sel:[1,0]
	v_mov_b32_e32 v9, v2
	v_pk_add_f32 v[6:7], v[10:11], v[6:7] neg_lo:[0,1] neg_hi:[0,1]
	v_mov_b32_e32 v14, v12
	v_pk_add_f32 v[2:3], v[8:9], v[6:7] neg_lo:[0,1] neg_hi:[0,1]
	v_mov_b32_e32 v13, v5
	v_pk_add_f32 v[6:7], v[14:15], v[2:3]
	s_nop 0
	v_pk_add_f32 v[8:9], v[6:7], v[6:7] op_sel:[0,1] op_sel_hi:[1,0]
	s_nop 0
	v_pk_add_f32 v[4:5], v[4:5], v[8:9] op_sel:[1,0] op_sel_hi:[0,1]
	v_mov_b32_e32 v7, v4
	v_pk_add_f32 v[10:11], v[6:7], v[12:13] neg_lo:[0,1] neg_hi:[0,1]
	v_mov_b32_e32 v3, v8
	v_sub_f32_e32 v5, v6, v10
	v_pk_add_f32 v[2:3], v[2:3], v[10:11] neg_lo:[0,1] neg_hi:[0,1]
	v_sub_f32_e32 v5, v12, v5
	v_add_f32_e32 v2, v2, v5
	v_add_f32_e32 v2, v2, v3
	v_add_f32_e32 v2, v4, v2
	v_cndmask_b32_e32 v2, v112, v2, vcc
	v_cmp_lt_f32_e64 vcc, |v16|, s89
	s_nop 1
	v_cndmask_b32_e32 v2, v2, v16, vcc
